# baseline (speedup 1.0000x reference)
_Z10k_final_lnPKDF16_PKDv2_fPKfS5_Pf:
	v_lshl_or_b32 v6, s2, 8, v0
	s_mov_b32 s3, 0x55555556
	v_mul_hi_u32 v0, v6, s3
	v_mov_b32_e32 v1, 0
	s_lshr_b32 s12, s2, 24
	v_mov_b32_e32 v2, 0x55555556
	v_mad_u64_u32 v[2:3], s[2:3], s12, v2, v[0:1]
	v_mov_b32_e32 v0, v2
	s_mov_b32 s2, 0x1555555
	v_mad_u64_u32 v[4:5], s[2:3], v6, s2, v[0:1]
	v_mov_b32_e32 v0, v5
	v_mov_b32_e32 v2, v3
	v_mov_b32_e32 v3, v1
	s_load_dwordx8 s[4:11], s[0:1], 0x0
	v_lshl_add_u64 v[0:1], v[2:3], 0, v[0:1]
	v_mov_b32_e32 v2, 0x1555555
	v_mad_u64_u32 v[0:1], s[2:3], s12, v2, v[0:1]
	s_movk_i32 s2, 0xff40
	s_nop 0
	v_mul_lo_u32 v1, v0, s2
	s_movk_i32 s2, 0x300
	v_add_lshl_u32 v2, v1, v6, 2
	v_mad_i64_i32 v[8:9], s[2:3], v0, s2, 0
	s_waitcnt lgkmcnt(0)
	v_lshl_add_u64 v[4:5], v[8:9], 1, s[4:5]
	v_ashrrev_i32_e32 v3, 31, v2
	v_lshl_add_u64 v[4:5], v[2:3], 1, v[4:5]
	global_load_dwordx2 v[10:11], v[4:5], off nt
	v_ashrrev_i32_e32 v1, 31, v0
	v_lshl_add_u64 v[0:1], v[0:1], 3, s[6:7]
	global_load_dwordx2 v[12:13], v[0:1], off
	v_lshlrev_b64 v[14:15], 2, v[2:3]
	v_lshl_add_u64 v[0:1], s[8:9], 0, v[14:15]
	v_lshl_add_u64 v[4:5], s[10:11], 0, v[14:15]
	global_load_dwordx4 v[0:3], v[0:1], off
	s_load_dwordx2 s[0:1], s[0:1], 0x20
	global_load_dwordx4 v[4:7], v[4:5], off
	s_waitcnt lgkmcnt(0)
	v_lshl_add_u64 v[8:9], v[8:9], 2, s[0:1]
	s_waitcnt vmcnt(3)
	v_cvt_f32_f16_e32 v16, v11
	v_cvt_f32_f16_sdwa v11, v11 dst_sel:DWORD dst_unused:UNUSED_PAD src0_sel:WORD_1
	v_cvt_f32_f16_e32 v17, v10
	v_cvt_f32_f16_sdwa v18, v10 dst_sel:DWORD dst_unused:UNUSED_PAD src0_sel:WORD_1
	s_waitcnt vmcnt(2)
	v_sub_f32_e32 v10, v16, v12
	v_sub_f32_e32 v11, v11, v12
	v_sub_f32_e32 v16, v17, v12
	v_sub_f32_e32 v17, v18, v12
	v_pk_mul_f32 v[16:17], v[12:13], v[16:17] op_sel:[1,0]
	v_pk_mul_f32 v[10:11], v[12:13], v[10:11] op_sel:[1,0]
	s_waitcnt vmcnt(0)
	v_pk_fma_f32 v[0:1], v[0:1], v[16:17], v[4:5]
	v_pk_fma_f32 v[2:3], v[2:3], v[10:11], v[6:7]
	v_lshl_add_u64 v[4:5], v[8:9], 0, v[14:15]
	global_store_dwordx4 v[4:5], v[0:3], off nt
	s_endpgm
	s_endpgm
	s_endpgm
	s_endpgm
	s_endpgm
	s_endpgm
	s_endpgm
	s_endpgm
	s_endpgm
	s_endpgm
	s_endpgm
	s_endpgm
	s_endpgm
	s_endpgm
	s_endpgm
	s_endpgm
	s_endpgm
	s_endpgm
	s_endpgm
	s_endpgm
	s_endpgm
	s_endpgm
	s_endpgm
	s_endpgm
	s_endpgm
	s_endpgm
	s_endpgm
	s_endpgm
	s_endpgm
	s_endpgm
	s_endpgm
	s_endpgm
	s_endpgm
	.section	.rodata,"a",@progbits
	.p2align	6, 0x0

.LBB7_26:
	s_min_u32 s77, s47, 2
	s_lshl_b32 s34, s70, 8
	s_add_i32 s34, s34, s48
	v_or_b32_e32 v250, s34, v165
	v_ashrrev_i32_e32 v251, 31, v250
	v_lshl_add_u64 v[250:251], v[250:251], 3, s[12:13]
	s_lshl_b32 s35, s67, 8
	s_or_b32 s35, s35, s51
	v_or_b32_e32 v252, s35, v164
	v_ashrrev_i32_e32 v253, 31, v252
	v_lshl_add_u64 v[252:253], v[252:253], 2, s[14:15]
	global_load_dword v226, v[250:251], off offset:4
	global_load_dword v227, v[250:251], off offset:132
	global_load_dword v228, v[250:251], off offset:260
	global_load_dword v229, v[250:251], off offset:388
	global_load_dword v230, v[250:251], off offset:1028
	global_load_dword v231, v[250:251], off offset:1156
	global_load_dword v232, v[250:251], off offset:1284
	global_load_dword v233, v[250:251], off offset:1412
	global_load_dwordx4 v[234:237], v[252:253], off
	global_load_dwordx4 v[238:241], v[252:253], off offset:16
	global_load_dwordx4 v[242:245], v[252:253], off offset:128
	global_load_dwordx4 v[246:249], v[252:253], off offset:144
	s_add_u32 s28, s28, 0x30080
	s_addc_u32 s29, s29, 0
	s_add_u32 s71, s30, 0x100
	v_mov_b32_e32 v0, 0
	s_addc_u32 s72, s31, 0
	s_mov_b32 s73, -2
	v_mov_b32_e32 v1, v0
	v_mov_b32_e32 v2, v0
	v_mov_b32_e32 v3, v0
	v_mov_b32_e32 v4, v0
	v_mov_b32_e32 v5, v0
	v_mov_b32_e32 v6, v0
	v_mov_b32_e32 v7, v0
	v_mov_b32_e32 v12, v0
	v_mov_b32_e32 v13, v0
	v_mov_b32_e32 v14, v0
	v_mov_b32_e32 v15, v0
	v_mov_b32_e32 v20, v0
	v_mov_b32_e32 v21, v0
	v_mov_b32_e32 v22, v0
	v_mov_b32_e32 v23, v0
	v_mov_b32_e32 v28, v0
	v_mov_b32_e32 v29, v0
	v_mov_b32_e32 v30, v0
	v_mov_b32_e32 v31, v0
	v_mov_b32_e32 v36, v0
	v_mov_b32_e32 v37, v0
	v_mov_b32_e32 v38, v0
	v_mov_b32_e32 v39, v0
	v_mov_b32_e32 v44, v0
	v_mov_b32_e32 v45, v0
	v_mov_b32_e32 v46, v0
	v_mov_b32_e32 v47, v0
	v_mov_b32_e32 v52, v0
	v_mov_b32_e32 v53, v0
	v_mov_b32_e32 v54, v0
	v_mov_b32_e32 v55, v0
	v_mov_b32_e32 v8, v0
	v_mov_b32_e32 v9, v0
	v_mov_b32_e32 v10, v0
	v_mov_b32_e32 v11, v0
	v_mov_b32_e32 v16, v0
	v_mov_b32_e32 v17, v0
	v_mov_b32_e32 v18, v0
	v_mov_b32_e32 v19, v0
	v_mov_b32_e32 v24, v0
	v_mov_b32_e32 v25, v0
	v_mov_b32_e32 v26, v0
	v_mov_b32_e32 v27, v0
	v_mov_b32_e32 v32, v0
	v_mov_b32_e32 v33, v0
	v_mov_b32_e32 v34, v0
	v_mov_b32_e32 v35, v0
	v_mov_b32_e32 v40, v0
	v_mov_b32_e32 v41, v0
	v_mov_b32_e32 v42, v0
	v_mov_b32_e32 v43, v0
	v_mov_b32_e32 v48, v0
	v_mov_b32_e32 v49, v0
	v_mov_b32_e32 v50, v0
	v_mov_b32_e32 v51, v0
	v_mov_b32_e32 v56, v0
	v_mov_b32_e32 v57, v0
	v_mov_b32_e32 v58, v0
	v_mov_b32_e32 v59, v0
	v_mov_b32_e32 v60, v0
	v_mov_b32_e32 v61, v0
	v_mov_b32_e32 v62, v0
	v_mov_b32_e32 v63, v0
	v_mov_b32_e32 v64, v0
	v_mov_b32_e32 v65, v0
	v_mov_b32_e32 v66, v0
	v_mov_b32_e32 v67, v0
	v_mov_b32_e32 v68, v0
	v_mov_b32_e32 v69, v0
	v_mov_b32_e32 v70, v0
	v_mov_b32_e32 v71, v0
	v_mov_b32_e32 v76, v0
	v_mov_b32_e32 v77, v0
	v_mov_b32_e32 v78, v0
	v_mov_b32_e32 v79, v0
	v_mov_b32_e32 v84, v0
	v_mov_b32_e32 v85, v0
	v_mov_b32_e32 v86, v0
	v_mov_b32_e32 v87, v0
	v_mov_b32_e32 v92, v0
	v_mov_b32_e32 v93, v0
	v_mov_b32_e32 v94, v0
	v_mov_b32_e32 v95, v0
	v_mov_b32_e32 v100, v0
	v_mov_b32_e32 v101, v0
	v_mov_b32_e32 v102, v0
	v_mov_b32_e32 v103, v0
	v_mov_b32_e32 v112, v0
	v_mov_b32_e32 v113, v0
	v_mov_b32_e32 v114, v0
	v_mov_b32_e32 v115, v0
	v_mov_b32_e32 v116, v0
	v_mov_b32_e32 v117, v0
	v_mov_b32_e32 v118, v0
	v_mov_b32_e32 v119, v0
	v_mov_b32_e32 v72, v0
	v_mov_b32_e32 v73, v0
	v_mov_b32_e32 v74, v0
	v_mov_b32_e32 v75, v0
	v_mov_b32_e32 v80, v0
	v_mov_b32_e32 v81, v0
	v_mov_b32_e32 v82, v0
	v_mov_b32_e32 v83, v0
	v_mov_b32_e32 v88, v0
	v_mov_b32_e32 v89, v0
	v_mov_b32_e32 v90, v0
	v_mov_b32_e32 v91, v0
	v_mov_b32_e32 v96, v0
	v_mov_b32_e32 v97, v0
	v_mov_b32_e32 v98, v0
	v_mov_b32_e32 v99, v0
	v_mov_b32_e32 v104, v0
	v_mov_b32_e32 v105, v0
	v_mov_b32_e32 v106, v0
	v_mov_b32_e32 v107, v0
	v_mov_b32_e32 v108, v0
	v_mov_b32_e32 v109, v0
	v_mov_b32_e32 v110, v0
	v_mov_b32_e32 v111, v0
	v_mov_b32_e32 v120, v0
	v_mov_b32_e32 v121, v0
	v_mov_b32_e32 v122, v0
	v_mov_b32_e32 v123, v0
	v_mov_b32_e32 v124, v0
	v_mov_b32_e32 v125, v0
	v_mov_b32_e32 v126, v0
	v_mov_b32_e32 v127, v0
.LBB7_27:
	ds_read_b128 v[128:131], v170
	ds_read_b128 v[132:135], v170 offset:1024
	ds_read_b128 v[136:139], v170 offset:2048
	ds_read_b128 v[140:143], v170 offset:3072
	s_add_u32 s30, s28, 0xfffd0080
	s_addc_u32 s31, s29, -1
	s_cmp_eq_u32 s73, 8
	s_cselect_b32 s35, s9, s31
	s_cselect_b32 s34, s8, s30
	s_cselect_b32 s31, s1, s72
	s_cselect_b32 s30, s0, s71
	v_lshl_add_u64 v[162:163], s[28:29], 0, v[152:153]
	s_add_i32 m0, s43, 0xc000
	ds_read_b128 v[158:161], v171
	ds_read_b128 v[176:179], v171 offset:1024
	ds_read_b128 v[180:183], v171 offset:2048
	ds_read_b128 v[184:187], v171 offset:3072
	ds_read_b128 v[188:191], v171 offset:4096
	ds_read_b128 v[192:195], v171 offset:5120
	ds_read_b128 v[196:199], v171 offset:6144
	ds_read_b128 v[200:203], v171 offset:7168
	global_load_lds_dwordx4 v[162:163], off
	v_lshl_add_u64 v[162:163], s[28:29], 0, v[154:155]
	s_add_i32 m0, s43, 0xe000
	s_nop 0
	global_load_lds_dwordx4 v[162:163], off
	s_cmp_eq_u32 s77, 0
	s_cbranch_scc0 .Lvw_7_1_o
	s_waitcnt vmcnt(10)
.Lvw_7_1_j:
	s_waitcnt lgkmcnt(8)
	s_barrier
	s_waitcnt lgkmcnt(0)
	s_setprio 1
	s_waitcnt lgkmcnt(0)
	v_mfma_f32_16x16x32_f16 v[124:127], v[128:131], v[158:161], v[124:127]
	v_mfma_f32_16x16x32_f16 v[120:123], v[136:139], v[158:161], v[120:123]
	v_mfma_f32_16x16x32_f16 v[108:111], v[128:131], v[180:183], v[108:111]
	v_mfma_f32_16x16x32_f16 v[104:107], v[136:139], v[180:183], v[104:107]
	v_mfma_f32_16x16x32_f16 v[96:99], v[128:131], v[188:191], v[96:99]
	v_mfma_f32_16x16x32_f16 v[88:91], v[136:139], v[188:191], v[88:91]
	v_mfma_f32_16x16x32_f16 v[80:83], v[128:131], v[196:199], v[80:83]
	v_mfma_f32_16x16x32_f16 v[72:75], v[136:139], v[196:199], v[72:75]
	v_mfma_f32_16x16x32_f16 v[124:127], v[132:135], v[176:179], v[124:127]
	v_mfma_f32_16x16x32_f16 v[120:123], v[140:143], v[176:179], v[120:123]
	v_mfma_f32_16x16x32_f16 v[108:111], v[132:135], v[184:187], v[108:111]
	v_mfma_f32_16x16x32_f16 v[104:107], v[140:143], v[184:187], v[104:107]
	v_mfma_f32_16x16x32_f16 v[96:99], v[132:135], v[192:195], v[96:99]
	v_mfma_f32_16x16x32_f16 v[88:91], v[140:143], v[192:195], v[88:91]
	v_mfma_f32_16x16x32_f16 v[80:83], v[132:135], v[200:203], v[80:83]
	v_mfma_f32_16x16x32_f16 v[72:75], v[140:143], v[200:203], v[72:75]
	s_setprio 0
	s_barrier
	s_add_i32 s74, s65, s42
	v_lshl_add_u64 v[162:163], s[30:31], 0, v[146:147]
	s_mov_b32 m0, s74
	ds_read_b128 v[204:207], v172
	ds_read_b128 v[208:211], v172 offset:1024
	ds_read_b128 v[212:215], v172 offset:2048
	ds_read_b128 v[216:219], v172 offset:3072
	global_load_lds_dwordx4 v[162:163], off
	v_lshl_add_u64 v[220:221], s[30:31], 0, v[150:151]
	s_add_i32 m0, s74, 0x2000
	s_nop 0
	global_load_lds_dwordx4 v[220:221], off
	s_cmp_eq_u32 s77, 0
	s_cbranch_scc0 .Lvw_7_2_o
	s_waitcnt vmcnt(10)
.Lvw_7_2_j:
	s_barrier
	s_waitcnt lgkmcnt(0)
	s_setprio 1
	s_waitcnt lgkmcnt(0)
	v_mfma_f32_16x16x32_f16 v[116:119], v[204:207], v[158:161], v[116:119]
	v_mfma_f32_16x16x32_f16 v[112:115], v[212:215], v[158:161], v[112:115]
	v_mfma_f32_16x16x32_f16 v[100:103], v[204:207], v[180:183], v[100:103]
	v_mfma_f32_16x16x32_f16 v[92:95], v[212:215], v[180:183], v[92:95]
	v_mfma_f32_16x16x32_f16 v[84:87], v[204:207], v[188:191], v[84:87]
	v_mfma_f32_16x16x32_f16 v[76:79], v[212:215], v[188:191], v[76:79]
	v_mfma_f32_16x16x32_f16 v[68:71], v[204:207], v[196:199], v[68:71]
	v_mfma_f32_16x16x32_f16 v[64:67], v[212:215], v[196:199], v[64:67]
	v_mfma_f32_16x16x32_f16 v[116:119], v[208:211], v[176:179], v[116:119]
	v_mfma_f32_16x16x32_f16 v[112:115], v[216:219], v[176:179], v[112:115]
	v_mfma_f32_16x16x32_f16 v[100:103], v[208:211], v[184:187], v[100:103]
	v_mfma_f32_16x16x32_f16 v[92:95], v[216:219], v[184:187], v[92:95]
	v_mfma_f32_16x16x32_f16 v[84:87], v[208:211], v[192:195], v[84:87]
	v_mfma_f32_16x16x32_f16 v[76:79], v[216:219], v[192:195], v[76:79]
	v_mfma_f32_16x16x32_f16 v[68:71], v[208:211], v[200:203], v[68:71]
	v_mfma_f32_16x16x32_f16 v[64:67], v[216:219], v[200:203], v[64:67]
	s_setprio 0
	s_mov_b32 m0, s43
	v_lshl_add_u64 v[222:223], s[34:35], 0, v[144:145]
	s_barrier
	ds_read_b128 v[158:161], v171 offset:16384
	ds_read_b128 v[176:179], v171 offset:17408
	ds_read_b128 v[180:183], v171 offset:18432
	ds_read_b128 v[184:187], v171 offset:19456
	ds_read_b128 v[188:191], v171 offset:20480
	ds_read_b128 v[192:195], v171 offset:21504
	ds_read_b128 v[196:199], v171 offset:22528
	ds_read_b128 v[200:203], v171 offset:23552
	global_load_lds_dwordx4 v[222:223], off
	v_lshl_add_u64 v[224:225], s[34:35], 0, v[148:149]
	s_mov_b32 m0, s44
	s_nop 0
	global_load_lds_dwordx4 v[224:225], off
	s_barrier
	s_waitcnt lgkmcnt(0)
	s_setprio 1
	s_waitcnt lgkmcnt(0)
	v_mfma_f32_16x16x32_f16 v[60:63], v[128:131], v[158:161], v[60:63]
	v_mfma_f32_16x16x32_f16 v[56:59], v[136:139], v[158:161], v[56:59]
	v_mfma_f32_16x16x32_f16 v[48:51], v[128:131], v[180:183], v[48:51]
	v_mfma_f32_16x16x32_f16 v[40:43], v[136:139], v[180:183], v[40:43]
	v_mfma_f32_16x16x32_f16 v[32:35], v[128:131], v[188:191], v[32:35]
	v_mfma_f32_16x16x32_f16 v[24:27], v[136:139], v[188:191], v[24:27]
	v_mfma_f32_16x16x32_f16 v[16:19], v[128:131], v[196:199], v[16:19]
	v_mfma_f32_16x16x32_f16 v[8:11], v[136:139], v[196:199], v[8:11]
	v_mfma_f32_16x16x32_f16 v[60:63], v[132:135], v[176:179], v[60:63]
	v_mfma_f32_16x16x32_f16 v[56:59], v[140:143], v[176:179], v[56:59]
	v_mfma_f32_16x16x32_f16 v[48:51], v[132:135], v[184:187], v[48:51]
	v_mfma_f32_16x16x32_f16 v[40:43], v[140:143], v[184:187], v[40:43]
	v_mfma_f32_16x16x32_f16 v[32:35], v[132:135], v[192:195], v[32:35]
	v_mfma_f32_16x16x32_f16 v[24:27], v[140:143], v[192:195], v[24:27]
	v_mfma_f32_16x16x32_f16 v[16:19], v[132:135], v[200:203], v[16:19]
	v_mfma_f32_16x16x32_f16 v[8:11], v[140:143], v[200:203], v[8:11]
	s_setprio 0
	s_barrier
	s_add_u32 s74, s30, 0xc000
	s_addc_u32 s75, s31, 0
	s_add_i32 s76, s66, s42
	v_lshl_add_u64 v[128:129], s[74:75], 0, v[146:147]
	s_mov_b32 m0, s76
	s_nop 0
	global_load_lds_dwordx4 v[128:129], off
	v_lshl_add_u64 v[128:129], s[74:75], 0, v[150:151]
	s_add_i32 m0, s76, 0x2000
	s_nop 0
	global_load_lds_dwordx4 v[128:129], off
	s_cmp_eq_u32 s77, 0
	s_cbranch_scc0 .Lvw_7_4_o
	s_waitcnt vmcnt(10)
.Lvw_7_4_j:
	s_barrier
	s_setprio 1
	v_mfma_f32_16x16x32_f16 v[52:55], v[204:207], v[158:161], v[52:55]
	v_mfma_f32_16x16x32_f16 v[44:47], v[212:215], v[158:161], v[44:47]
	v_mfma_f32_16x16x32_f16 v[36:39], v[204:207], v[180:183], v[36:39]
	v_mfma_f32_16x16x32_f16 v[28:31], v[212:215], v[180:183], v[28:31]
	v_mfma_f32_16x16x32_f16 v[20:23], v[204:207], v[188:191], v[20:23]
	v_mfma_f32_16x16x32_f16 v[12:15], v[212:215], v[188:191], v[12:15]
	v_mfma_f32_16x16x32_f16 v[4:7], v[204:207], v[196:199], v[4:7]
	v_mfma_f32_16x16x32_f16 v[0:3], v[212:215], v[196:199], v[0:3]
	v_mfma_f32_16x16x32_f16 v[52:55], v[208:211], v[176:179], v[52:55]
	v_mfma_f32_16x16x32_f16 v[44:47], v[216:219], v[176:179], v[44:47]
	v_mfma_f32_16x16x32_f16 v[36:39], v[208:211], v[184:187], v[36:39]
	v_mfma_f32_16x16x32_f16 v[28:31], v[216:219], v[184:187], v[28:31]
	v_mfma_f32_16x16x32_f16 v[20:23], v[208:211], v[192:195], v[20:23]
	v_mfma_f32_16x16x32_f16 v[12:15], v[216:219], v[192:195], v[12:15]
	v_mfma_f32_16x16x32_f16 v[4:7], v[208:211], v[200:203], v[4:7]
	v_mfma_f32_16x16x32_f16 v[0:3], v[216:219], v[200:203], v[0:3]
	s_setprio 0
	s_add_i32 s74, 0, 0x18000
	v_add_u32_e32 v140, s74, v166
	s_barrier
	ds_read_b128 v[128:131], v140
	ds_read_b128 v[132:135], v140 offset:1024
	ds_read_b128 v[136:139], v140 offset:2048
	ds_read_b128 v[140:143], v140 offset:3072
	s_add_u32 s34, s34, 0x30000
	s_addc_u32 s35, s35, 0
	s_mov_b32 m0, s45
	v_lshl_add_u64 v[204:205], s[34:35], 0, v[144:145]
	ds_read_b128 v[158:161], v171 offset:32768
	ds_read_b128 v[176:179], v171 offset:33792
	ds_read_b128 v[180:183], v171 offset:34816
	ds_read_b128 v[184:187], v171 offset:35840
	ds_read_b128 v[188:191], v171 offset:36864
	ds_read_b128 v[192:195], v171 offset:37888
	ds_read_b128 v[196:199], v171 offset:38912
	ds_read_b128 v[200:203], v171 offset:39936
	global_load_lds_dwordx4 v[204:205], off
	v_lshl_add_u64 v[204:205], s[34:35], 0, v[148:149]
	s_mov_b32 m0, s46
	s_nop 0
	global_load_lds_dwordx4 v[204:205], off
	s_cmp_eq_u32 s77, 0
	s_cbranch_scc0 .Lvw_7_5_o
	s_waitcnt vmcnt(10)
.Lvw_7_5_j:
	s_waitcnt lgkmcnt(8)
	s_barrier
	s_waitcnt lgkmcnt(0)
	s_setprio 1
	s_waitcnt lgkmcnt(0)
	v_mfma_f32_16x16x32_f16 v[124:127], v[128:131], v[158:161], v[124:127]
	v_mfma_f32_16x16x32_f16 v[120:123], v[136:139], v[158:161], v[120:123]
	v_mfma_f32_16x16x32_f16 v[108:111], v[128:131], v[180:183], v[108:111]
	v_mfma_f32_16x16x32_f16 v[104:107], v[136:139], v[180:183], v[104:107]
	v_mfma_f32_16x16x32_f16 v[96:99], v[128:131], v[188:191], v[96:99]
	v_mfma_f32_16x16x32_f16 v[88:91], v[136:139], v[188:191], v[88:91]
	v_mfma_f32_16x16x32_f16 v[80:83], v[128:131], v[196:199], v[80:83]
	v_mfma_f32_16x16x32_f16 v[72:75], v[136:139], v[196:199], v[72:75]
	v_mfma_f32_16x16x32_f16 v[124:127], v[132:135], v[176:179], v[124:127]
	v_mfma_f32_16x16x32_f16 v[120:123], v[140:143], v[176:179], v[120:123]
	v_mfma_f32_16x16x32_f16 v[108:111], v[132:135], v[184:187], v[108:111]
	v_mfma_f32_16x16x32_f16 v[104:107], v[140:143], v[184:187], v[104:107]
	v_mfma_f32_16x16x32_f16 v[96:99], v[132:135], v[192:195], v[96:99]
	v_mfma_f32_16x16x32_f16 v[88:91], v[140:143], v[192:195], v[88:91]
	v_mfma_f32_16x16x32_f16 v[80:83], v[132:135], v[200:203], v[80:83]
	v_mfma_f32_16x16x32_f16 v[72:75], v[140:143], v[200:203], v[72:75]
	s_setprio 0
	s_barrier
	s_add_i32 s34, 0, 0x1c000
	s_add_i32 s35, s74, s42
	v_add_u32_e32 v175, s34, v166
	v_lshl_add_u64 v[162:163], v[162:163], 0, s[26:27]
	s_mov_b32 m0, s35
	ds_read_b128 v[204:207], v175
	ds_read_b128 v[208:211], v175 offset:1024
	ds_read_b128 v[212:215], v175 offset:2048
	ds_read_b128 v[216:219], v175 offset:3072
	global_load_lds_dwordx4 v[162:163], off
	v_lshl_add_u64 v[162:163], v[220:221], 0, s[26:27]
	s_add_i32 m0, s35, 0x2000
	s_nop 0
	global_load_lds_dwordx4 v[162:163], off
	s_waitcnt vmcnt(10)
	s_barrier
	s_waitcnt lgkmcnt(0)
	s_setprio 1
	s_waitcnt lgkmcnt(0)
	v_mfma_f32_16x16x32_f16 v[116:119], v[204:207], v[158:161], v[116:119]
	v_mfma_f32_16x16x32_f16 v[112:115], v[212:215], v[158:161], v[112:115]
	v_mfma_f32_16x16x32_f16 v[100:103], v[204:207], v[180:183], v[100:103]
	v_mfma_f32_16x16x32_f16 v[92:95], v[212:215], v[180:183], v[92:95]
	v_mfma_f32_16x16x32_f16 v[84:87], v[204:207], v[188:191], v[84:87]
	v_mfma_f32_16x16x32_f16 v[76:79], v[212:215], v[188:191], v[76:79]
	v_mfma_f32_16x16x32_f16 v[68:71], v[204:207], v[196:199], v[68:71]
	v_mfma_f32_16x16x32_f16 v[64:67], v[212:215], v[196:199], v[64:67]
	v_mfma_f32_16x16x32_f16 v[116:119], v[208:211], v[176:179], v[116:119]
	v_mfma_f32_16x16x32_f16 v[112:115], v[216:219], v[176:179], v[112:115]
	v_mfma_f32_16x16x32_f16 v[100:103], v[208:211], v[184:187], v[100:103]
	v_mfma_f32_16x16x32_f16 v[92:95], v[216:219], v[184:187], v[92:95]
	v_mfma_f32_16x16x32_f16 v[84:87], v[208:211], v[192:195], v[84:87]
	v_mfma_f32_16x16x32_f16 v[76:79], v[216:219], v[192:195], v[76:79]
	v_mfma_f32_16x16x32_f16 v[68:71], v[208:211], v[200:203], v[68:71]
	v_mfma_f32_16x16x32_f16 v[64:67], v[216:219], v[200:203], v[64:67]
	s_setprio 0
	s_mov_b32 m0, s49
	v_lshl_add_u64 v[162:163], v[222:223], 0, s[26:27]
	s_barrier
	ds_read_b128 v[158:161], v171 offset:49152
	ds_read_b128 v[176:179], v171 offset:50176
	ds_read_b128 v[180:183], v171 offset:51200
	ds_read_b128 v[184:187], v171 offset:52224
	ds_read_b128 v[188:191], v171 offset:53248
	ds_read_b128 v[192:195], v171 offset:54272
	ds_read_b128 v[196:199], v171 offset:55296
	ds_read_b128 v[200:203], v171 offset:56320
	global_load_lds_dwordx4 v[162:163], off
	v_lshl_add_u64 v[162:163], v[224:225], 0, s[26:27]
	s_mov_b32 m0, s50
	s_nop 0
	global_load_lds_dwordx4 v[162:163], off
	s_barrier
	s_waitcnt lgkmcnt(0)
	s_setprio 1
	s_waitcnt lgkmcnt(0)
	v_mfma_f32_16x16x32_f16 v[60:63], v[128:131], v[158:161], v[60:63]
	v_mfma_f32_16x16x32_f16 v[56:59], v[136:139], v[158:161], v[56:59]
	v_mfma_f32_16x16x32_f16 v[48:51], v[128:131], v[180:183], v[48:51]
	v_mfma_f32_16x16x32_f16 v[40:43], v[136:139], v[180:183], v[40:43]
	v_mfma_f32_16x16x32_f16 v[32:35], v[128:131], v[188:191], v[32:35]
	v_mfma_f32_16x16x32_f16 v[24:27], v[136:139], v[188:191], v[24:27]
	v_mfma_f32_16x16x32_f16 v[16:19], v[128:131], v[196:199], v[16:19]
	v_mfma_f32_16x16x32_f16 v[8:11], v[136:139], v[196:199], v[8:11]
	v_mfma_f32_16x16x32_f16 v[60:63], v[132:135], v[176:179], v[60:63]
	v_mfma_f32_16x16x32_f16 v[56:59], v[140:143], v[176:179], v[56:59]
	v_mfma_f32_16x16x32_f16 v[48:51], v[132:135], v[184:187], v[48:51]
	v_mfma_f32_16x16x32_f16 v[40:43], v[140:143], v[184:187], v[40:43]
	v_mfma_f32_16x16x32_f16 v[32:35], v[132:135], v[192:195], v[32:35]
	v_mfma_f32_16x16x32_f16 v[24:27], v[140:143], v[192:195], v[24:27]
	v_mfma_f32_16x16x32_f16 v[16:19], v[132:135], v[200:203], v[16:19]
	v_mfma_f32_16x16x32_f16 v[8:11], v[140:143], v[200:203], v[8:11]
	s_setprio 0
	s_barrier
	s_add_u32 s30, s30, 0xc080
	s_addc_u32 s31, s31, 0
	s_add_i32 s34, s34, s42
	v_lshl_add_u64 v[128:129], s[30:31], 0, v[146:147]
	s_mov_b32 m0, s34
	s_nop 0
	global_load_lds_dwordx4 v[128:129], off
	v_lshl_add_u64 v[128:129], s[30:31], 0, v[150:151]
	s_add_i32 m0, s34, 0x2000
	s_nop 0
	global_load_lds_dwordx4 v[128:129], off
	s_waitcnt vmcnt(10)
	s_barrier
	s_setprio 1
	v_mfma_f32_16x16x32_f16 v[52:55], v[204:207], v[158:161], v[52:55]
	v_mfma_f32_16x16x32_f16 v[44:47], v[212:215], v[158:161], v[44:47]
	v_mfma_f32_16x16x32_f16 v[36:39], v[204:207], v[180:183], v[36:39]
	v_mfma_f32_16x16x32_f16 v[28:31], v[212:215], v[180:183], v[28:31]
	v_mfma_f32_16x16x32_f16 v[20:23], v[204:207], v[188:191], v[20:23]
	v_mfma_f32_16x16x32_f16 v[12:15], v[212:215], v[188:191], v[12:15]
	v_mfma_f32_16x16x32_f16 v[4:7], v[204:207], v[196:199], v[4:7]
	v_mfma_f32_16x16x32_f16 v[0:3], v[212:215], v[196:199], v[0:3]
	v_mfma_f32_16x16x32_f16 v[52:55], v[208:211], v[176:179], v[52:55]
	v_mfma_f32_16x16x32_f16 v[44:47], v[216:219], v[176:179], v[44:47]
	v_mfma_f32_16x16x32_f16 v[36:39], v[208:211], v[184:187], v[36:39]
	v_mfma_f32_16x16x32_f16 v[28:31], v[216:219], v[184:187], v[28:31]
	v_mfma_f32_16x16x32_f16 v[20:23], v[208:211], v[192:195], v[20:23]
	v_mfma_f32_16x16x32_f16 v[12:15], v[216:219], v[192:195], v[12:15]
	v_mfma_f32_16x16x32_f16 v[4:7], v[208:211], v[200:203], v[4:7]
	v_mfma_f32_16x16x32_f16 v[0:3], v[216:219], v[200:203], v[0:3]
	s_setprio 0
	s_add_i32 s73, s73, 2
	s_add_u32 s28, s28, 0x100
	s_addc_u32 s29, s29, 0
	s_add_u32 s71, s71, 0x100
	s_addc_u32 s72, s72, 0
	s_mov_b32 s77, 0
	s_cmp_gt_u32 s73, 9
	s_barrier
	s_cbranch_scc0 .LBB7_27
	s_lshl_b32 s28, s70, 8
	s_add_i32 s28, s28, s48
	s_lshl_b32 s29, s67, 8
	s_or_b32 s29, s29, s51
	s_waitcnt vmcnt(6)
	v_pk_fma_f32 v[126:127], v[126:127], v[226:227], v[236:237] op_sel_hi:[1,0,1]
	v_pk_fma_f32 v[124:125], v[124:125], v[226:227], v[234:235] op_sel_hi:[1,0,1]
	v_pk_fma_f32 v[186:187], v[122:123], v[226:227], v[240:241] op_sel_hi:[1,0,1]
	v_pk_fma_f32 v[122:123], v[120:121], v[226:227], v[238:239] op_sel_hi:[1,0,1]
	v_cvt_pk_f16_f32 v120, v124, v125
	v_cvt_pk_f16_f32 v121, v126, v127
	v_cvt_pk_f16_f32 v122, v122, v123
	v_cvt_pk_f16_f32 v123, v186, v187
	ds_write_b128 v173, v[120:123]
	v_pk_fma_f32 v[118:119], v[118:119], v[226:227], v[244:245] op_sel_hi:[1,0,1]
	v_pk_fma_f32 v[116:117], v[116:117], v[226:227], v[242:243] op_sel_hi:[1,0,1]
	v_pk_fma_f32 v[120:121], v[114:115], v[226:227], v[248:249] op_sel_hi:[1,0,1]
	v_pk_fma_f32 v[114:115], v[112:113], v[226:227], v[246:247] op_sel_hi:[1,0,1]
	v_cvt_pk_f16_f32 v112, v116, v117
	v_cvt_pk_f16_f32 v113, v118, v119
	v_cvt_pk_f16_f32 v114, v114, v115
	v_cvt_pk_f16_f32 v115, v120, v121
	ds_write_b128 v173, v[112:115] offset:64
	v_or_b32_e32 v116, s28, v167
	ds_read_b128 v[112:115], v174
	v_mul_lo_u32 v116, v116, s10
	v_add_u32_e32 v120, s29, v116
	v_lshlrev_b32_e32 v121, 1, v120
	v_add_u32_e32 v122, v121, v168
	ds_read_b128 v[116:119], v174 offset:1152
	s_waitcnt lgkmcnt(0)
	buffer_store_dwordx4 v[112:115], v122, s[20:23], 0 offen nt
	v_pk_fma_f32 v[110:111], v[110:111], v[226:227], v[236:237] op_sel:[0,1,0]
	v_pk_fma_f32 v[108:109], v[108:109], v[226:227], v[234:235] op_sel:[0,1,0]
	v_pk_fma_f32 v[112:113], v[106:107], v[226:227], v[240:241] op_sel:[0,1,0]
	v_pk_fma_f32 v[106:107], v[104:105], v[226:227], v[238:239] op_sel:[0,1,0]
	v_cvt_pk_f16_f32 v104, v108, v109
	v_cvt_pk_f16_f32 v105, v110, v111
	v_cvt_pk_f16_f32 v106, v106, v107
	v_cvt_pk_f16_f32 v107, v112, v113
	ds_write_b128 v173, v[104:107]
	v_pk_fma_f32 v[102:103], v[102:103], v[226:227], v[244:245] op_sel:[0,1,0]
	v_pk_fma_f32 v[100:101], v[100:101], v[226:227], v[242:243] op_sel:[0,1,0]
	v_pk_fma_f32 v[104:105], v[94:95], v[226:227], v[248:249] op_sel:[0,1,0]
	v_pk_fma_f32 v[94:95], v[92:93], v[226:227], v[246:247] op_sel:[0,1,0]
	v_cvt_pk_f16_f32 v92, v100, v101
	v_cvt_pk_f16_f32 v93, v102, v103
	v_cvt_pk_f16_f32 v94, v94, v95
	v_cvt_pk_f16_f32 v95, v104, v105
	ds_write_b128 v173, v[92:95] offset:64
	ds_read_b128 v[92:95], v174
	ds_read_b128 v[100:103], v174 offset:1152
	v_add_u32_e32 v104, s55, v121
	v_add_u32_e32 v114, v121, v169
	v_add_u32_e32 v105, v104, v168
	buffer_store_dwordx4 v[116:119], v114, s[20:23], 0 offen nt
	s_waitcnt lgkmcnt(1)
	buffer_store_dwordx4 v[92:95], v105, s[20:23], 0 offen nt
	v_pk_fma_f32 v[86:87], v[86:87], v[228:229], v[244:245] op_sel_hi:[1,0,1]
	v_pk_fma_f32 v[84:85], v[84:85], v[228:229], v[242:243] op_sel_hi:[1,0,1]
	v_pk_fma_f32 v[92:93], v[98:99], v[228:229], v[236:237] op_sel_hi:[1,0,1]
	v_pk_fma_f32 v[94:95], v[96:97], v[228:229], v[234:235] op_sel_hi:[1,0,1]
	v_pk_fma_f32 v[96:97], v[90:91], v[228:229], v[240:241] op_sel_hi:[1,0,1]
	v_pk_fma_f32 v[90:91], v[88:89], v[228:229], v[238:239] op_sel_hi:[1,0,1]
	v_cvt_pk_f16_f32 v88, v94, v95
	v_cvt_pk_f16_f32 v89, v92, v93
	v_cvt_pk_f16_f32 v90, v90, v91
	v_cvt_pk_f16_f32 v91, v96, v97
	ds_write_b128 v173, v[88:91]
	v_pk_fma_f32 v[88:89], v[78:79], v[228:229], v[248:249] op_sel_hi:[1,0,1]
	v_pk_fma_f32 v[78:79], v[76:77], v[228:229], v[246:247] op_sel_hi:[1,0,1]
	v_cvt_pk_f16_f32 v76, v84, v85
	v_cvt_pk_f16_f32 v77, v86, v87
	v_cvt_pk_f16_f32 v78, v78, v79
	v_cvt_pk_f16_f32 v79, v88, v89
	ds_write_b128 v173, v[76:79] offset:64
	ds_read_b128 v[76:79], v174
	ds_read_b128 v[84:87], v174 offset:1152
	v_add_u32_e32 v88, s55, v104
	v_add_u32_e32 v105, v104, v169
	v_add_u32_e32 v89, v88, v168
	s_waitcnt lgkmcnt(4)
	buffer_store_dwordx4 v[100:103], v105, s[20:23], 0 offen nt
	s_waitcnt lgkmcnt(1)
	buffer_store_dwordx4 v[76:79], v89, s[20:23], 0 offen nt
	v_pk_fma_f32 v[70:71], v[70:71], v[228:229], v[244:245] op_sel:[0,1,0]
	v_pk_fma_f32 v[68:69], v[68:69], v[228:229], v[242:243] op_sel:[0,1,0]
	v_add_u32_e32 v76, v88, v169
	s_waitcnt lgkmcnt(0)
	buffer_store_dwordx4 v[84:87], v76, s[20:23], 0 offen nt
	v_pk_fma_f32 v[76:77], v[82:83], v[228:229], v[236:237] op_sel:[0,1,0]
	v_pk_fma_f32 v[78:79], v[80:81], v[228:229], v[234:235] op_sel:[0,1,0]
	v_pk_fma_f32 v[80:81], v[74:75], v[228:229], v[240:241] op_sel:[0,1,0]
	v_pk_fma_f32 v[74:75], v[72:73], v[228:229], v[238:239] op_sel:[0,1,0]
	v_cvt_pk_f16_f32 v72, v78, v79
	v_cvt_pk_f16_f32 v73, v76, v77
	v_cvt_pk_f16_f32 v74, v74, v75
	v_cvt_pk_f16_f32 v75, v80, v81
	ds_write_b128 v173, v[72:75]
	v_pk_fma_f32 v[72:73], v[66:67], v[228:229], v[248:249] op_sel:[0,1,0]
	v_pk_fma_f32 v[66:67], v[64:65], v[228:229], v[246:247] op_sel:[0,1,0]
	v_cvt_pk_f16_f32 v64, v68, v69
	v_cvt_pk_f16_f32 v65, v70, v71
	v_cvt_pk_f16_f32 v66, v66, v67
	v_cvt_pk_f16_f32 v67, v72, v73
	ds_write_b128 v173, v[64:67] offset:64
	ds_read_b128 v[64:67], v174
	ds_read_b128 v[68:71], v174 offset:1152
	v_add_u32_e32 v72, s56, v120
	v_lshlrev_b32_e32 v73, 1, v72
	v_add_u32_e32 v74, v73, v168
	s_waitcnt lgkmcnt(1)
	buffer_store_dwordx4 v[64:67], v74, s[20:23], 0 offen nt
	v_pk_fma_f32 v[62:63], v[62:63], v[230:231], v[236:237] op_sel_hi:[1,0,1]
	v_pk_fma_f32 v[60:61], v[60:61], v[230:231], v[234:235] op_sel_hi:[1,0,1]
	v_pk_fma_f32 v[64:65], v[58:59], v[230:231], v[240:241] op_sel_hi:[1,0,1]
	v_pk_fma_f32 v[58:59], v[56:57], v[230:231], v[238:239] op_sel_hi:[1,0,1]
	v_cvt_pk_f16_f32 v56, v60, v61
	v_cvt_pk_f16_f32 v57, v62, v63
	v_cvt_pk_f16_f32 v58, v58, v59
	v_cvt_pk_f16_f32 v59, v64, v65
	ds_write_b128 v173, v[56:59]
	v_pk_fma_f32 v[54:55], v[54:55], v[230:231], v[244:245] op_sel_hi:[1,0,1]
	v_pk_fma_f32 v[52:53], v[52:53], v[230:231], v[242:243] op_sel_hi:[1,0,1]
	v_pk_fma_f32 v[56:57], v[46:47], v[230:231], v[248:249] op_sel_hi:[1,0,1]
	v_pk_fma_f32 v[46:47], v[44:45], v[230:231], v[246:247] op_sel_hi:[1,0,1]
	v_cvt_pk_f16_f32 v44, v52, v53
	v_cvt_pk_f16_f32 v45, v54, v55
	v_cvt_pk_f16_f32 v46, v46, v47
	v_cvt_pk_f16_f32 v47, v56, v57
	ds_write_b128 v173, v[44:47] offset:64
	ds_read_b128 v[44:47], v174
	ds_read_b128 v[52:55], v174 offset:1152
	v_add_u32_e32 v56, s62, v88
	v_add_u32_e32 v66, v73, v169
	v_add_u32_e32 v57, v56, v168
	s_waitcnt lgkmcnt(4)
	buffer_store_dwordx4 v[68:71], v66, s[20:23], 0 offen nt
	s_waitcnt lgkmcnt(1)
	buffer_store_dwordx4 v[44:47], v57, s[20:23], 0 offen nt
	v_pk_fma_f32 v[38:39], v[38:39], v[230:231], v[244:245] op_sel:[0,1,0]
	v_pk_fma_f32 v[36:37], v[36:37], v[230:231], v[242:243] op_sel:[0,1,0]
	v_add_u32_e32 v44, v56, v169
	s_waitcnt lgkmcnt(0)
	buffer_store_dwordx4 v[52:55], v44, s[20:23], 0 offen nt
	v_pk_fma_f32 v[44:45], v[50:51], v[230:231], v[236:237] op_sel:[0,1,0]
	v_pk_fma_f32 v[46:47], v[48:49], v[230:231], v[234:235] op_sel:[0,1,0]
	v_pk_fma_f32 v[48:49], v[42:43], v[230:231], v[240:241] op_sel:[0,1,0]
	v_pk_fma_f32 v[42:43], v[40:41], v[230:231], v[238:239] op_sel:[0,1,0]
	v_cvt_pk_f16_f32 v40, v46, v47
	v_cvt_pk_f16_f32 v41, v44, v45
	v_cvt_pk_f16_f32 v42, v42, v43
	v_cvt_pk_f16_f32 v43, v48, v49
	ds_write_b128 v173, v[40:43]
	v_pk_fma_f32 v[40:41], v[30:31], v[230:231], v[248:249] op_sel:[0,1,0]
	v_pk_fma_f32 v[30:31], v[28:29], v[230:231], v[246:247] op_sel:[0,1,0]
	v_cvt_pk_f16_f32 v28, v36, v37
	v_cvt_pk_f16_f32 v29, v38, v39
	v_cvt_pk_f16_f32 v30, v30, v31
	v_cvt_pk_f16_f32 v31, v40, v41
	ds_write_b128 v173, v[28:31] offset:64
	ds_read_b128 v[28:31], v174
	ds_read_b128 v[36:39], v174 offset:1152
	v_add_u32_e32 v40, s63, v72
	v_lshlrev_b32_e32 v41, 1, v40
	v_add_u32_e32 v42, v41, v168
	s_waitcnt lgkmcnt(1)
	buffer_store_dwordx4 v[28:31], v42, s[20:23], 0 offen nt
	v_pk_fma_f32 v[22:23], v[22:23], v[232:233], v[244:245] op_sel_hi:[1,0,1]
	v_pk_fma_f32 v[20:21], v[20:21], v[232:233], v[242:243] op_sel_hi:[1,0,1]
	v_add_u32_e32 v28, v41, v169
	s_waitcnt lgkmcnt(0)
	buffer_store_dwordx4 v[36:39], v28, s[20:23], 0 offen nt
	v_pk_fma_f32 v[28:29], v[34:35], v[232:233], v[236:237] op_sel_hi:[1,0,1]
	v_pk_fma_f32 v[30:31], v[32:33], v[232:233], v[234:235] op_sel_hi:[1,0,1]
	v_pk_fma_f32 v[32:33], v[26:27], v[232:233], v[240:241] op_sel_hi:[1,0,1]
	v_pk_fma_f32 v[26:27], v[24:25], v[232:233], v[238:239] op_sel_hi:[1,0,1]
	v_cvt_pk_f16_f32 v24, v30, v31
	v_cvt_pk_f16_f32 v25, v28, v29
	v_cvt_pk_f16_f32 v26, v26, v27
	v_cvt_pk_f16_f32 v27, v32, v33
	ds_write_b128 v173, v[24:27]
	v_pk_fma_f32 v[24:25], v[14:15], v[232:233], v[248:249] op_sel_hi:[1,0,1]
	v_pk_fma_f32 v[14:15], v[12:13], v[232:233], v[246:247] op_sel_hi:[1,0,1]
	v_cvt_pk_f16_f32 v12, v20, v21
	v_cvt_pk_f16_f32 v13, v22, v23
	v_cvt_pk_f16_f32 v14, v14, v15
	v_cvt_pk_f16_f32 v15, v24, v25
	ds_write_b128 v173, v[12:15] offset:64
	ds_read_b128 v[12:15], v174
	ds_read_b128 v[20:23], v174 offset:1152
	v_add_u32_e32 v24, s64, v40
	v_lshlrev_b32_e32 v25, 1, v24
	v_add_u32_e32 v26, v25, v168
	s_waitcnt lgkmcnt(1)
	buffer_store_dwordx4 v[12:15], v26, s[20:23], 0 offen nt
	v_pk_fma_f32 v[6:7], v[6:7], v[232:233], v[244:245] op_sel:[0,1,0]
	v_pk_fma_f32 v[4:5], v[4:5], v[232:233], v[242:243] op_sel:[0,1,0]
	v_pk_fma_f32 v[12:13], v[18:19], v[232:233], v[236:237] op_sel:[0,1,0]
	v_pk_fma_f32 v[14:15], v[16:17], v[232:233], v[234:235] op_sel:[0,1,0]
	v_pk_fma_f32 v[16:17], v[10:11], v[232:233], v[240:241] op_sel:[0,1,0]
	v_pk_fma_f32 v[10:11], v[8:9], v[232:233], v[238:239] op_sel:[0,1,0]
	v_cvt_pk_f16_f32 v8, v14, v15
	v_cvt_pk_f16_f32 v9, v12, v13
	v_cvt_pk_f16_f32 v10, v10, v11
	v_cvt_pk_f16_f32 v11, v16, v17
	ds_write_b128 v173, v[8:11]
	v_pk_fma_f32 v[8:9], v[2:3], v[232:233], v[248:249] op_sel:[0,1,0]
	v_pk_fma_f32 v[2:3], v[0:1], v[232:233], v[246:247] op_sel:[0,1,0]
	v_cvt_pk_f16_f32 v0, v4, v5
	v_cvt_pk_f16_f32 v1, v6, v7
	v_cvt_pk_f16_f32 v2, v2, v3
	v_cvt_pk_f16_f32 v3, v8, v9
	ds_write_b128 v173, v[0:3] offset:64
	ds_read_b128 v[0:3], v174
	ds_read_b128 v[4:7], v174 offset:1152
	v_add_lshl_u32 v8, v24, s64, 1
	v_add_u32_e32 v25, v25, v169
	v_add_u32_e32 v9, v8, v168
	s_waitcnt lgkmcnt(4)
	buffer_store_dwordx4 v[20:23], v25, s[20:23], 0 offen nt
	s_waitcnt lgkmcnt(1)
	buffer_store_dwordx4 v[0:3], v9, s[20:23], 0 offen nt
	s_mov_b32 s67, s68
	s_mov_b32 s70, s69
	v_add_u32_e32 v0, v8, v169
	s_mov_b64 s[30:31], s[0:1]
	s_mov_b64 s[28:29], s[8:9]
	s_mov_b64 vcc, s[6:7]
	s_waitcnt lgkmcnt(0)
	buffer_store_dwordx4 v[4:7], v0, s[20:23], 0 offen nt
	s_cbranch_vccz .LBB7_12
	s_waitcnt vmcnt(0)
	s_cmpk_gt_u32 s36, 0xff
	s_cbranch_scc1 .LBB7_31
	s_barrier

.Lvw_7_1_o:
	s_cmp_eq_u32 s77, 1
	s_cbranch_scc1 .Lvw_7_1_t0
	s_waitcnt vmcnt(38)
	s_branch .Lvw_7_1_j
.Lvw_7_1_t0:
	s_waitcnt vmcnt(22)
	s_branch .Lvw_7_1_j

.Lvw_7_4_t0:
	s_waitcnt vmcnt(22)
	s_branch .Lvw_7_4_j
	s_endpgm
	s_endpgm
	s_endpgm
	s_endpgm
	s_endpgm
	s_endpgm
	s_endpgm
	s_endpgm
	s_endpgm
	s_endpgm
	s_endpgm
	s_endpgm
	s_endpgm
	s_endpgm
	s_endpgm
	s_endpgm

	.amdhsa_kernel _Z6k_gemmIN2pg6EpiLinILi0EEELi768EEvNS0_4GemmET_
		.amdhsa_group_segment_fixed_size 0
		.amdhsa_private_segment_fixed_size 0
		.amdhsa_kernarg_size 320
		.amdhsa_user_sgpr_count 2
		.amdhsa_user_sgpr_dispatch_ptr 0
		.amdhsa_user_sgpr_queue_ptr 0
		.amdhsa_user_sgpr_kernarg_segment_ptr 1
		.amdhsa_user_sgpr_dispatch_id 0
		.amdhsa_user_sgpr_kernarg_preload_length 0
		.amdhsa_user_sgpr_kernarg_preload_offset 0
		.amdhsa_user_sgpr_private_segment_size 0
		.amdhsa_uses_dynamic_stack 0
		.amdhsa_enable_private_segment 0
		.amdhsa_system_sgpr_workgroup_id_x 1
		.amdhsa_system_sgpr_workgroup_id_y 0
		.amdhsa_system_sgpr_workgroup_id_z 0
		.amdhsa_system_sgpr_workgroup_info 0
		.amdhsa_system_vgpr_workitem_id 0
		.amdhsa_next_free_vgpr 254
		.amdhsa_next_free_sgpr 78
		.amdhsa_accum_offset 256
		.amdhsa_reserve_vcc 1
		.amdhsa_float_round_mode_32 0
		.amdhsa_float_round_mode_16_64 0
		.amdhsa_float_denorm_mode_32 3
		.amdhsa_float_denorm_mode_16_64 3
		.amdhsa_dx10_clamp 1
		.amdhsa_ieee_mode 1
		.amdhsa_fp16_overflow 0
		.amdhsa_tg_split 0
		.amdhsa_exception_fp_ieee_invalid_op 0
		.amdhsa_exception_fp_denorm_src 0
		.amdhsa_exception_fp_ieee_div_zero 0
		.amdhsa_exception_fp_ieee_overflow 0
		.amdhsa_exception_fp_ieee_underflow 0
		.amdhsa_exception_fp_ieee_inexact 0
		.amdhsa_exception_int_div_zero 0
	.end_amdhsa_kernel

.LBB8_26:
	s_cmp_eq_u32 s80, 1
	s_cselect_b32 s91, 0, 2
	s_add_u32 s38, s38, 0x30080
	s_addc_u32 s39, s39, 0
	s_add_u32 s85, s40, 0x100
	v_mov_b32_e32 v0, 0
	s_addc_u32 s86, s41, 0
	s_mov_b32 s87, -2
	v_mov_b32_e32 v1, v0
	v_mov_b32_e32 v2, v0
	v_mov_b32_e32 v3, v0
	v_mov_b32_e32 v4, v0
	v_mov_b32_e32 v5, v0
	v_mov_b32_e32 v6, v0
	v_mov_b32_e32 v7, v0
	v_mov_b32_e32 v16, v0
	v_mov_b32_e32 v17, v0
	v_mov_b32_e32 v18, v0
	v_mov_b32_e32 v19, v0
	v_mov_b32_e32 v20, v0
	v_mov_b32_e32 v21, v0
	v_mov_b32_e32 v22, v0
	v_mov_b32_e32 v23, v0
	v_mov_b32_e32 v32, v0
	v_mov_b32_e32 v33, v0
	v_mov_b32_e32 v34, v0
	v_mov_b32_e32 v35, v0
	v_mov_b32_e32 v36, v0
	v_mov_b32_e32 v37, v0
	v_mov_b32_e32 v38, v0
	v_mov_b32_e32 v39, v0
	v_mov_b32_e32 v48, v0
	v_mov_b32_e32 v49, v0
	v_mov_b32_e32 v50, v0
	v_mov_b32_e32 v51, v0
	v_mov_b32_e32 v52, v0
	v_mov_b32_e32 v53, v0
	v_mov_b32_e32 v54, v0
	v_mov_b32_e32 v55, v0
	v_mov_b32_e32 v8, v0
	v_mov_b32_e32 v9, v0
	v_mov_b32_e32 v10, v0
	v_mov_b32_e32 v11, v0
	v_mov_b32_e32 v12, v0
	v_mov_b32_e32 v13, v0
	v_mov_b32_e32 v14, v0
	v_mov_b32_e32 v15, v0
	v_mov_b32_e32 v24, v0
	v_mov_b32_e32 v25, v0
	v_mov_b32_e32 v26, v0
	v_mov_b32_e32 v27, v0
	v_mov_b32_e32 v28, v0
	v_mov_b32_e32 v29, v0
	v_mov_b32_e32 v30, v0
	v_mov_b32_e32 v31, v0
	v_mov_b32_e32 v40, v0
	v_mov_b32_e32 v41, v0
	v_mov_b32_e32 v42, v0
	v_mov_b32_e32 v43, v0
	v_mov_b32_e32 v44, v0
	v_mov_b32_e32 v45, v0
	v_mov_b32_e32 v46, v0
	v_mov_b32_e32 v47, v0
	v_mov_b32_e32 v56, v0
	v_mov_b32_e32 v57, v0
	v_mov_b32_e32 v58, v0
	v_mov_b32_e32 v59, v0
	v_mov_b32_e32 v60, v0
	v_mov_b32_e32 v61, v0
	v_mov_b32_e32 v62, v0
	v_mov_b32_e32 v63, v0
	v_mov_b32_e32 v64, v0
	v_mov_b32_e32 v65, v0
	v_mov_b32_e32 v66, v0
	v_mov_b32_e32 v67, v0
	v_mov_b32_e32 v68, v0
	v_mov_b32_e32 v69, v0
	v_mov_b32_e32 v70, v0
	v_mov_b32_e32 v71, v0
	v_mov_b32_e32 v96, v0
	v_mov_b32_e32 v97, v0
	v_mov_b32_e32 v98, v0
	v_mov_b32_e32 v99, v0
	v_mov_b32_e32 v100, v0
	v_mov_b32_e32 v101, v0
	v_mov_b32_e32 v102, v0
	v_mov_b32_e32 v103, v0
	v_mov_b32_e32 v112, v0
	v_mov_b32_e32 v113, v0
	v_mov_b32_e32 v114, v0
	v_mov_b32_e32 v115, v0
	v_mov_b32_e32 v116, v0
	v_mov_b32_e32 v117, v0
	v_mov_b32_e32 v118, v0
	v_mov_b32_e32 v119, v0
	v_mov_b32_e32 v128, v0
	v_mov_b32_e32 v129, v0
	v_mov_b32_e32 v130, v0
	v_mov_b32_e32 v131, v0
	v_mov_b32_e32 v132, v0
	v_mov_b32_e32 v133, v0
	v_mov_b32_e32 v134, v0
	v_mov_b32_e32 v135, v0
	v_mov_b32_e32 v76, v0
	v_mov_b32_e32 v77, v0
	v_mov_b32_e32 v78, v0
	v_mov_b32_e32 v79, v0
	v_mov_b32_e32 v84, v0
	v_mov_b32_e32 v85, v0
	v_mov_b32_e32 v86, v0
	v_mov_b32_e32 v87, v0
	v_mov_b32_e32 v104, v0
	v_mov_b32_e32 v105, v0
	v_mov_b32_e32 v106, v0
	v_mov_b32_e32 v107, v0
	v_mov_b32_e32 v108, v0
	v_mov_b32_e32 v109, v0
	v_mov_b32_e32 v110, v0
	v_mov_b32_e32 v111, v0
	v_mov_b32_e32 v120, v0
	v_mov_b32_e32 v121, v0
	v_mov_b32_e32 v122, v0
	v_mov_b32_e32 v123, v0
	v_mov_b32_e32 v124, v0
	v_mov_b32_e32 v125, v0
	v_mov_b32_e32 v126, v0
	v_mov_b32_e32 v127, v0
	v_mov_b32_e32 v140, v0
	v_mov_b32_e32 v141, v0
	v_mov_b32_e32 v142, v0
	v_mov_b32_e32 v143, v0
	v_mov_b32_e32 v144, v0
	v_mov_b32_e32 v145, v0
	v_mov_b32_e32 v146, v0
	v_mov_b32_e32 v147, v0
.LBB8_27:
	ds_read_b128 v[72:75], v231
	ds_read_b128 v[80:83], v231 offset:1024
	ds_read_b128 v[88:91], v231 offset:2048
	ds_read_b128 v[92:95], v231 offset:3072
	s_add_u32 s40, s38, 0xfffd0080
	s_addc_u32 s41, s39, -1
	s_cmp_eq_u32 s87, 8
	s_cselect_b32 s43, s9, s41
	s_cselect_b32 s42, s8, s40
	s_cselect_b32 s41, s1, s86
	s_cselect_b32 s40, s0, s85
	v_lshl_add_u64 v[190:191], s[38:39], 0, v[184:185]
	s_add_i32 m0, s51, 0xc000
	ds_read_b128 v[136:139], v232
	ds_read_b128 v[148:151], v232 offset:1024
	ds_read_b128 v[152:155], v232 offset:2048
	ds_read_b128 v[156:159], v232 offset:3072
	ds_read_b128 v[160:163], v232 offset:4096
	ds_read_b128 v[164:167], v232 offset:5120
	ds_read_b128 v[168:171], v232 offset:6144
	ds_read_b128 v[172:175], v232 offset:7168
	global_load_lds_dwordx4 v[190:191], off
	v_lshl_add_u64 v[190:191], s[38:39], 0, v[186:187]
	s_add_i32 m0, s51, 0xe000
	s_nop 0
	global_load_lds_dwordx4 v[190:191], off
	s_cmp_eq_u32 s91, 0
	s_cbranch_scc0 .Lvw_8_1_j
	s_waitcnt vmcnt(10)
.Lvw_8_1_j:
	s_waitcnt lgkmcnt(8)
	s_barrier
	s_waitcnt lgkmcnt(0)
	s_setprio 1
	s_waitcnt lgkmcnt(0)
	v_mfma_f32_16x16x32_f16 v[144:147], v[72:75], v[136:139], v[144:147]
	v_mfma_f32_16x16x32_f16 v[140:143], v[88:91], v[136:139], v[140:143]
	v_mfma_f32_16x16x32_f16 v[124:127], v[72:75], v[152:155], v[124:127]
	v_mfma_f32_16x16x32_f16 v[120:123], v[88:91], v[152:155], v[120:123]
	v_mfma_f32_16x16x32_f16 v[108:111], v[72:75], v[160:163], v[108:111]
	v_mfma_f32_16x16x32_f16 v[104:107], v[88:91], v[160:163], v[104:107]
	v_mfma_f32_16x16x32_f16 v[84:87], v[72:75], v[168:171], v[84:87]
	v_mfma_f32_16x16x32_f16 v[76:79], v[88:91], v[168:171], v[76:79]
	v_mfma_f32_16x16x32_f16 v[144:147], v[80:83], v[148:151], v[144:147]
	v_mfma_f32_16x16x32_f16 v[140:143], v[92:95], v[148:151], v[140:143]
	v_mfma_f32_16x16x32_f16 v[124:127], v[80:83], v[156:159], v[124:127]
	v_mfma_f32_16x16x32_f16 v[120:123], v[92:95], v[156:159], v[120:123]
	v_mfma_f32_16x16x32_f16 v[108:111], v[80:83], v[164:167], v[108:111]
	v_mfma_f32_16x16x32_f16 v[104:107], v[92:95], v[164:167], v[104:107]
	v_mfma_f32_16x16x32_f16 v[84:87], v[80:83], v[172:175], v[84:87]
	v_mfma_f32_16x16x32_f16 v[76:79], v[92:95], v[172:175], v[76:79]
	s_setprio 0
	s_barrier
	s_add_i32 s88, s70, s50
	v_lshl_add_u64 v[206:207], s[40:41], 0, v[178:179]
	s_mov_b32 m0, s88
	ds_read_b128 v[190:193], v233
	ds_read_b128 v[194:197], v233 offset:1024
	ds_read_b128 v[198:201], v233 offset:2048
	ds_read_b128 v[202:205], v233 offset:3072
	global_load_lds_dwordx4 v[206:207], off
	v_lshl_add_u64 v[208:209], s[40:41], 0, v[182:183]
	s_add_i32 m0, s88, 0x2000
	s_nop 0
	global_load_lds_dwordx4 v[208:209], off
	s_cmp_eq_u32 s91, 0
	s_cbranch_scc0 .Lvw_8_2_j
	s_waitcnt vmcnt(10)
.Lvw_8_2_j:
	s_barrier
	s_waitcnt lgkmcnt(0)
	s_setprio 1
	s_waitcnt lgkmcnt(0)
	v_mfma_f32_16x16x32_f16 v[132:135], v[190:193], v[136:139], v[132:135]
	v_mfma_f32_16x16x32_f16 v[128:131], v[198:201], v[136:139], v[128:131]
	v_mfma_f32_16x16x32_f16 v[116:119], v[190:193], v[152:155], v[116:119]
	v_mfma_f32_16x16x32_f16 v[112:115], v[198:201], v[152:155], v[112:115]
	v_mfma_f32_16x16x32_f16 v[100:103], v[190:193], v[160:163], v[100:103]
	v_mfma_f32_16x16x32_f16 v[96:99], v[198:201], v[160:163], v[96:99]
	v_mfma_f32_16x16x32_f16 v[68:71], v[190:193], v[168:171], v[68:71]
	v_mfma_f32_16x16x32_f16 v[64:67], v[198:201], v[168:171], v[64:67]
	v_mfma_f32_16x16x32_f16 v[132:135], v[194:197], v[148:151], v[132:135]
	v_mfma_f32_16x16x32_f16 v[128:131], v[202:205], v[148:151], v[128:131]
	v_mfma_f32_16x16x32_f16 v[116:119], v[194:197], v[156:159], v[116:119]
	v_mfma_f32_16x16x32_f16 v[112:115], v[202:205], v[156:159], v[112:115]
	v_mfma_f32_16x16x32_f16 v[100:103], v[194:197], v[164:167], v[100:103]
	v_mfma_f32_16x16x32_f16 v[96:99], v[202:205], v[164:167], v[96:99]
	v_mfma_f32_16x16x32_f16 v[68:71], v[194:197], v[172:175], v[68:71]
	v_mfma_f32_16x16x32_f16 v[64:67], v[202:205], v[172:175], v[64:67]
	s_setprio 0
	s_mov_b32 m0, s51
	v_lshl_add_u64 v[210:211], s[42:43], 0, v[176:177]
	s_barrier
	ds_read_b128 v[136:139], v232 offset:16384
	ds_read_b128 v[148:151], v232 offset:17408
	ds_read_b128 v[152:155], v232 offset:18432
	ds_read_b128 v[156:159], v232 offset:19456
	ds_read_b128 v[160:163], v232 offset:20480
	ds_read_b128 v[164:167], v232 offset:21504
	ds_read_b128 v[168:171], v232 offset:22528
	ds_read_b128 v[172:175], v232 offset:23552
	global_load_lds_dwordx4 v[210:211], off
	v_lshl_add_u64 v[212:213], s[42:43], 0, v[180:181]
	s_mov_b32 m0, s52
	s_nop 0
	global_load_lds_dwordx4 v[212:213], off
	s_barrier
	s_waitcnt lgkmcnt(0)
	s_setprio 1
	s_waitcnt lgkmcnt(0)
	v_mfma_f32_16x16x32_f16 v[60:63], v[72:75], v[136:139], v[60:63]
	v_mfma_f32_16x16x32_f16 v[56:59], v[88:91], v[136:139], v[56:59]
	v_mfma_f32_16x16x32_f16 v[44:47], v[72:75], v[152:155], v[44:47]
	v_mfma_f32_16x16x32_f16 v[40:43], v[88:91], v[152:155], v[40:43]
	v_mfma_f32_16x16x32_f16 v[28:31], v[72:75], v[160:163], v[28:31]
	v_mfma_f32_16x16x32_f16 v[24:27], v[88:91], v[160:163], v[24:27]
	v_mfma_f32_16x16x32_f16 v[12:15], v[72:75], v[168:171], v[12:15]
	v_mfma_f32_16x16x32_f16 v[8:11], v[88:91], v[168:171], v[8:11]
	v_mfma_f32_16x16x32_f16 v[60:63], v[80:83], v[148:151], v[60:63]
	v_mfma_f32_16x16x32_f16 v[56:59], v[92:95], v[148:151], v[56:59]
	v_mfma_f32_16x16x32_f16 v[44:47], v[80:83], v[156:159], v[44:47]
	v_mfma_f32_16x16x32_f16 v[40:43], v[92:95], v[156:159], v[40:43]
	v_mfma_f32_16x16x32_f16 v[28:31], v[80:83], v[164:167], v[28:31]
	v_mfma_f32_16x16x32_f16 v[24:27], v[92:95], v[164:167], v[24:27]
	v_mfma_f32_16x16x32_f16 v[12:15], v[80:83], v[172:175], v[12:15]
	v_mfma_f32_16x16x32_f16 v[8:11], v[92:95], v[172:175], v[8:11]
	s_setprio 0
	s_barrier
	s_add_u32 s88, s40, 0xc000
	s_addc_u32 s89, s41, 0
	s_add_i32 s90, s71, s50
	v_lshl_add_u64 v[72:73], s[88:89], 0, v[178:179]
	s_mov_b32 m0, s90
	s_nop 0
	global_load_lds_dwordx4 v[72:73], off
	v_lshl_add_u64 v[72:73], s[88:89], 0, v[182:183]
	s_add_i32 m0, s90, 0x2000
	s_nop 0
	global_load_lds_dwordx4 v[72:73], off
	s_cmp_eq_u32 s91, 0
	s_cbranch_scc0 .Lvw_8_4_j
	s_waitcnt vmcnt(10)
.Lvw_8_4_j:
	s_barrier
	s_setprio 1
	v_mfma_f32_16x16x32_f16 v[52:55], v[190:193], v[136:139], v[52:55]
	v_mfma_f32_16x16x32_f16 v[48:51], v[198:201], v[136:139], v[48:51]
	v_mfma_f32_16x16x32_f16 v[36:39], v[190:193], v[152:155], v[36:39]
	v_mfma_f32_16x16x32_f16 v[32:35], v[198:201], v[152:155], v[32:35]
	v_mfma_f32_16x16x32_f16 v[20:23], v[190:193], v[160:163], v[20:23]
	v_mfma_f32_16x16x32_f16 v[16:19], v[198:201], v[160:163], v[16:19]
	v_mfma_f32_16x16x32_f16 v[4:7], v[190:193], v[168:171], v[4:7]
	v_mfma_f32_16x16x32_f16 v[0:3], v[198:201], v[168:171], v[0:3]
	v_mfma_f32_16x16x32_f16 v[52:55], v[194:197], v[148:151], v[52:55]
	v_mfma_f32_16x16x32_f16 v[48:51], v[202:205], v[148:151], v[48:51]
	v_mfma_f32_16x16x32_f16 v[36:39], v[194:197], v[156:159], v[36:39]
	v_mfma_f32_16x16x32_f16 v[32:35], v[202:205], v[156:159], v[32:35]
	v_mfma_f32_16x16x32_f16 v[20:23], v[194:197], v[164:167], v[20:23]
	v_mfma_f32_16x16x32_f16 v[16:19], v[202:205], v[164:167], v[16:19]
	v_mfma_f32_16x16x32_f16 v[4:7], v[194:197], v[172:175], v[4:7]
	v_mfma_f32_16x16x32_f16 v[0:3], v[202:205], v[172:175], v[0:3]
	s_setprio 0
	s_add_i32 s88, 0, 0x18000
	v_add_u32_e32 v92, s88, v228
	s_barrier
	ds_read_b128 v[72:75], v92
	ds_read_b128 v[80:83], v92 offset:1024
	ds_read_b128 v[88:91], v92 offset:2048
	ds_read_b128 v[92:95], v92 offset:3072
	s_add_u32 s42, s42, 0x30000
	s_addc_u32 s43, s43, 0
	s_mov_b32 m0, s53
	v_lshl_add_u64 v[190:191], s[42:43], 0, v[176:177]
	ds_read_b128 v[136:139], v232 offset:32768
	ds_read_b128 v[148:151], v232 offset:33792
	ds_read_b128 v[152:155], v232 offset:34816
	ds_read_b128 v[156:159], v232 offset:35840
	ds_read_b128 v[160:163], v232 offset:36864
	ds_read_b128 v[164:167], v232 offset:37888
	ds_read_b128 v[168:171], v232 offset:38912
	ds_read_b128 v[172:175], v232 offset:39936
	global_load_lds_dwordx4 v[190:191], off
	v_lshl_add_u64 v[190:191], s[42:43], 0, v[180:181]
	s_mov_b32 m0, s54
	s_nop 0
	global_load_lds_dwordx4 v[190:191], off
	s_cmp_eq_u32 s91, 0
	s_cbranch_scc0 .Lvw_8_5_j
	s_waitcnt vmcnt(10)
.Lvw_8_5_j:
	s_waitcnt lgkmcnt(8)
	s_barrier
	s_waitcnt lgkmcnt(0)
	s_setprio 1
	s_waitcnt lgkmcnt(0)
	v_mfma_f32_16x16x32_f16 v[144:147], v[72:75], v[136:139], v[144:147]
	v_mfma_f32_16x16x32_f16 v[140:143], v[88:91], v[136:139], v[140:143]
	v_mfma_f32_16x16x32_f16 v[124:127], v[72:75], v[152:155], v[124:127]
	v_mfma_f32_16x16x32_f16 v[120:123], v[88:91], v[152:155], v[120:123]
	v_mfma_f32_16x16x32_f16 v[108:111], v[72:75], v[160:163], v[108:111]
	v_mfma_f32_16x16x32_f16 v[104:107], v[88:91], v[160:163], v[104:107]
	v_mfma_f32_16x16x32_f16 v[84:87], v[72:75], v[168:171], v[84:87]
	v_mfma_f32_16x16x32_f16 v[76:79], v[88:91], v[168:171], v[76:79]
	v_mfma_f32_16x16x32_f16 v[144:147], v[80:83], v[148:151], v[144:147]
	v_mfma_f32_16x16x32_f16 v[140:143], v[92:95], v[148:151], v[140:143]
	v_mfma_f32_16x16x32_f16 v[124:127], v[80:83], v[156:159], v[124:127]
	v_mfma_f32_16x16x32_f16 v[120:123], v[92:95], v[156:159], v[120:123]
	v_mfma_f32_16x16x32_f16 v[108:111], v[80:83], v[164:167], v[108:111]
	v_mfma_f32_16x16x32_f16 v[104:107], v[92:95], v[164:167], v[104:107]
	v_mfma_f32_16x16x32_f16 v[84:87], v[80:83], v[172:175], v[84:87]
	v_mfma_f32_16x16x32_f16 v[76:79], v[92:95], v[172:175], v[76:79]
	s_setprio 0
	s_barrier
	s_add_i32 s42, 0, 0x1c000
	s_add_i32 s43, s88, s50
	v_add_u32_e32 v202, s42, v228
	v_lshl_add_u64 v[206:207], v[206:207], 0, s[36:37]
	s_mov_b32 m0, s43
	ds_read_b128 v[190:193], v202
	ds_read_b128 v[194:197], v202 offset:1024
	ds_read_b128 v[198:201], v202 offset:2048
	ds_read_b128 v[202:205], v202 offset:3072
	global_load_lds_dwordx4 v[206:207], off
	v_lshl_add_u64 v[206:207], v[208:209], 0, s[36:37]
	s_add_i32 m0, s43, 0x2000
	s_nop 0
	global_load_lds_dwordx4 v[206:207], off
	s_waitcnt vmcnt(10)
	s_barrier
	s_waitcnt lgkmcnt(0)
	s_setprio 1
	s_waitcnt lgkmcnt(0)
	v_mfma_f32_16x16x32_f16 v[132:135], v[190:193], v[136:139], v[132:135]
	v_mfma_f32_16x16x32_f16 v[128:131], v[198:201], v[136:139], v[128:131]
	v_mfma_f32_16x16x32_f16 v[116:119], v[190:193], v[152:155], v[116:119]
	v_mfma_f32_16x16x32_f16 v[112:115], v[198:201], v[152:155], v[112:115]
	v_mfma_f32_16x16x32_f16 v[100:103], v[190:193], v[160:163], v[100:103]
	v_mfma_f32_16x16x32_f16 v[96:99], v[198:201], v[160:163], v[96:99]
	v_mfma_f32_16x16x32_f16 v[68:71], v[190:193], v[168:171], v[68:71]
	v_mfma_f32_16x16x32_f16 v[64:67], v[198:201], v[168:171], v[64:67]
	v_mfma_f32_16x16x32_f16 v[132:135], v[194:197], v[148:151], v[132:135]
	v_mfma_f32_16x16x32_f16 v[128:131], v[202:205], v[148:151], v[128:131]
	v_mfma_f32_16x16x32_f16 v[116:119], v[194:197], v[156:159], v[116:119]
	v_mfma_f32_16x16x32_f16 v[112:115], v[202:205], v[156:159], v[112:115]
	v_mfma_f32_16x16x32_f16 v[100:103], v[194:197], v[164:167], v[100:103]
	v_mfma_f32_16x16x32_f16 v[96:99], v[202:205], v[164:167], v[96:99]
	v_mfma_f32_16x16x32_f16 v[68:71], v[194:197], v[172:175], v[68:71]
	v_mfma_f32_16x16x32_f16 v[64:67], v[202:205], v[172:175], v[64:67]
	s_setprio 0
	s_mov_b32 m0, s59
	v_lshl_add_u64 v[206:207], v[210:211], 0, s[36:37]
	s_barrier
	ds_read_b128 v[136:139], v232 offset:49152
	ds_read_b128 v[148:151], v232 offset:50176
	ds_read_b128 v[152:155], v232 offset:51200
	ds_read_b128 v[156:159], v232 offset:52224
	ds_read_b128 v[160:163], v232 offset:53248
	ds_read_b128 v[164:167], v232 offset:54272
	ds_read_b128 v[168:171], v232 offset:55296
	ds_read_b128 v[172:175], v232 offset:56320
	global_load_lds_dwordx4 v[206:207], off
	v_lshl_add_u64 v[206:207], v[212:213], 0, s[36:37]
	s_mov_b32 m0, s60
	s_nop 0
	global_load_lds_dwordx4 v[206:207], off
	s_barrier
	s_waitcnt lgkmcnt(0)
	s_setprio 1
	s_waitcnt lgkmcnt(0)
	v_mfma_f32_16x16x32_f16 v[60:63], v[72:75], v[136:139], v[60:63]
	v_mfma_f32_16x16x32_f16 v[56:59], v[88:91], v[136:139], v[56:59]
	v_mfma_f32_16x16x32_f16 v[44:47], v[72:75], v[152:155], v[44:47]
	v_mfma_f32_16x16x32_f16 v[40:43], v[88:91], v[152:155], v[40:43]
	v_mfma_f32_16x16x32_f16 v[28:31], v[72:75], v[160:163], v[28:31]
	v_mfma_f32_16x16x32_f16 v[24:27], v[88:91], v[160:163], v[24:27]
	v_mfma_f32_16x16x32_f16 v[12:15], v[72:75], v[168:171], v[12:15]
	v_mfma_f32_16x16x32_f16 v[8:11], v[88:91], v[168:171], v[8:11]
	v_mfma_f32_16x16x32_f16 v[60:63], v[80:83], v[148:151], v[60:63]
	v_mfma_f32_16x16x32_f16 v[56:59], v[92:95], v[148:151], v[56:59]
	v_mfma_f32_16x16x32_f16 v[44:47], v[80:83], v[156:159], v[44:47]
	v_mfma_f32_16x16x32_f16 v[40:43], v[92:95], v[156:159], v[40:43]
	v_mfma_f32_16x16x32_f16 v[28:31], v[80:83], v[164:167], v[28:31]
	v_mfma_f32_16x16x32_f16 v[24:27], v[92:95], v[164:167], v[24:27]
	v_mfma_f32_16x16x32_f16 v[12:15], v[80:83], v[172:175], v[12:15]
	v_mfma_f32_16x16x32_f16 v[8:11], v[92:95], v[172:175], v[8:11]
	s_setprio 0
	s_barrier
	s_add_u32 s40, s40, 0xc080
	s_addc_u32 s41, s41, 0
	s_add_i32 s42, s42, s50
	v_lshl_add_u64 v[72:73], s[40:41], 0, v[178:179]
	s_mov_b32 m0, s42
	s_nop 0
	global_load_lds_dwordx4 v[72:73], off
	v_lshl_add_u64 v[72:73], s[40:41], 0, v[182:183]
	s_add_i32 m0, s42, 0x2000
	s_nop 0
	global_load_lds_dwordx4 v[72:73], off
	s_waitcnt vmcnt(10)
	s_barrier
	s_setprio 1
	v_mfma_f32_16x16x32_f16 v[52:55], v[190:193], v[136:139], v[52:55]
	v_mfma_f32_16x16x32_f16 v[48:51], v[198:201], v[136:139], v[48:51]
	v_mfma_f32_16x16x32_f16 v[36:39], v[190:193], v[152:155], v[36:39]
	v_mfma_f32_16x16x32_f16 v[32:35], v[198:201], v[152:155], v[32:35]
	v_mfma_f32_16x16x32_f16 v[20:23], v[190:193], v[160:163], v[20:23]
	v_mfma_f32_16x16x32_f16 v[16:19], v[198:201], v[160:163], v[16:19]
	v_mfma_f32_16x16x32_f16 v[4:7], v[190:193], v[168:171], v[4:7]
	v_mfma_f32_16x16x32_f16 v[0:3], v[198:201], v[168:171], v[0:3]
	v_mfma_f32_16x16x32_f16 v[52:55], v[194:197], v[148:151], v[52:55]
	v_mfma_f32_16x16x32_f16 v[48:51], v[202:205], v[148:151], v[48:51]
	v_mfma_f32_16x16x32_f16 v[36:39], v[194:197], v[156:159], v[36:39]
	v_mfma_f32_16x16x32_f16 v[32:35], v[202:205], v[156:159], v[32:35]
	v_mfma_f32_16x16x32_f16 v[20:23], v[194:197], v[164:167], v[20:23]
	v_mfma_f32_16x16x32_f16 v[16:19], v[202:205], v[164:167], v[16:19]
	v_mfma_f32_16x16x32_f16 v[4:7], v[194:197], v[172:175], v[4:7]
	v_mfma_f32_16x16x32_f16 v[0:3], v[202:205], v[172:175], v[0:3]
	s_setprio 0
	s_add_i32 s87, s87, 2
	s_add_u32 s38, s38, 0x100
	s_addc_u32 s39, s39, 0
	s_add_u32 s85, s85, 0x100
	s_addc_u32 s86, s86, 0
	s_mov_b32 s91, 0
	s_cmp_gt_u32 s87, 9
	s_barrier
	s_cbranch_scc0 .LBB8_27
	s_lshl_b32 s38, s84, 8
	s_lshl_b32 s39, s83, 8
	s_add_i32 s38, s38, s58
	s_or_b32 s39, s39, s61
	v_or_b32_e32 v72, s39, v226
	v_or_b32_e32 v220, s38, v227
	v_mov_b64_e32 v[74:75], s[10:11]
	v_mad_i64_i32 v[74:75], s[40:41], v220, s72, v[74:75]
	v_ashrrev_i32_e32 v73, 31, v72
	v_lshl_add_u64 v[214:215], v[72:73], 1, v[74:75]
	v_add_co_u32_e32 v74, vcc, 0x6000, v214
	global_load_dwordx4 v[172:175], v[214:215], off nt
	global_load_dwordx4 v[168:171], v[214:215], off offset:64 nt
	v_addc_co_u32_e32 v75, vcc, 0, v215, vcc
	global_load_dwordx4 v[164:167], v[74:75], off nt
	global_load_dwordx4 v[160:163], v[74:75], off offset:64 nt
	v_add_co_u32_e32 v74, vcc, 0xc000, v214
	v_ashrrev_i32_e32 v221, 31, v220
	s_nop 0
	v_addc_co_u32_e32 v75, vcc, 0, v215, vcc
	global_load_dwordx4 v[156:159], v[74:75], off nt
	global_load_dwordx4 v[152:155], v[74:75], off offset:64 nt
	v_add_co_u32_e32 v74, vcc, s57, v214
	v_lshlrev_b64 v[72:73], 2, v[72:73]
	s_nop 0
	v_addc_co_u32_e32 v75, vcc, 0, v215, vcc
	global_load_dwordx4 v[148:151], v[74:75], off nt
	global_load_dwordx4 v[136:139], v[74:75], off offset:64 nt
	v_lshl_add_u64 v[74:75], v[220:221], 3, s[12:13]
	v_lshl_add_u64 v[238:239], s[14:15], 0, v[72:73]
	global_load_dwordx2 v[224:225], v[74:75], off
	global_load_dwordx2 v[222:223], v[74:75], off offset:128
	global_load_dwordx2 v[218:219], v[74:75], off offset:256
	global_load_dwordx2 v[216:217], v[74:75], off offset:384
	global_load_dwordx2 v[212:213], v[74:75], off offset:1024
	global_load_dwordx2 v[210:211], v[74:75], off offset:1152
	global_load_dwordx2 v[196:197], v[74:75], off offset:1280
	global_load_dwordx2 v[190:191], v[74:75], off offset:1408
	v_lshl_add_u64 v[242:243], s[16:17], 0, v[72:73]
	v_lshl_add_u64 v[246:247], s[18:19], 0, v[72:73]
	global_load_dwordx4 v[88:91], v[238:239], off offset:16
	global_load_dwordx4 v[92:95], v[238:239], off
	global_load_dwordx4 v[72:75], v[242:243], off offset:16
	global_load_dwordx4 v[80:83], v[242:243], off
	global_load_dwordx4 v[192:195], v[246:247], off offset:16
	global_load_dwordx4 v[198:201], v[246:247], off
	v_or_b32_e32 v221, s38, v229
	v_mul_lo_u32 v221, v221, s56
	v_and_b32_e32 v237, 64, v234
	v_add_u32_e32 v237, 64, v237
	s_lshl_b32 s38, s83, 2
	s_waitcnt vmcnt(0)
	v_pk_add_f32 v[202:203], v[74:75], v[194:195]
	v_pk_add_f32 v[206:207], v[82:83], v[200:201]
	v_pk_add_f32 v[208:209], v[80:81], v[198:199]
	v_pk_add_f32 v[204:205], v[72:73], v[192:193]
	global_load_dwordx4 v[72:75], v[238:239], off offset:144
	global_load_dwordx4 v[80:83], v[238:239], off offset:128
	s_nop 0
	global_load_dwordx4 v[238:241], v[242:243], off offset:144
	global_load_dwordx4 v[192:195], v[242:243], off offset:128
	s_nop 0
	global_load_dwordx4 v[242:245], v[246:247], off offset:144
	s_nop 0
	global_load_dwordx4 v[246:249], v[246:247], off offset:128
	v_pk_add_f32 v[146:147], v[146:147], v[206:207]
	v_pk_add_f32 v[144:145], v[144:145], v[208:209]
	v_pk_add_f32 v[142:143], v[142:143], v[202:203]
	v_pk_add_f32 v[140:141], v[140:141], v[204:205]
	v_pk_add_f32 v[126:127], v[126:127], v[206:207]
	v_pk_add_f32 v[124:125], v[124:125], v[208:209]
	v_pk_add_f32 v[122:123], v[122:123], v[202:203]
	v_pk_add_f32 v[120:121], v[120:121], v[204:205]
	s_waitcnt vmcnt(0)
	v_pk_add_f32 v[198:199], v[194:195], v[248:249]
	v_pk_add_f32 v[194:195], v[238:239], v[242:243]
	v_add_u32_e32 v238, s39, v221
	v_xor_b32_e32 v221, 16, v234
	v_cmp_lt_i32_e32 vcc, v221, v237
	v_xor_b32_e32 v239, 32, v234
	v_pk_add_f32 v[200:201], v[192:193], v[246:247]
	v_cndmask_b32_e32 v221, v234, v221, vcc
	v_cmp_lt_i32_e32 vcc, v239, v237
	v_pk_add_f32 v[192:193], v[240:241], v[244:245]
	v_cvt_f32_f16_e32 v240, v172
	v_cndmask_b32_e32 v237, v234, v239, vcc
	v_cvt_f32_f16_sdwa v239, v172 dst_sel:DWORD dst_unused:UNUSED_PAD src0_sel:WORD_1
	v_cvt_f32_f16_sdwa v241, v173 dst_sel:DWORD dst_unused:UNUSED_PAD src0_sel:WORD_1
	v_cvt_f32_f16_e32 v172, v173
	v_cvt_f32_f16_sdwa v242, v174 dst_sel:DWORD dst_unused:UNUSED_PAD src0_sel:WORD_1
	v_cvt_f32_f16_e32 v243, v174
	v_cvt_f32_f16_sdwa v244, v175 dst_sel:DWORD dst_unused:UNUSED_PAD src0_sel:WORD_1
	v_cvt_f32_f16_e32 v245, v175
	v_sub_f32_e32 v172, v172, v224
	v_sub_f32_e32 v173, v241, v224
	v_sub_f32_e32 v174, v240, v224
	v_sub_f32_e32 v175, v239, v224
	v_pk_mul_f32 v[174:175], v[224:225], v[174:175] op_sel:[1,0]
	v_pk_mul_f32 v[172:173], v[224:225], v[172:173] op_sel:[1,0]
	v_pk_fma_f32 v[144:145], v[174:175], v[92:93], v[144:145]
	v_pk_fma_f32 v[146:147], v[172:173], v[94:95], v[146:147]
	v_sub_f32_e32 v172, v245, v224
	v_sub_f32_e32 v173, v244, v224
	v_sub_f32_e32 v174, v243, v224
	v_sub_f32_e32 v175, v242, v224
	v_pk_mul_f32 v[174:175], v[224:225], v[174:175] op_sel:[1,0]
	v_pk_mul_f32 v[172:173], v[224:225], v[172:173] op_sel:[1,0]
	v_pk_add_f32 v[134:135], v[134:135], v[198:199]
	v_pk_fma_f32 v[172:173], v[172:173], v[90:91], v[142:143]
	v_pk_fma_f32 v[142:143], v[174:175], v[88:89], v[140:141]
	v_cvt_f16_f32_e32 v174, v144
	v_cvt_f16_f32_e32 v175, v145
	v_cvt_pk_f16_f32 v140, v144, v145
	v_cvt_f16_f32_e32 v144, v146
	v_cvt_f16_f32_e32 v145, v147
	v_cvt_pk_f16_f32 v141, v146, v147
	v_cvt_f16_f32_e32 v146, v142
	v_cvt_f16_f32_e32 v147, v143
	v_cvt_f16_f32_e32 v239, v172
	v_cvt_f16_f32_e32 v240, v173
	v_cvt_pk_f16_f32 v142, v142, v143
	v_cvt_pk_f16_f32 v143, v172, v173
	ds_write_b128 v235, v[140:143]
	v_cvt_f32_f16_e32 v140, v174
	v_cvt_f32_f16_e32 v141, v175
	v_cvt_f32_f16_e32 v142, v144
	v_cvt_f32_f16_e32 v143, v145
	v_cvt_f32_f16_e32 v145, v146
	v_cvt_f32_f16_e32 v147, v147
	v_cvt_f32_f16_e32 v172, v239
	v_cvt_f32_f16_e32 v173, v240
	v_add_f32_e32 v140, v140, v141
	v_add_f32_e32 v142, v142, v143
	v_add_f32_e32 v140, v140, v142
	v_add_f32_e32 v142, v145, v147
	v_add_f32_e32 v145, v172, v173
	v_add_f32_e32 v142, v142, v145
	v_add_f32_e32 v140, v140, v142
	v_add_f32_e32 v145, 0, v140
	v_mul_f32_e32 v140, v141, v141
	v_mul_f32_e32 v141, v143, v143
	v_fma_mix_f32 v140, v174, v174, v140 op_sel_hi:[1,1,0]
	v_fma_mix_f32 v141, v144, v144, v141 op_sel_hi:[1,1,0]
	v_mul_f32_e32 v142, v173, v173
	v_add_f32_e32 v140, v140, v141
	v_mul_f32_e32 v141, v147, v147
	v_fma_mix_f32 v141, v146, v146, v141 op_sel_hi:[1,1,0]
	v_fma_mix_f32 v142, v239, v239, v142 op_sel_hi:[1,1,0]
	v_cvt_f32_f16_sdwa v143, v168 dst_sel:DWORD dst_unused:UNUSED_PAD src0_sel:WORD_1
	v_add_f32_e32 v141, v141, v142
	v_add_f32_e32 v144, v140, v141
	v_cvt_f32_f16_e32 v142, v168
	v_cvt_f32_f16_sdwa v141, v169 dst_sel:DWORD dst_unused:UNUSED_PAD src0_sel:WORD_1
	v_cvt_f32_f16_e32 v140, v169
	v_cvt_f32_f16_sdwa v146, v170 dst_sel:DWORD dst_unused:UNUSED_PAD src0_sel:WORD_1
	v_cvt_f32_f16_e32 v147, v170
	v_cvt_f32_f16_sdwa v168, v171 dst_sel:DWORD dst_unused:UNUSED_PAD src0_sel:WORD_1
	v_cvt_f32_f16_e32 v169, v171
	v_sub_f32_e32 v140, v140, v224
	v_sub_f32_e32 v141, v141, v224
	v_sub_f32_e32 v142, v142, v224
	v_sub_f32_e32 v143, v143, v224
	v_pk_add_f32 v[132:133], v[132:133], v[200:201]
	v_pk_mul_f32 v[142:143], v[224:225], v[142:143] op_sel:[1,0]
	v_pk_mul_f32 v[140:141], v[224:225], v[140:141] op_sel:[1,0]
	v_pk_fma_f32 v[132:133], v[142:143], v[80:81], v[132:133]
	v_pk_fma_f32 v[134:135], v[140:141], v[82:83], v[134:135]
	v_sub_f32_e32 v140, v169, v224
	v_sub_f32_e32 v141, v168, v224
	v_sub_f32_e32 v142, v147, v224
	v_sub_f32_e32 v143, v146, v224
	v_pk_add_f32 v[130:131], v[130:131], v[192:193]
	v_pk_add_f32 v[128:129], v[128:129], v[194:195]
	v_pk_mul_f32 v[142:143], v[224:225], v[142:143] op_sel:[1,0]
	v_pk_mul_f32 v[140:141], v[224:225], v[140:141] op_sel:[1,0]
	v_lshlrev_b32_e32 v221, 2, v221
	v_pk_fma_f32 v[140:141], v[140:141], v[74:75], v[130:131]
	v_pk_fma_f32 v[130:131], v[142:143], v[72:73], v[128:129]
	v_cvt_f16_f32_e32 v142, v132
	v_cvt_f16_f32_e32 v143, v133
	v_cvt_pk_f16_f32 v128, v132, v133
	v_cvt_f16_f32_e32 v132, v134
	v_cvt_f16_f32_e32 v133, v135
	v_cvt_pk_f16_f32 v129, v134, v135
	v_cvt_f16_f32_e32 v134, v130
	v_cvt_f16_f32_e32 v135, v131
	v_cvt_f16_f32_e32 v146, v140
	v_cvt_f16_f32_e32 v147, v141
	v_cvt_pk_f16_f32 v130, v130, v131
	v_cvt_pk_f16_f32 v131, v140, v141
	ds_write_b128 v235, v[128:131] offset:64
	v_cvt_f32_f16_e32 v128, v142
	v_cvt_f32_f16_e32 v129, v143
	v_cvt_f32_f16_e32 v130, v132
	v_cvt_f32_f16_e32 v131, v133
	v_cvt_f32_f16_e32 v133, v134
	v_cvt_f32_f16_e32 v135, v135
	v_cvt_f32_f16_e32 v140, v146
	v_cvt_f32_f16_e32 v141, v147
	v_add_f32_e32 v128, v128, v129
	v_add_f32_e32 v130, v130, v131
	v_add_f32_e32 v128, v128, v130
	v_add_f32_e32 v130, v133, v135
	v_add_f32_e32 v133, v140, v141
	v_add_f32_e32 v130, v130, v133
	v_add_f32_e32 v128, v128, v130
	v_add_f32_e32 v140, v145, v128
	v_mul_f32_e32 v128, v129, v129
	v_mul_f32_e32 v129, v131, v131
	v_fma_mix_f32 v128, v142, v142, v128 op_sel_hi:[1,1,0]
	v_fma_mix_f32 v129, v132, v132, v129 op_sel_hi:[1,1,0]
	v_mul_f32_e32 v130, v141, v141
	v_add_f32_e32 v128, v128, v129
	v_mul_f32_e32 v129, v135, v135
	ds_bpermute_b32 v142, v221, v140
	v_fma_mix_f32 v129, v134, v134, v129 op_sel_hi:[1,1,0]
	v_fma_mix_f32 v130, v146, v146, v130 op_sel_hi:[1,1,0]
	v_lshlrev_b32_e32 v237, 2, v237
	v_add_f32_e32 v129, v129, v130
	v_add_f32_e32 v128, v128, v129
	v_add_f32_e32 v141, v144, v128
	s_waitcnt lgkmcnt(0)
	v_add_f32_e32 v140, v140, v142
	ds_bpermute_b32 v142, v221, v141
	v_cvt_f32_f16_sdwa v145, v164 dst_sel:DWORD dst_unused:UNUSED_PAD src0_sel:WORD_1
	v_cvt_f32_f16_e32 v144, v164
	v_cvt_f32_f16_sdwa v146, v166 dst_sel:DWORD dst_unused:UNUSED_PAD src0_sel:WORD_1
	v_cvt_f32_f16_e32 v147, v166
	s_waitcnt lgkmcnt(0)
	v_add_f32_e32 v141, v141, v142
	ds_bpermute_b32 v142, v237, v140
	v_cvt_f32_f16_sdwa v164, v167 dst_sel:DWORD dst_unused:UNUSED_PAD src0_sel:WORD_1
	v_sub_f32_e32 v144, v144, v222
	v_sub_f32_e32 v145, v145, v222
	v_pk_mul_f32 v[144:145], v[222:223], v[144:145] op_sel:[1,0]
	s_waitcnt lgkmcnt(0)
	v_add_f32_e32 v142, v140, v142
	ds_bpermute_b32 v140, v237, v141
	v_pk_fma_f32 v[124:125], v[144:145], v[92:93], v[124:125]
	v_sub_f32_e32 v144, v147, v222
	v_sub_f32_e32 v145, v146, v222
	v_pk_mul_f32 v[144:145], v[222:223], v[144:145] op_sel:[1,0]
	s_waitcnt lgkmcnt(0)
	v_add_f32_e32 v143, v141, v140
	v_cvt_f32_f16_sdwa v141, v165 dst_sel:DWORD dst_unused:UNUSED_PAD src0_sel:WORD_1
	v_cvt_f32_f16_e32 v140, v165
	v_cvt_f32_f16_e32 v165, v167
	ds_read_b128 v[132:135], v236
	ds_read_b128 v[128:131], v236 offset:1152
	v_sub_f32_e32 v141, v141, v222
	v_sub_f32_e32 v140, v140, v222
	v_pk_mul_f32 v[140:141], v[222:223], v[140:141] op_sel:[1,0]
	v_pk_add_f32 v[118:119], v[118:119], v[198:199]
	v_pk_fma_f32 v[126:127], v[140:141], v[94:95], v[126:127]
	v_sub_f32_e32 v140, v165, v222
	v_sub_f32_e32 v141, v164, v222
	v_pk_mul_f32 v[140:141], v[222:223], v[140:141] op_sel:[1,0]
	v_pk_add_f32 v[116:117], v[116:117], v[200:201]
	v_pk_fma_f32 v[140:141], v[140:141], v[90:91], v[122:123]
	v_pk_fma_f32 v[122:123], v[144:145], v[88:89], v[120:121]
	v_cvt_f16_f32_e32 v144, v124
	v_cvt_f16_f32_e32 v145, v125
	v_cvt_pk_f16_f32 v120, v124, v125
	v_cvt_f16_f32_e32 v124, v126
	v_cvt_f16_f32_e32 v125, v127
	v_cvt_pk_f16_f32 v121, v126, v127
	v_cvt_f16_f32_e32 v126, v122
	v_cvt_f16_f32_e32 v127, v123
	v_cvt_f16_f32_e32 v146, v140
	v_cvt_f16_f32_e32 v147, v141
	v_cvt_pk_f16_f32 v122, v122, v123
	v_cvt_pk_f16_f32 v123, v140, v141
	ds_write_b128 v235, v[120:123]
	v_cvt_f32_f16_e32 v120, v144
	v_cvt_f32_f16_e32 v121, v145
	v_cvt_f32_f16_e32 v122, v124
	v_cvt_f32_f16_e32 v123, v125
	v_cvt_f32_f16_e32 v125, v126
	v_cvt_f32_f16_e32 v127, v127
	v_cvt_f32_f16_e32 v140, v146
	v_cvt_f32_f16_e32 v141, v147
	v_add_f32_e32 v120, v120, v121
	v_add_f32_e32 v122, v122, v123
	v_add_f32_e32 v120, v120, v122
	v_add_f32_e32 v122, v125, v127
	v_add_f32_e32 v125, v140, v141
	v_add_f32_e32 v122, v122, v125
	v_add_f32_e32 v120, v120, v122
	v_add_f32_e32 v125, 0, v120
	v_mul_f32_e32 v120, v121, v121
	v_mul_f32_e32 v121, v123, v123
	v_fma_mix_f32 v120, v144, v144, v120 op_sel_hi:[1,1,0]
	v_fma_mix_f32 v121, v124, v124, v121 op_sel_hi:[1,1,0]
	v_mul_f32_e32 v122, v141, v141
	v_add_f32_e32 v120, v120, v121
	v_mul_f32_e32 v121, v127, v127
	v_fma_mix_f32 v121, v126, v126, v121 op_sel_hi:[1,1,0]
	v_fma_mix_f32 v122, v146, v146, v122 op_sel_hi:[1,1,0]
	v_cvt_f32_f16_sdwa v123, v160 dst_sel:DWORD dst_unused:UNUSED_PAD src0_sel:WORD_1
	v_add_f32_e32 v121, v121, v122
	v_add_f32_e32 v124, v120, v121
	v_cvt_f32_f16_e32 v122, v160
	v_cvt_f32_f16_sdwa v121, v161 dst_sel:DWORD dst_unused:UNUSED_PAD src0_sel:WORD_1
	v_cvt_f32_f16_e32 v120, v161
	v_cvt_f32_f16_sdwa v126, v162 dst_sel:DWORD dst_unused:UNUSED_PAD src0_sel:WORD_1
	v_cvt_f32_f16_e32 v127, v162
	v_cvt_f32_f16_sdwa v140, v163 dst_sel:DWORD dst_unused:UNUSED_PAD src0_sel:WORD_1
	v_cvt_f32_f16_e32 v141, v163
	v_sub_f32_e32 v120, v120, v222
	v_sub_f32_e32 v121, v121, v222
	v_sub_f32_e32 v122, v122, v222
	v_sub_f32_e32 v123, v123, v222
	v_pk_mul_f32 v[122:123], v[222:223], v[122:123] op_sel:[1,0]
	v_pk_mul_f32 v[120:121], v[222:223], v[120:121] op_sel:[1,0]
	v_pk_fma_f32 v[116:117], v[122:123], v[80:81], v[116:117]
	v_pk_fma_f32 v[118:119], v[120:121], v[82:83], v[118:119]
	v_sub_f32_e32 v120, v141, v222
	v_sub_f32_e32 v121, v140, v222
	v_sub_f32_e32 v122, v127, v222
	v_sub_f32_e32 v123, v126, v222
	v_pk_add_f32 v[114:115], v[114:115], v[192:193]
	v_pk_add_f32 v[112:113], v[112:113], v[194:195]
	v_pk_mul_f32 v[122:123], v[222:223], v[122:123] op_sel:[1,0]
	v_pk_mul_f32 v[120:121], v[222:223], v[120:121] op_sel:[1,0]
	s_ashr_i32 s39, s38, 31
	v_pk_fma_f32 v[120:121], v[120:121], v[74:75], v[114:115]
	v_pk_fma_f32 v[114:115], v[122:123], v[72:73], v[112:113]
	v_cvt_f16_f32_e32 v122, v116
	v_cvt_f16_f32_e32 v123, v117
	v_cvt_pk_f16_f32 v112, v116, v117
	v_cvt_f16_f32_e32 v116, v118
	v_cvt_f16_f32_e32 v117, v119
	v_cvt_pk_f16_f32 v113, v118, v119
	v_cvt_f16_f32_e32 v118, v114
	v_cvt_f16_f32_e32 v119, v115
	v_cvt_f16_f32_e32 v126, v120
	v_cvt_f16_f32_e32 v127, v121
	v_cvt_pk_f16_f32 v114, v114, v115
	v_cvt_pk_f16_f32 v115, v120, v121
	ds_write_b128 v235, v[112:115] offset:64
	v_cvt_f32_f16_e32 v112, v122
	v_cvt_f32_f16_e32 v113, v123
	v_cvt_f32_f16_e32 v114, v116
	v_cvt_f32_f16_e32 v115, v117
	v_cvt_f32_f16_e32 v117, v118
	v_cvt_f32_f16_e32 v119, v119
	v_cvt_f32_f16_e32 v120, v126
	v_cvt_f32_f16_e32 v121, v127
	v_add_f32_e32 v112, v112, v113
	v_add_f32_e32 v114, v114, v115
	v_add_f32_e32 v112, v112, v114
	v_add_f32_e32 v114, v117, v119
	v_add_f32_e32 v117, v120, v121
	v_add_f32_e32 v114, v114, v117
	v_add_f32_e32 v112, v112, v114
	v_mul_f32_e32 v113, v113, v113
	v_mul_f32_e32 v114, v115, v115
	v_fma_mix_f32 v113, v122, v122, v113 op_sel_hi:[1,1,0]
	v_fma_mix_f32 v114, v116, v116, v114 op_sel_hi:[1,1,0]
	v_mul_f32_e32 v115, v121, v121
	v_add_f32_e32 v113, v113, v114
	v_mul_f32_e32 v114, v119, v119
	v_fma_mix_f32 v114, v118, v118, v114 op_sel_hi:[1,1,0]
	v_fma_mix_f32 v115, v126, v126, v115 op_sel_hi:[1,1,0]
	v_add_f32_e32 v112, v125, v112
	v_add_f32_e32 v114, v114, v115
	v_add_f32_e32 v113, v113, v114
	ds_bpermute_b32 v114, v221, v112
	v_add_f32_e32 v113, v124, v113
	ds_read_b128 v[160:163], v236
	ds_read_b128 v[164:167], v236 offset:1152
	s_waitcnt lgkmcnt(2)
	v_add_f32_e32 v112, v112, v114
	ds_bpermute_b32 v114, v221, v113
	s_waitcnt lgkmcnt(0)
	v_add_f32_e32 v113, v113, v114
	ds_bpermute_b32 v114, v237, v112
	s_waitcnt lgkmcnt(0)
	v_add_f32_e32 v146, v112, v114
	ds_bpermute_b32 v112, v237, v113
	s_waitcnt lgkmcnt(0)
	v_add_f32_e32 v147, v113, v112
	v_mov_b64_e32 v[112:113], s[28:29]
	v_mad_i64_i32 v[112:113], s[40:41], v220, s73, v[112:113]
	v_lshl_add_u64 v[140:141], s[38:39], 3, v[112:113]
	v_add_co_u32_e32 v112, vcc, s74, v214
	v_lshl_or_b32 v144, v238, 1, v230
	s_nop 0
	v_addc_co_u32_e32 v113, vcc, 0, v215, vcc
	global_load_dwordx4 v[124:127], v[112:113], off nt
	global_load_dwordx4 v[120:123], v[112:113], off offset:64 nt
	v_add_co_u32_e32 v112, vcc, s75, v214
	v_lshl_add_u64 v[140:141], v[140:141], 0, s[34:35]
	s_nop 0
	v_addc_co_u32_e32 v113, vcc, 0, v215, vcc
	global_load_dwordx4 v[116:119], v[112:113], off nt
	s_nop 0
	global_load_dwordx4 v[112:115], v[112:113], off offset:64 nt
	s_nop 0
	buffer_store_dwordx4 v[132:135], v144, s[24:27], 0 offen nt
	s_nop 1
	v_add_u32_e32 v132, 0x3000, v144
	buffer_store_dwordx4 v[128:131], v132, s[24:27], 0 offen nt
	global_store_dwordx2 v[140:141], v[142:143], off
	s_nop 0
	v_add_u32_e32 v128, 0x6000, v144
	buffer_store_dwordx4 v[160:163], v128, s[24:27], 0 offen nt
	v_add_u32_e32 v128, 0x9000, v144
	buffer_store_dwordx4 v[164:167], v128, s[24:27], 0 offen nt
	global_store_dwordx2 v[140:141], v[146:147], off offset:1536
	v_cvt_f32_f16_sdwa v131, v156 dst_sel:DWORD dst_unused:UNUSED_PAD src0_sel:WORD_1
	v_cvt_f32_f16_e32 v130, v156
	v_cvt_f32_f16_sdwa v129, v157 dst_sel:DWORD dst_unused:UNUSED_PAD src0_sel:WORD_1
	v_cvt_f32_f16_e32 v128, v157
	v_cvt_f32_f16_sdwa v132, v158 dst_sel:DWORD dst_unused:UNUSED_PAD src0_sel:WORD_1
	v_cvt_f32_f16_e32 v133, v158
	v_cvt_f32_f16_sdwa v134, v159 dst_sel:DWORD dst_unused:UNUSED_PAD src0_sel:WORD_1
	v_cvt_f32_f16_e32 v135, v159
	v_sub_f32_e32 v128, v128, v218
	v_sub_f32_e32 v129, v129, v218
	v_sub_f32_e32 v130, v130, v218
	v_sub_f32_e32 v131, v131, v218
	v_pk_add_f32 v[110:111], v[110:111], v[206:207]
	v_pk_add_f32 v[108:109], v[108:109], v[208:209]
	v_pk_mul_f32 v[130:131], v[218:219], v[130:131] op_sel:[1,0]
	v_pk_mul_f32 v[128:129], v[218:219], v[128:129] op_sel:[1,0]
	v_pk_fma_f32 v[108:109], v[130:131], v[92:93], v[108:109]
	v_pk_fma_f32 v[110:111], v[128:129], v[94:95], v[110:111]
	v_sub_f32_e32 v128, v135, v218
	v_sub_f32_e32 v129, v134, v218
	v_sub_f32_e32 v130, v133, v218
	v_sub_f32_e32 v131, v132, v218
	v_pk_add_f32 v[106:107], v[106:107], v[202:203]
	v_pk_add_f32 v[104:105], v[104:105], v[204:205]
	v_pk_mul_f32 v[130:131], v[218:219], v[130:131] op_sel:[1,0]
	v_pk_mul_f32 v[128:129], v[218:219], v[128:129] op_sel:[1,0]
	v_pk_add_f32 v[102:103], v[102:103], v[198:199]
	v_pk_fma_f32 v[128:129], v[128:129], v[90:91], v[106:107]
	v_pk_fma_f32 v[106:107], v[130:131], v[88:89], v[104:105]
	v_cvt_f16_f32_e32 v130, v108
	v_cvt_f16_f32_e32 v131, v109
	v_cvt_pk_f16_f32 v104, v108, v109
	v_cvt_f16_f32_e32 v108, v110
	v_cvt_f16_f32_e32 v109, v111
	v_cvt_pk_f16_f32 v105, v110, v111
	v_cvt_f16_f32_e32 v110, v106
	v_cvt_f16_f32_e32 v111, v107
	v_cvt_f16_f32_e32 v132, v128
	v_cvt_f16_f32_e32 v133, v129
	v_cvt_pk_f16_f32 v106, v106, v107
	v_cvt_pk_f16_f32 v107, v128, v129
	ds_write_b128 v235, v[104:107]
	v_cvt_f32_f16_e32 v104, v130
	v_cvt_f32_f16_e32 v105, v131
	v_cvt_f32_f16_e32 v106, v108
	v_cvt_f32_f16_e32 v107, v109
	v_cvt_f32_f16_e32 v109, v110
	v_cvt_f32_f16_e32 v111, v111
	v_cvt_f32_f16_e32 v128, v132
	v_cvt_f32_f16_e32 v129, v133
	v_add_f32_e32 v104, v104, v105
	v_add_f32_e32 v106, v106, v107
	v_add_f32_e32 v104, v104, v106
	v_add_f32_e32 v106, v109, v111
	v_add_f32_e32 v109, v128, v129
	v_add_f32_e32 v106, v106, v109
	v_add_f32_e32 v104, v104, v106
	v_add_f32_e32 v109, 0, v104
	v_mul_f32_e32 v104, v105, v105
	v_mul_f32_e32 v105, v107, v107
	v_fma_mix_f32 v104, v130, v130, v104 op_sel_hi:[1,1,0]
	v_fma_mix_f32 v105, v108, v108, v105 op_sel_hi:[1,1,0]
	v_mul_f32_e32 v106, v129, v129
	v_add_f32_e32 v104, v104, v105
	v_mul_f32_e32 v105, v111, v111
	v_fma_mix_f32 v105, v110, v110, v105 op_sel_hi:[1,1,0]
	v_fma_mix_f32 v106, v132, v132, v106 op_sel_hi:[1,1,0]
	v_cvt_f32_f16_sdwa v107, v152 dst_sel:DWORD dst_unused:UNUSED_PAD src0_sel:WORD_1
	v_add_f32_e32 v105, v105, v106
	v_add_f32_e32 v108, v104, v105
	v_cvt_f32_f16_e32 v106, v152
	v_cvt_f32_f16_sdwa v105, v153 dst_sel:DWORD dst_unused:UNUSED_PAD src0_sel:WORD_1
	v_cvt_f32_f16_e32 v104, v153
	v_cvt_f32_f16_sdwa v110, v154 dst_sel:DWORD dst_unused:UNUSED_PAD src0_sel:WORD_1
	v_cvt_f32_f16_e32 v111, v154
	v_cvt_f32_f16_sdwa v128, v155 dst_sel:DWORD dst_unused:UNUSED_PAD src0_sel:WORD_1
	v_cvt_f32_f16_e32 v129, v155
	v_sub_f32_e32 v104, v104, v218
	v_sub_f32_e32 v105, v105, v218
	v_sub_f32_e32 v106, v106, v218
	v_sub_f32_e32 v107, v107, v218
	v_pk_add_f32 v[100:101], v[100:101], v[200:201]
	v_pk_mul_f32 v[106:107], v[218:219], v[106:107] op_sel:[1,0]
	v_pk_mul_f32 v[104:105], v[218:219], v[104:105] op_sel:[1,0]
	v_pk_fma_f32 v[100:101], v[106:107], v[80:81], v[100:101]
	v_pk_fma_f32 v[102:103], v[104:105], v[82:83], v[102:103]
	v_sub_f32_e32 v104, v129, v218
	v_sub_f32_e32 v105, v128, v218
	v_sub_f32_e32 v106, v111, v218
	v_sub_f32_e32 v107, v110, v218
	v_pk_add_f32 v[98:99], v[98:99], v[192:193]
	v_pk_add_f32 v[96:97], v[96:97], v[194:195]
	v_pk_mul_f32 v[106:107], v[218:219], v[106:107] op_sel:[1,0]
	v_pk_mul_f32 v[104:105], v[218:219], v[104:105] op_sel:[1,0]
	v_pk_add_f32 v[86:87], v[86:87], v[206:207]
	v_pk_fma_f32 v[104:105], v[104:105], v[74:75], v[98:99]
	v_pk_fma_f32 v[98:99], v[106:107], v[72:73], v[96:97]
	v_cvt_f16_f32_e32 v106, v100
	v_cvt_f16_f32_e32 v107, v101
	v_cvt_pk_f16_f32 v96, v100, v101
	v_cvt_f16_f32_e32 v100, v102
	v_cvt_f16_f32_e32 v101, v103
	v_cvt_pk_f16_f32 v97, v102, v103
	v_cvt_f16_f32_e32 v103, v99
	v_cvt_f16_f32_e32 v111, v105
	v_cvt_f16_f32_e32 v102, v98
	v_cvt_f16_f32_e32 v110, v104
	v_cvt_pk_f16_f32 v98, v98, v99
	v_cvt_pk_f16_f32 v99, v104, v105
	v_cvt_f32_f16_e32 v105, v107
	v_cvt_f32_f16_e32 v107, v100
	v_cvt_f32_f16_e32 v101, v101
	v_cvt_f32_f16_e32 v103, v103
	v_cvt_f32_f16_e32 v104, v106
	v_cvt_f32_f16_e32 v111, v111
	v_cvt_f32_f16_e32 v128, v102
	v_cvt_f32_f16_e32 v129, v110
	v_add_f32_e32 v107, v107, v101
	v_mul_f32_e32 v101, v101, v101
	v_fma_mix_f32 v100, v100, v100, v101 op_sel_hi:[1,1,0]
	v_mul_f32_e32 v101, v103, v103
	v_add_f32_e32 v104, v104, v105
	v_mul_f32_e32 v105, v105, v105
	v_fma_mix_f32 v101, v102, v102, v101 op_sel_hi:[1,1,0]
	v_mul_f32_e32 v102, v111, v111
	v_add_f32_e32 v104, v104, v107
	v_add_f32_e32 v107, v128, v103
	v_add_f32_e32 v128, v129, v111
	v_fma_mix_f32 v105, v106, v106, v105 op_sel_hi:[1,1,0]
	v_fma_mix_f32 v102, v110, v110, v102 op_sel_hi:[1,1,0]
	v_add_f32_e32 v107, v107, v128
	v_add_f32_e32 v100, v105, v100
	v_add_f32_e32 v101, v101, v102
	v_add_f32_e32 v104, v104, v107
	v_add_f32_e32 v100, v100, v101
	v_add_f32_e32 v104, v109, v104
	v_add_f32_e32 v105, v108, v100
	ds_bpermute_b32 v106, v221, v104
	ds_bpermute_b32 v107, v221, v105
	v_cvt_f32_f16_sdwa v108, v150 dst_sel:DWORD dst_unused:UNUSED_PAD src0_sel:WORD_1
	v_cvt_f32_f16_e32 v109, v150
	v_cvt_f32_f16_sdwa v110, v151 dst_sel:DWORD dst_unused:UNUSED_PAD src0_sel:WORD_1
	s_waitcnt lgkmcnt(1)
	v_add_f32_e32 v128, v104, v106
	s_waitcnt lgkmcnt(0)
	v_add_f32_e32 v129, v105, v107
	v_cvt_f32_f16_sdwa v107, v148 dst_sel:DWORD dst_unused:UNUSED_PAD src0_sel:WORD_1
	v_cvt_f32_f16_e32 v106, v148
	v_cvt_f32_f16_sdwa v105, v149 dst_sel:DWORD dst_unused:UNUSED_PAD src0_sel:WORD_1
	v_cvt_f32_f16_e32 v104, v149
	v_cvt_f32_f16_e32 v111, v151
	v_sub_f32_e32 v106, v106, v216
	v_sub_f32_e32 v105, v105, v216
	v_sub_f32_e32 v104, v104, v216
	v_sub_f32_e32 v107, v107, v216
	v_pk_add_f32 v[84:85], v[84:85], v[208:209]
	v_pk_mul_f32 v[106:107], v[216:217], v[106:107] op_sel:[1,0]
	v_pk_mul_f32 v[104:105], v[216:217], v[104:105] op_sel:[1,0]
	v_pk_fma_f32 v[84:85], v[106:107], v[92:93], v[84:85]
	v_pk_fma_f32 v[86:87], v[104:105], v[94:95], v[86:87]
	v_sub_f32_e32 v104, v111, v216
	v_sub_f32_e32 v105, v110, v216
	v_sub_f32_e32 v106, v109, v216
	v_sub_f32_e32 v107, v108, v216
	v_pk_add_f32 v[78:79], v[78:79], v[202:203]
	v_pk_add_f32 v[76:77], v[76:77], v[204:205]
	v_pk_mul_f32 v[106:107], v[216:217], v[106:107] op_sel:[1,0]
	v_pk_mul_f32 v[104:105], v[216:217], v[104:105] op_sel:[1,0]
	ds_write_b128 v235, v[96:99] offset:64
	v_pk_fma_f32 v[104:105], v[104:105], v[90:91], v[78:79]
	v_pk_fma_f32 v[78:79], v[106:107], v[88:89], v[76:77]
	v_cvt_f16_f32_e32 v106, v84
	v_cvt_f16_f32_e32 v107, v85
	v_cvt_pk_f16_f32 v76, v84, v85
	v_cvt_f16_f32_e32 v84, v86
	v_cvt_f16_f32_e32 v85, v87
	v_cvt_pk_f16_f32 v77, v86, v87
	v_cvt_f16_f32_e32 v86, v78
	v_cvt_f16_f32_e32 v87, v79
	v_cvt_f16_f32_e32 v108, v104
	v_cvt_f16_f32_e32 v109, v105
	v_cvt_pk_f16_f32 v78, v78, v79
	v_cvt_pk_f16_f32 v79, v104, v105
	ds_read_b128 v[96:99], v236
	ds_read_b128 v[100:103], v236 offset:1152
	ds_write_b128 v235, v[76:79]
	v_cvt_f32_f16_e32 v76, v106
	v_cvt_f32_f16_e32 v77, v107
	v_cvt_f32_f16_e32 v78, v84
	v_cvt_f32_f16_e32 v79, v85
	v_cvt_f32_f16_e32 v85, v86
	v_cvt_f32_f16_e32 v87, v87
	v_cvt_f32_f16_e32 v104, v108
	v_cvt_f32_f16_e32 v105, v109
	v_add_f32_e32 v76, v76, v77
	v_add_f32_e32 v78, v78, v79
	v_add_f32_e32 v76, v76, v78
	v_add_f32_e32 v78, v85, v87
	v_add_f32_e32 v85, v104, v105
	v_add_f32_e32 v78, v78, v85
	v_add_f32_e32 v76, v76, v78
	v_add_f32_e32 v85, 0, v76
	v_mul_f32_e32 v76, v77, v77
	v_mul_f32_e32 v77, v79, v79
	v_fma_mix_f32 v76, v106, v106, v76 op_sel_hi:[1,1,0]
	v_fma_mix_f32 v77, v84, v84, v77 op_sel_hi:[1,1,0]
	v_mul_f32_e32 v78, v105, v105
	v_add_f32_e32 v76, v76, v77
	v_mul_f32_e32 v77, v87, v87
	v_fma_mix_f32 v77, v86, v86, v77 op_sel_hi:[1,1,0]
	v_fma_mix_f32 v78, v108, v108, v78 op_sel_hi:[1,1,0]
	v_cvt_f32_f16_sdwa v79, v136 dst_sel:DWORD dst_unused:UNUSED_PAD src0_sel:WORD_1
	v_add_f32_e32 v77, v77, v78
	v_add_f32_e32 v84, v76, v77
	v_cvt_f32_f16_e32 v78, v136
	v_cvt_f32_f16_sdwa v77, v137 dst_sel:DWORD dst_unused:UNUSED_PAD src0_sel:WORD_1
	v_cvt_f32_f16_e32 v76, v137
	v_cvt_f32_f16_sdwa v86, v138 dst_sel:DWORD dst_unused:UNUSED_PAD src0_sel:WORD_1
	v_cvt_f32_f16_e32 v87, v138
	v_cvt_f32_f16_sdwa v104, v139 dst_sel:DWORD dst_unused:UNUSED_PAD src0_sel:WORD_1
	v_cvt_f32_f16_e32 v105, v139
	v_sub_f32_e32 v76, v76, v216
	v_sub_f32_e32 v77, v77, v216
	v_sub_f32_e32 v78, v78, v216
	v_sub_f32_e32 v79, v79, v216
	v_pk_add_f32 v[70:71], v[70:71], v[198:199]
	v_pk_add_f32 v[68:69], v[68:69], v[200:201]
	v_pk_mul_f32 v[78:79], v[216:217], v[78:79] op_sel:[1,0]
	v_pk_mul_f32 v[76:77], v[216:217], v[76:77] op_sel:[1,0]
	v_pk_fma_f32 v[68:69], v[78:79], v[80:81], v[68:69]
	v_pk_fma_f32 v[70:71], v[76:77], v[82:83], v[70:71]
	v_sub_f32_e32 v76, v105, v216
	v_sub_f32_e32 v77, v104, v216
	v_sub_f32_e32 v78, v87, v216
	v_sub_f32_e32 v79, v86, v216
	v_pk_add_f32 v[66:67], v[66:67], v[192:193]
	v_pk_add_f32 v[64:65], v[64:65], v[194:195]
	v_pk_mul_f32 v[78:79], v[216:217], v[78:79] op_sel:[1,0]
	v_pk_mul_f32 v[76:77], v[216:217], v[76:77] op_sel:[1,0]
	ds_bpermute_b32 v130, v237, v128
	v_pk_fma_f32 v[76:77], v[76:77], v[74:75], v[66:67]
	v_pk_fma_f32 v[66:67], v[78:79], v[72:73], v[64:65]
	v_cvt_f16_f32_e32 v78, v68
	v_cvt_f16_f32_e32 v79, v69
	v_cvt_pk_f16_f32 v64, v68, v69
	v_cvt_f16_f32_e32 v68, v70
	v_cvt_f16_f32_e32 v69, v71
	v_cvt_pk_f16_f32 v65, v70, v71
	v_cvt_f16_f32_e32 v71, v67
	v_cvt_f16_f32_e32 v87, v77
	v_cvt_f16_f32_e32 v70, v66
	v_cvt_f16_f32_e32 v86, v76
	v_cvt_f32_f16_e32 v105, v68
	v_cvt_f32_f16_e32 v69, v69
	v_cvt_f32_f16_e32 v71, v71
	v_cvt_f32_f16_e32 v104, v78
	v_cvt_f32_f16_e32 v79, v79
	v_cvt_f32_f16_e32 v87, v87
	v_cvt_f32_f16_e32 v106, v70
	v_cvt_f32_f16_e32 v107, v86
	v_add_f32_e32 v105, v105, v69
	v_mul_f32_e32 v69, v69, v69
	v_fma_mix_f32 v68, v68, v68, v69 op_sel_hi:[1,1,0]
	v_mul_f32_e32 v69, v71, v71
	v_add_f32_e32 v104, v104, v79
	v_mul_f32_e32 v79, v79, v79
	v_fma_mix_f32 v69, v70, v70, v69 op_sel_hi:[1,1,0]
	v_mul_f32_e32 v70, v87, v87
	v_add_f32_e32 v104, v104, v105
	v_add_f32_e32 v105, v106, v71
	v_add_f32_e32 v106, v107, v87
	v_fma_mix_f32 v78, v78, v78, v79 op_sel_hi:[1,1,0]
	v_fma_mix_f32 v70, v86, v86, v70 op_sel_hi:[1,1,0]
	v_add_f32_e32 v105, v105, v106
	v_add_f32_e32 v68, v78, v68
	v_add_f32_e32 v69, v69, v70
	v_add_f32_e32 v104, v104, v105
	v_add_f32_e32 v68, v68, v69
	v_add_f32_e32 v85, v85, v104
	v_add_f32_e32 v68, v84, v68
	ds_bpermute_b32 v69, v221, v85
	ds_bpermute_b32 v70, v221, v68
	v_cvt_pk_f16_f32 v66, v66, v67
	v_cvt_pk_f16_f32 v67, v76, v77
	ds_write_b128 v235, v[64:67] offset:64
	s_waitcnt lgkmcnt(2)
	v_add_f32_e32 v64, v85, v69
	s_waitcnt lgkmcnt(1)
	v_add_f32_e32 v65, v68, v70
	ds_bpermute_b32 v131, v237, v129
	ds_bpermute_b32 v66, v237, v64
	ds_bpermute_b32 v67, v237, v65
	ds_read_b128 v[104:107], v236
	ds_read_b128 v[108:111], v236 offset:1152
	v_add_f32_e32 v128, v128, v130
	s_waitcnt lgkmcnt(4)
	v_add_f32_e32 v129, v129, v131
	s_waitcnt lgkmcnt(3)
	v_add_f32_e32 v130, v64, v66
	s_waitcnt lgkmcnt(2)
	v_add_f32_e32 v131, v65, v67
	v_add_co_u32_e32 v64, vcc, s77, v214
	s_nop 1
	v_addc_co_u32_e32 v65, vcc, 0, v215, vcc
	global_load_dwordx4 v[84:87], v[64:65], off nt
	global_load_dwordx4 v[76:79], v[64:65], off offset:64 nt
	v_add_co_u32_e32 v64, vcc, s78, v214
	s_nop 1
	v_addc_co_u32_e32 v65, vcc, 0, v215, vcc
	global_load_dwordx4 v[68:71], v[64:65], off nt
	s_nop 0
	global_load_dwordx4 v[64:67], v[64:65], off offset:64 nt
	v_add_u32_e32 v132, 0xc000, v144
	buffer_store_dwordx4 v[96:99], v132, s[24:27], 0 offen nt
	s_nop 1
	v_add_u32_e32 v96, 0xf000, v144
	buffer_store_dwordx4 v[100:103], v96, s[24:27], 0 offen nt
	v_add_u32_e32 v96, 0x12000, v144
	global_store_dwordx2 v[140:141], v[128:129], off offset:3072
	s_waitcnt lgkmcnt(1)
	buffer_store_dwordx4 v[104:107], v96, s[24:27], 0 offen nt
	v_add_u32_e32 v96, 0x15000, v144
	s_waitcnt lgkmcnt(0)
	buffer_store_dwordx4 v[108:111], v96, s[24:27], 0 offen nt
	v_add_co_u32_e32 v96, vcc, s79, v140
	s_nop 1
	v_addc_co_u32_e32 v97, vcc, 0, v141, vcc
	global_store_dwordx2 v[96:97], v[130:131], off offset:512
	s_waitcnt vmcnt(19)
	v_cvt_f32_f16_sdwa v99, v124 dst_sel:DWORD dst_unused:UNUSED_PAD src0_sel:WORD_1
	v_cvt_f32_f16_e32 v98, v124
	v_cvt_f32_f16_sdwa v97, v125 dst_sel:DWORD dst_unused:UNUSED_PAD src0_sel:WORD_1
	v_cvt_f32_f16_e32 v96, v125
	v_cvt_f32_f16_sdwa v100, v126 dst_sel:DWORD dst_unused:UNUSED_PAD src0_sel:WORD_1
	v_cvt_f32_f16_e32 v101, v126
	v_cvt_f32_f16_sdwa v102, v127 dst_sel:DWORD dst_unused:UNUSED_PAD src0_sel:WORD_1
	v_cvt_f32_f16_e32 v103, v127
	v_sub_f32_e32 v96, v96, v212
	v_sub_f32_e32 v97, v97, v212
	v_sub_f32_e32 v98, v98, v212
	v_sub_f32_e32 v99, v99, v212
	v_pk_add_f32 v[62:63], v[62:63], v[206:207]
	v_pk_add_f32 v[60:61], v[60:61], v[208:209]
	v_pk_mul_f32 v[98:99], v[212:213], v[98:99] op_sel:[1,0]
	v_pk_mul_f32 v[96:97], v[212:213], v[96:97] op_sel:[1,0]
	v_pk_fma_f32 v[60:61], v[92:93], v[98:99], v[60:61]
	v_pk_fma_f32 v[62:63], v[94:95], v[96:97], v[62:63]
	v_sub_f32_e32 v96, v103, v212
	v_sub_f32_e32 v97, v102, v212
	v_sub_f32_e32 v98, v101, v212
	v_sub_f32_e32 v99, v100, v212
	v_pk_add_f32 v[58:59], v[58:59], v[202:203]
	v_pk_add_f32 v[56:57], v[56:57], v[204:205]
	v_pk_mul_f32 v[98:99], v[212:213], v[98:99] op_sel:[1,0]
	v_pk_mul_f32 v[96:97], v[212:213], v[96:97] op_sel:[1,0]
	v_pk_add_f32 v[54:55], v[54:55], v[198:199]
	v_pk_fma_f32 v[96:97], v[90:91], v[96:97], v[58:59]
	v_pk_fma_f32 v[58:59], v[88:89], v[98:99], v[56:57]
	v_cvt_f16_f32_e32 v98, v60
	v_cvt_f16_f32_e32 v99, v61
	v_cvt_pk_f16_f32 v56, v60, v61
	v_cvt_f16_f32_e32 v60, v62
	v_cvt_f16_f32_e32 v61, v63
	v_cvt_pk_f16_f32 v57, v62, v63
	v_cvt_f16_f32_e32 v62, v58
	v_cvt_f16_f32_e32 v63, v59
	v_cvt_f16_f32_e32 v100, v96
	v_cvt_f16_f32_e32 v101, v97
	v_cvt_pk_f16_f32 v58, v58, v59
	v_cvt_pk_f16_f32 v59, v96, v97
	ds_write_b128 v235, v[56:59]
	v_cvt_f32_f16_e32 v56, v98
	v_cvt_f32_f16_e32 v57, v99
	v_cvt_f32_f16_e32 v58, v60
	v_cvt_f32_f16_e32 v59, v61
	v_cvt_f32_f16_e32 v61, v62
	v_cvt_f32_f16_e32 v63, v63
	v_cvt_f32_f16_e32 v96, v100
	v_cvt_f32_f16_e32 v97, v101
	v_add_f32_e32 v56, v56, v57
	v_add_f32_e32 v58, v58, v59
	v_add_f32_e32 v56, v56, v58
	v_add_f32_e32 v58, v61, v63
	v_add_f32_e32 v61, v96, v97
	v_add_f32_e32 v58, v58, v61
	v_add_f32_e32 v56, v56, v58
	v_add_f32_e32 v61, 0, v56
	v_mul_f32_e32 v56, v57, v57
	v_mul_f32_e32 v57, v59, v59
	v_fma_mix_f32 v56, v98, v98, v56 op_sel_hi:[1,1,0]
	v_fma_mix_f32 v57, v60, v60, v57 op_sel_hi:[1,1,0]
	v_mul_f32_e32 v58, v97, v97
	v_add_f32_e32 v56, v56, v57
	v_mul_f32_e32 v57, v63, v63
	v_fma_mix_f32 v57, v62, v62, v57 op_sel_hi:[1,1,0]
	v_fma_mix_f32 v58, v100, v100, v58 op_sel_hi:[1,1,0]
	s_waitcnt vmcnt(18)
	v_cvt_f32_f16_sdwa v59, v120 dst_sel:DWORD dst_unused:UNUSED_PAD src0_sel:WORD_1
	v_add_f32_e32 v57, v57, v58
	v_add_f32_e32 v60, v56, v57
	v_cvt_f32_f16_e32 v58, v120
	v_cvt_f32_f16_sdwa v57, v121 dst_sel:DWORD dst_unused:UNUSED_PAD src0_sel:WORD_1
	v_cvt_f32_f16_e32 v56, v121
	v_cvt_f32_f16_sdwa v62, v122 dst_sel:DWORD dst_unused:UNUSED_PAD src0_sel:WORD_1
	v_cvt_f32_f16_e32 v63, v122
	v_cvt_f32_f16_sdwa v96, v123 dst_sel:DWORD dst_unused:UNUSED_PAD src0_sel:WORD_1
	v_cvt_f32_f16_e32 v97, v123
	v_sub_f32_e32 v56, v56, v212
	v_sub_f32_e32 v57, v57, v212
	v_sub_f32_e32 v58, v58, v212
	v_sub_f32_e32 v59, v59, v212
	v_pk_add_f32 v[52:53], v[52:53], v[200:201]
	v_pk_mul_f32 v[58:59], v[212:213], v[58:59] op_sel:[1,0]
	v_pk_mul_f32 v[56:57], v[212:213], v[56:57] op_sel:[1,0]
	v_pk_fma_f32 v[52:53], v[80:81], v[58:59], v[52:53]
	v_pk_fma_f32 v[54:55], v[82:83], v[56:57], v[54:55]
	v_sub_f32_e32 v56, v97, v212
	v_sub_f32_e32 v57, v96, v212
	v_sub_f32_e32 v58, v63, v212
	v_sub_f32_e32 v59, v62, v212
	v_pk_add_f32 v[50:51], v[50:51], v[192:193]
	v_pk_add_f32 v[48:49], v[48:49], v[194:195]
	v_pk_mul_f32 v[58:59], v[212:213], v[58:59] op_sel:[1,0]
	v_pk_mul_f32 v[56:57], v[212:213], v[56:57] op_sel:[1,0]
	s_waitcnt vmcnt(17)
	v_cvt_f32_f16_sdwa v98, v119 dst_sel:DWORD dst_unused:UNUSED_PAD src0_sel:WORD_1
	v_pk_fma_f32 v[56:57], v[74:75], v[56:57], v[50:51]
	v_pk_fma_f32 v[50:51], v[72:73], v[58:59], v[48:49]
	v_cvt_f16_f32_e32 v58, v52
	v_cvt_f16_f32_e32 v59, v53
	v_cvt_pk_f16_f32 v48, v52, v53
	v_cvt_f16_f32_e32 v52, v54
	v_cvt_f16_f32_e32 v53, v55
	v_cvt_pk_f16_f32 v49, v54, v55
	v_cvt_f16_f32_e32 v55, v51
	v_cvt_f16_f32_e32 v63, v57
	v_cvt_f16_f32_e32 v54, v50
	v_cvt_f16_f32_e32 v62, v56
	v_cvt_pk_f16_f32 v50, v50, v51
	v_cvt_pk_f16_f32 v51, v56, v57
	v_cvt_f32_f16_e32 v57, v59
	v_cvt_f32_f16_e32 v59, v52
	v_cvt_f32_f16_e32 v53, v53
	v_cvt_f32_f16_e32 v55, v55
	v_cvt_f32_f16_e32 v56, v58
	v_cvt_f32_f16_e32 v63, v63
	v_cvt_f32_f16_e32 v96, v54
	v_cvt_f32_f16_e32 v97, v62
	v_add_f32_e32 v59, v59, v53
	v_mul_f32_e32 v53, v53, v53
	v_fma_mix_f32 v52, v52, v52, v53 op_sel_hi:[1,1,0]
	v_mul_f32_e32 v53, v55, v55
	v_add_f32_e32 v56, v56, v57
	v_mul_f32_e32 v57, v57, v57
	v_fma_mix_f32 v53, v54, v54, v53 op_sel_hi:[1,1,0]
	v_mul_f32_e32 v54, v63, v63
	v_add_f32_e32 v56, v56, v59
	v_add_f32_e32 v59, v96, v55
	v_add_f32_e32 v96, v97, v63
	v_fma_mix_f32 v57, v58, v58, v57 op_sel_hi:[1,1,0]
	v_fma_mix_f32 v54, v62, v62, v54 op_sel_hi:[1,1,0]
	v_add_f32_e32 v59, v59, v96
	v_add_f32_e32 v52, v57, v52
	v_add_f32_e32 v53, v53, v54
	v_add_f32_e32 v56, v56, v59
	v_add_f32_e32 v52, v52, v53
	v_add_f32_e32 v56, v61, v56
	v_add_f32_e32 v57, v60, v52
	ds_bpermute_b32 v58, v221, v56
	ds_bpermute_b32 v59, v221, v57
	v_cvt_f32_f16_sdwa v96, v118 dst_sel:DWORD dst_unused:UNUSED_PAD src0_sel:WORD_1
	v_cvt_f32_f16_e32 v97, v118
	v_cvt_f32_f16_e32 v99, v119
	s_waitcnt lgkmcnt(1)
	v_add_f32_e32 v60, v56, v58
	s_waitcnt lgkmcnt(0)
	v_add_f32_e32 v61, v57, v59
	v_cvt_f32_f16_sdwa v59, v116 dst_sel:DWORD dst_unused:UNUSED_PAD src0_sel:WORD_1
	v_cvt_f32_f16_e32 v58, v116
	v_cvt_f32_f16_sdwa v57, v117 dst_sel:DWORD dst_unused:UNUSED_PAD src0_sel:WORD_1
	v_cvt_f32_f16_e32 v56, v117
	v_sub_f32_e32 v59, v59, v210
	v_sub_f32_e32 v58, v58, v210
	v_sub_f32_e32 v57, v57, v210
	v_sub_f32_e32 v56, v56, v210
	v_pk_add_f32 v[46:47], v[46:47], v[206:207]
	v_pk_add_f32 v[44:45], v[44:45], v[208:209]
	v_pk_mul_f32 v[58:59], v[210:211], v[58:59] op_sel:[1,0]
	v_pk_mul_f32 v[56:57], v[210:211], v[56:57] op_sel:[1,0]
	v_pk_fma_f32 v[44:45], v[92:93], v[58:59], v[44:45]
	v_pk_fma_f32 v[46:47], v[94:95], v[56:57], v[46:47]
	v_sub_f32_e32 v56, v99, v210
	v_sub_f32_e32 v57, v98, v210
	v_sub_f32_e32 v58, v97, v210
	v_sub_f32_e32 v59, v96, v210
	v_pk_add_f32 v[42:43], v[42:43], v[202:203]
	v_pk_add_f32 v[40:41], v[40:41], v[204:205]
	v_pk_mul_f32 v[58:59], v[210:211], v[58:59] op_sel:[1,0]
	v_pk_mul_f32 v[56:57], v[210:211], v[56:57] op_sel:[1,0]
	ds_write_b128 v235, v[48:51] offset:64
	v_pk_fma_f32 v[56:57], v[90:91], v[56:57], v[42:43]
	v_pk_fma_f32 v[42:43], v[88:89], v[58:59], v[40:41]
	v_cvt_f16_f32_e32 v58, v44
	v_cvt_f16_f32_e32 v59, v45
	v_cvt_pk_f16_f32 v40, v44, v45
	v_cvt_f16_f32_e32 v44, v46
	v_cvt_f16_f32_e32 v45, v47
	v_cvt_pk_f16_f32 v41, v46, v47
	v_cvt_f16_f32_e32 v46, v42
	v_cvt_f16_f32_e32 v47, v43
	v_cvt_f16_f32_e32 v96, v56
	v_cvt_f16_f32_e32 v97, v57
	v_cvt_pk_f16_f32 v42, v42, v43
	v_cvt_pk_f16_f32 v43, v56, v57
	ds_read_b128 v[48:51], v236
	ds_read_b128 v[52:55], v236 offset:1152
	ds_write_b128 v235, v[40:43]
	v_cvt_f32_f16_e32 v40, v58
	v_cvt_f32_f16_e32 v41, v59
	v_cvt_f32_f16_e32 v42, v44
	v_cvt_f32_f16_e32 v43, v45
	v_cvt_f32_f16_e32 v45, v46
	v_cvt_f32_f16_e32 v47, v47
	v_cvt_f32_f16_e32 v56, v96
	v_cvt_f32_f16_e32 v57, v97
	v_add_f32_e32 v40, v40, v41
	v_add_f32_e32 v42, v42, v43
	v_add_f32_e32 v40, v40, v42
	v_add_f32_e32 v42, v45, v47
	v_add_f32_e32 v45, v56, v57
	v_add_f32_e32 v42, v42, v45
	v_add_f32_e32 v40, v40, v42
	v_add_f32_e32 v45, 0, v40
	v_mul_f32_e32 v40, v41, v41
	v_mul_f32_e32 v41, v43, v43
	v_fma_mix_f32 v40, v58, v58, v40 op_sel_hi:[1,1,0]
	v_fma_mix_f32 v41, v44, v44, v41 op_sel_hi:[1,1,0]
	v_mul_f32_e32 v42, v57, v57
	v_add_f32_e32 v40, v40, v41
	v_mul_f32_e32 v41, v47, v47
	v_fma_mix_f32 v41, v46, v46, v41 op_sel_hi:[1,1,0]
	v_fma_mix_f32 v42, v96, v96, v42 op_sel_hi:[1,1,0]
	s_waitcnt vmcnt(16)
	v_cvt_f32_f16_sdwa v43, v112 dst_sel:DWORD dst_unused:UNUSED_PAD src0_sel:WORD_1
	v_add_f32_e32 v41, v41, v42
	v_add_f32_e32 v44, v40, v41
	v_cvt_f32_f16_e32 v42, v112
	v_cvt_f32_f16_sdwa v41, v113 dst_sel:DWORD dst_unused:UNUSED_PAD src0_sel:WORD_1
	v_cvt_f32_f16_e32 v40, v113
	v_cvt_f32_f16_sdwa v46, v114 dst_sel:DWORD dst_unused:UNUSED_PAD src0_sel:WORD_1
	v_cvt_f32_f16_e32 v47, v114
	v_cvt_f32_f16_sdwa v56, v115 dst_sel:DWORD dst_unused:UNUSED_PAD src0_sel:WORD_1
	v_cvt_f32_f16_e32 v57, v115
	v_sub_f32_e32 v40, v40, v210
	v_sub_f32_e32 v41, v41, v210
	v_sub_f32_e32 v42, v42, v210
	v_sub_f32_e32 v43, v43, v210
	v_pk_add_f32 v[38:39], v[38:39], v[198:199]
	v_pk_add_f32 v[36:37], v[36:37], v[200:201]
	v_pk_mul_f32 v[42:43], v[210:211], v[42:43] op_sel:[1,0]
	v_pk_mul_f32 v[40:41], v[210:211], v[40:41] op_sel:[1,0]
	v_pk_fma_f32 v[36:37], v[80:81], v[42:43], v[36:37]
	v_pk_fma_f32 v[38:39], v[82:83], v[40:41], v[38:39]
	v_sub_f32_e32 v40, v57, v210
	v_sub_f32_e32 v41, v56, v210
	v_sub_f32_e32 v42, v47, v210
	v_sub_f32_e32 v43, v46, v210
	v_pk_add_f32 v[34:35], v[34:35], v[192:193]
	v_pk_add_f32 v[32:33], v[32:33], v[194:195]
	v_pk_mul_f32 v[42:43], v[210:211], v[42:43] op_sel:[1,0]
	v_pk_mul_f32 v[40:41], v[210:211], v[40:41] op_sel:[1,0]
	ds_bpermute_b32 v62, v237, v60
	v_pk_fma_f32 v[40:41], v[74:75], v[40:41], v[34:35]
	v_pk_fma_f32 v[34:35], v[72:73], v[42:43], v[32:33]
	v_cvt_f16_f32_e32 v42, v36
	v_cvt_f16_f32_e32 v43, v37
	v_cvt_pk_f16_f32 v32, v36, v37
	v_cvt_f16_f32_e32 v36, v38
	v_cvt_f16_f32_e32 v37, v39
	v_cvt_pk_f16_f32 v33, v38, v39
	v_cvt_f16_f32_e32 v39, v35
	v_cvt_f16_f32_e32 v47, v41
	v_cvt_f16_f32_e32 v38, v34
	v_cvt_f16_f32_e32 v46, v40
	v_cvt_f32_f16_e32 v57, v36
	v_cvt_f32_f16_e32 v37, v37
	v_cvt_f32_f16_e32 v39, v39
	v_cvt_f32_f16_e32 v56, v42
	v_cvt_f32_f16_e32 v43, v43
	v_cvt_f32_f16_e32 v47, v47
	v_cvt_f32_f16_e32 v58, v38
	v_cvt_f32_f16_e32 v59, v46
	v_add_f32_e32 v57, v57, v37
	v_mul_f32_e32 v37, v37, v37
	v_fma_mix_f32 v36, v36, v36, v37 op_sel_hi:[1,1,0]
	v_mul_f32_e32 v37, v39, v39
	v_add_f32_e32 v56, v56, v43
	v_mul_f32_e32 v43, v43, v43
	v_fma_mix_f32 v37, v38, v38, v37 op_sel_hi:[1,1,0]
	v_mul_f32_e32 v38, v47, v47
	v_add_f32_e32 v56, v56, v57
	v_add_f32_e32 v57, v58, v39
	v_add_f32_e32 v58, v59, v47
	v_fma_mix_f32 v42, v42, v42, v43 op_sel_hi:[1,1,0]
	v_fma_mix_f32 v38, v46, v46, v38 op_sel_hi:[1,1,0]
	v_add_f32_e32 v57, v57, v58
	v_add_f32_e32 v36, v42, v36
	v_add_f32_e32 v37, v37, v38
	v_add_f32_e32 v56, v56, v57
	v_add_f32_e32 v36, v36, v37
	v_add_f32_e32 v45, v45, v56
	v_add_f32_e32 v36, v44, v36
	ds_bpermute_b32 v37, v221, v45
	ds_bpermute_b32 v38, v221, v36
	v_cvt_pk_f16_f32 v34, v34, v35
	v_cvt_pk_f16_f32 v35, v40, v41
	ds_write_b128 v235, v[32:35] offset:64
	s_waitcnt lgkmcnt(2)
	v_add_f32_e32 v32, v45, v37
	s_waitcnt lgkmcnt(1)
	v_add_f32_e32 v33, v36, v38
	ds_bpermute_b32 v63, v237, v61
	ds_bpermute_b32 v44, v237, v32
	ds_bpermute_b32 v45, v237, v33
	ds_read_b128 v[34:37], v236
	ds_read_b128 v[38:41], v236 offset:1152
	v_add_f32_e32 v42, v60, v62
	s_waitcnt lgkmcnt(4)
	v_add_f32_e32 v43, v61, v63
	s_waitcnt lgkmcnt(3)
	v_add_f32_e32 v44, v32, v44
	s_waitcnt lgkmcnt(2)
	v_add_f32_e32 v45, v33, v45
	v_add_u32_e32 v32, 0x30000, v144
	buffer_store_dwordx4 v[48:51], v32, s[24:27], 0 offen nt
	v_add_u32_e32 v32, 0x33000, v144
	buffer_store_dwordx4 v[52:55], v32, s[24:27], 0 offen nt
	v_add_co_u32_e32 v32, vcc, s76, v140
	s_nop 1
	v_addc_co_u32_e32 v33, vcc, 0, v141, vcc
	global_store_dwordx2 v[32:33], v[42:43], off
	v_add_u32_e32 v42, 0x36000, v144
	s_waitcnt lgkmcnt(1)
	buffer_store_dwordx4 v[34:37], v42, s[24:27], 0 offen nt
	s_nop 1
	v_add_u32_e32 v34, 0x39000, v144
	s_waitcnt lgkmcnt(0)
	buffer_store_dwordx4 v[38:41], v34, s[24:27], 0 offen nt
	global_store_dwordx2 v[32:33], v[44:45], off offset:1536
	s_waitcnt vmcnt(15)
	v_cvt_f32_f16_sdwa v37, v84 dst_sel:DWORD dst_unused:UNUSED_PAD src0_sel:WORD_1
	v_cvt_f32_f16_e32 v36, v84
	v_cvt_f32_f16_sdwa v35, v85 dst_sel:DWORD dst_unused:UNUSED_PAD src0_sel:WORD_1
	v_cvt_f32_f16_e32 v34, v85
	v_cvt_f32_f16_sdwa v38, v86 dst_sel:DWORD dst_unused:UNUSED_PAD src0_sel:WORD_1
	v_cvt_f32_f16_e32 v39, v86
	v_cvt_f32_f16_sdwa v40, v87 dst_sel:DWORD dst_unused:UNUSED_PAD src0_sel:WORD_1
	v_cvt_f32_f16_e32 v41, v87
	v_sub_f32_e32 v34, v34, v196
	v_sub_f32_e32 v35, v35, v196
	v_sub_f32_e32 v36, v36, v196
	v_sub_f32_e32 v37, v37, v196
	v_pk_add_f32 v[30:31], v[30:31], v[206:207]
	v_pk_add_f32 v[28:29], v[28:29], v[208:209]
	v_pk_mul_f32 v[36:37], v[196:197], v[36:37] op_sel:[1,0]
	v_pk_mul_f32 v[34:35], v[196:197], v[34:35] op_sel:[1,0]
	v_pk_fma_f32 v[28:29], v[92:93], v[36:37], v[28:29]
	v_pk_fma_f32 v[30:31], v[94:95], v[34:35], v[30:31]
	v_sub_f32_e32 v34, v41, v196
	v_sub_f32_e32 v35, v40, v196
	v_sub_f32_e32 v36, v39, v196
	v_sub_f32_e32 v37, v38, v196
	v_pk_add_f32 v[26:27], v[26:27], v[202:203]
	v_pk_add_f32 v[24:25], v[24:25], v[204:205]
	v_pk_mul_f32 v[36:37], v[196:197], v[36:37] op_sel:[1,0]
	v_pk_mul_f32 v[34:35], v[196:197], v[34:35] op_sel:[1,0]
	v_pk_add_f32 v[22:23], v[22:23], v[198:199]
	v_pk_fma_f32 v[34:35], v[90:91], v[34:35], v[26:27]
	v_pk_fma_f32 v[26:27], v[88:89], v[36:37], v[24:25]
	v_cvt_f16_f32_e32 v36, v28
	v_cvt_f16_f32_e32 v37, v29
	v_cvt_pk_f16_f32 v24, v28, v29
	v_cvt_f16_f32_e32 v28, v30
	v_cvt_f16_f32_e32 v29, v31
	v_cvt_pk_f16_f32 v25, v30, v31
	v_cvt_f16_f32_e32 v30, v26
	v_cvt_f16_f32_e32 v31, v27
	v_cvt_f16_f32_e32 v38, v34
	v_cvt_f16_f32_e32 v39, v35
	v_cvt_pk_f16_f32 v26, v26, v27
	v_cvt_pk_f16_f32 v27, v34, v35
	ds_write_b128 v235, v[24:27]
	v_cvt_f32_f16_e32 v24, v36
	v_cvt_f32_f16_e32 v25, v37
	v_cvt_f32_f16_e32 v26, v28
	v_cvt_f32_f16_e32 v27, v29
	v_cvt_f32_f16_e32 v29, v30
	v_cvt_f32_f16_e32 v31, v31
	v_cvt_f32_f16_e32 v34, v38
	v_cvt_f32_f16_e32 v35, v39
	v_add_f32_e32 v24, v24, v25
	v_add_f32_e32 v26, v26, v27
	v_add_f32_e32 v24, v24, v26
	v_add_f32_e32 v26, v29, v31
	v_add_f32_e32 v29, v34, v35
	v_add_f32_e32 v26, v26, v29
	v_add_f32_e32 v24, v24, v26
	v_add_f32_e32 v29, 0, v24
	v_mul_f32_e32 v24, v25, v25
	v_mul_f32_e32 v25, v27, v27
	v_fma_mix_f32 v24, v36, v36, v24 op_sel_hi:[1,1,0]
	v_fma_mix_f32 v25, v28, v28, v25 op_sel_hi:[1,1,0]
	v_mul_f32_e32 v26, v35, v35
	v_add_f32_e32 v24, v24, v25
	v_mul_f32_e32 v25, v31, v31
	v_fma_mix_f32 v25, v30, v30, v25 op_sel_hi:[1,1,0]
	v_fma_mix_f32 v26, v38, v38, v26 op_sel_hi:[1,1,0]
	s_waitcnt vmcnt(14)
	v_cvt_f32_f16_sdwa v27, v76 dst_sel:DWORD dst_unused:UNUSED_PAD src0_sel:WORD_1
	v_add_f32_e32 v25, v25, v26
	v_add_f32_e32 v28, v24, v25
	v_cvt_f32_f16_e32 v26, v76
	v_cvt_f32_f16_sdwa v25, v77 dst_sel:DWORD dst_unused:UNUSED_PAD src0_sel:WORD_1
	v_cvt_f32_f16_e32 v24, v77
	v_cvt_f32_f16_sdwa v30, v78 dst_sel:DWORD dst_unused:UNUSED_PAD src0_sel:WORD_1
	v_cvt_f32_f16_e32 v31, v78
	v_cvt_f32_f16_sdwa v34, v79 dst_sel:DWORD dst_unused:UNUSED_PAD src0_sel:WORD_1
	v_cvt_f32_f16_e32 v35, v79
	v_sub_f32_e32 v24, v24, v196
	v_sub_f32_e32 v25, v25, v196
	v_sub_f32_e32 v26, v26, v196
	v_sub_f32_e32 v27, v27, v196
	v_pk_add_f32 v[20:21], v[20:21], v[200:201]
	v_pk_mul_f32 v[26:27], v[196:197], v[26:27] op_sel:[1,0]
	v_pk_mul_f32 v[24:25], v[196:197], v[24:25] op_sel:[1,0]
	v_pk_fma_f32 v[20:21], v[80:81], v[26:27], v[20:21]
	v_pk_fma_f32 v[22:23], v[82:83], v[24:25], v[22:23]
	v_sub_f32_e32 v24, v35, v196
	v_sub_f32_e32 v25, v34, v196
	v_sub_f32_e32 v26, v31, v196
	v_sub_f32_e32 v27, v30, v196
	v_pk_add_f32 v[18:19], v[18:19], v[192:193]
	v_pk_add_f32 v[16:17], v[16:17], v[194:195]
	v_pk_mul_f32 v[26:27], v[196:197], v[26:27] op_sel:[1,0]
	v_pk_mul_f32 v[24:25], v[196:197], v[24:25] op_sel:[1,0]
	s_waitcnt vmcnt(13)
	v_cvt_f32_f16_sdwa v36, v71 dst_sel:DWORD dst_unused:UNUSED_PAD src0_sel:WORD_1
	v_pk_fma_f32 v[24:25], v[74:75], v[24:25], v[18:19]
	v_pk_fma_f32 v[18:19], v[72:73], v[26:27], v[16:17]
	v_cvt_f16_f32_e32 v26, v20
	v_cvt_f16_f32_e32 v27, v21
	v_cvt_pk_f16_f32 v16, v20, v21
	v_cvt_f16_f32_e32 v20, v22
	v_cvt_f16_f32_e32 v21, v23
	v_cvt_pk_f16_f32 v17, v22, v23
	v_cvt_f16_f32_e32 v23, v19
	v_cvt_f16_f32_e32 v31, v25
	v_cvt_f16_f32_e32 v22, v18
	v_cvt_f16_f32_e32 v30, v24
	v_cvt_pk_f16_f32 v18, v18, v19
	v_cvt_pk_f16_f32 v19, v24, v25
	v_cvt_f32_f16_e32 v25, v27
	v_cvt_f32_f16_e32 v27, v20
	v_cvt_f32_f16_e32 v21, v21
	v_cvt_f32_f16_e32 v23, v23
	v_cvt_f32_f16_e32 v24, v26
	v_cvt_f32_f16_e32 v31, v31
	v_cvt_f32_f16_e32 v34, v22
	v_cvt_f32_f16_e32 v35, v30
	v_add_f32_e32 v27, v27, v21
	v_mul_f32_e32 v21, v21, v21
	v_fma_mix_f32 v20, v20, v20, v21 op_sel_hi:[1,1,0]
	v_mul_f32_e32 v21, v23, v23
	v_add_f32_e32 v24, v24, v25
	v_mul_f32_e32 v25, v25, v25
	v_fma_mix_f32 v21, v22, v22, v21 op_sel_hi:[1,1,0]
	v_mul_f32_e32 v22, v31, v31
	v_add_f32_e32 v24, v24, v27
	v_add_f32_e32 v27, v34, v23
	v_add_f32_e32 v34, v35, v31
	v_fma_mix_f32 v25, v26, v26, v25 op_sel_hi:[1,1,0]
	v_fma_mix_f32 v22, v30, v30, v22 op_sel_hi:[1,1,0]
	v_add_f32_e32 v27, v27, v34
	v_add_f32_e32 v20, v25, v20
	v_add_f32_e32 v21, v21, v22
	v_add_f32_e32 v24, v24, v27
	v_add_f32_e32 v20, v20, v21
	v_add_f32_e32 v24, v29, v24
	v_add_f32_e32 v25, v28, v20
	ds_bpermute_b32 v26, v221, v24
	ds_bpermute_b32 v27, v221, v25
	v_cvt_f32_f16_sdwa v34, v70 dst_sel:DWORD dst_unused:UNUSED_PAD src0_sel:WORD_1
	v_cvt_f32_f16_e32 v35, v70
	v_cvt_f32_f16_e32 v37, v71
	s_waitcnt lgkmcnt(1)
	v_add_f32_e32 v28, v24, v26
	s_waitcnt lgkmcnt(0)
	v_add_f32_e32 v29, v25, v27
	v_cvt_f32_f16_sdwa v27, v68 dst_sel:DWORD dst_unused:UNUSED_PAD src0_sel:WORD_1
	v_cvt_f32_f16_e32 v26, v68
	v_cvt_f32_f16_sdwa v25, v69 dst_sel:DWORD dst_unused:UNUSED_PAD src0_sel:WORD_1
	v_cvt_f32_f16_e32 v24, v69
	v_sub_f32_e32 v27, v27, v190
	v_sub_f32_e32 v26, v26, v190
	v_sub_f32_e32 v25, v25, v190
	v_sub_f32_e32 v24, v24, v190
	v_pk_add_f32 v[14:15], v[14:15], v[206:207]
	v_pk_add_f32 v[12:13], v[12:13], v[208:209]
	v_pk_mul_f32 v[26:27], v[190:191], v[26:27] op_sel:[1,0]
	v_pk_mul_f32 v[24:25], v[190:191], v[24:25] op_sel:[1,0]
	v_pk_fma_f32 v[12:13], v[92:93], v[26:27], v[12:13]
	v_pk_fma_f32 v[14:15], v[94:95], v[24:25], v[14:15]
	v_sub_f32_e32 v24, v37, v190
	v_sub_f32_e32 v25, v36, v190
	v_sub_f32_e32 v26, v35, v190
	v_sub_f32_e32 v27, v34, v190
	v_pk_add_f32 v[10:11], v[10:11], v[202:203]
	v_pk_add_f32 v[8:9], v[8:9], v[204:205]
	v_pk_mul_f32 v[26:27], v[190:191], v[26:27] op_sel:[1,0]
	v_pk_mul_f32 v[24:25], v[190:191], v[24:25] op_sel:[1,0]
	ds_write_b128 v235, v[16:19] offset:64
	v_pk_fma_f32 v[24:25], v[90:91], v[24:25], v[10:11]
	v_pk_fma_f32 v[10:11], v[88:89], v[26:27], v[8:9]
	v_cvt_f16_f32_e32 v26, v12
	v_cvt_f16_f32_e32 v27, v13
	v_cvt_pk_f16_f32 v8, v12, v13
	v_cvt_f16_f32_e32 v12, v14
	v_cvt_f16_f32_e32 v13, v15
	v_cvt_pk_f16_f32 v9, v14, v15
	v_cvt_f16_f32_e32 v14, v10
	v_cvt_f16_f32_e32 v15, v11
	v_cvt_f16_f32_e32 v34, v24
	v_cvt_f16_f32_e32 v35, v25
	v_cvt_pk_f16_f32 v10, v10, v11
	v_cvt_pk_f16_f32 v11, v24, v25
	ds_read_b128 v[16:19], v236
	ds_read_b128 v[20:23], v236 offset:1152
	ds_write_b128 v235, v[8:11]
	v_cvt_f32_f16_e32 v8, v26
	v_cvt_f32_f16_e32 v9, v27
	v_cvt_f32_f16_e32 v10, v12
	v_cvt_f32_f16_e32 v11, v13
	v_cvt_f32_f16_e32 v13, v14
	v_cvt_f32_f16_e32 v15, v15
	v_cvt_f32_f16_e32 v24, v34
	v_cvt_f32_f16_e32 v25, v35
	v_add_f32_e32 v8, v8, v9
	v_add_f32_e32 v10, v10, v11
	v_add_f32_e32 v8, v8, v10
	v_add_f32_e32 v10, v13, v15
	v_add_f32_e32 v13, v24, v25
	v_add_f32_e32 v10, v10, v13
	v_add_f32_e32 v8, v8, v10
	v_add_f32_e32 v13, 0, v8
	v_mul_f32_e32 v8, v9, v9
	v_mul_f32_e32 v9, v11, v11
	v_fma_mix_f32 v8, v26, v26, v8 op_sel_hi:[1,1,0]
	v_fma_mix_f32 v9, v12, v12, v9 op_sel_hi:[1,1,0]
	v_mul_f32_e32 v10, v25, v25
	v_add_f32_e32 v8, v8, v9
	v_mul_f32_e32 v9, v15, v15
	v_fma_mix_f32 v9, v14, v14, v9 op_sel_hi:[1,1,0]
	v_fma_mix_f32 v10, v34, v34, v10 op_sel_hi:[1,1,0]
	s_waitcnt vmcnt(12)
	v_cvt_f32_f16_sdwa v11, v64 dst_sel:DWORD dst_unused:UNUSED_PAD src0_sel:WORD_1
	v_add_f32_e32 v9, v9, v10
	v_add_f32_e32 v12, v8, v9
	v_cvt_f32_f16_e32 v10, v64
	v_cvt_f32_f16_sdwa v9, v65 dst_sel:DWORD dst_unused:UNUSED_PAD src0_sel:WORD_1
	v_cvt_f32_f16_e32 v8, v65
	v_cvt_f32_f16_sdwa v14, v66 dst_sel:DWORD dst_unused:UNUSED_PAD src0_sel:WORD_1
	v_cvt_f32_f16_e32 v15, v66
	v_cvt_f32_f16_sdwa v24, v67 dst_sel:DWORD dst_unused:UNUSED_PAD src0_sel:WORD_1
	v_cvt_f32_f16_e32 v25, v67
	v_sub_f32_e32 v8, v8, v190
	v_sub_f32_e32 v9, v9, v190
	v_sub_f32_e32 v10, v10, v190
	v_sub_f32_e32 v11, v11, v190
	v_pk_add_f32 v[6:7], v[6:7], v[198:199]
	v_pk_add_f32 v[4:5], v[4:5], v[200:201]
	v_pk_mul_f32 v[10:11], v[190:191], v[10:11] op_sel:[1,0]
	v_pk_mul_f32 v[8:9], v[190:191], v[8:9] op_sel:[1,0]
	v_pk_fma_f32 v[4:5], v[80:81], v[10:11], v[4:5]
	v_pk_fma_f32 v[6:7], v[82:83], v[8:9], v[6:7]
	v_sub_f32_e32 v8, v25, v190
	v_sub_f32_e32 v9, v24, v190
	v_sub_f32_e32 v10, v15, v190
	v_sub_f32_e32 v11, v14, v190
	v_pk_add_f32 v[2:3], v[2:3], v[192:193]
	v_pk_add_f32 v[0:1], v[0:1], v[194:195]
	v_pk_mul_f32 v[10:11], v[190:191], v[10:11] op_sel:[1,0]
	v_pk_mul_f32 v[8:9], v[190:191], v[8:9] op_sel:[1,0]
	ds_bpermute_b32 v30, v237, v28
	v_pk_fma_f32 v[8:9], v[74:75], v[8:9], v[2:3]
	v_pk_fma_f32 v[2:3], v[72:73], v[10:11], v[0:1]
	v_cvt_f16_f32_e32 v10, v4
	v_cvt_f16_f32_e32 v11, v5
	v_cvt_pk_f16_f32 v0, v4, v5
	v_cvt_f16_f32_e32 v4, v6
	v_cvt_f16_f32_e32 v5, v7
	v_cvt_pk_f16_f32 v1, v6, v7
	v_cvt_f16_f32_e32 v7, v3
	v_cvt_f16_f32_e32 v15, v9
	v_cvt_f16_f32_e32 v6, v2
	v_cvt_f16_f32_e32 v14, v8
	v_cvt_f32_f16_e32 v25, v4
	v_cvt_f32_f16_e32 v5, v5
	v_cvt_f32_f16_e32 v7, v7
	v_cvt_f32_f16_e32 v24, v10
	v_cvt_f32_f16_e32 v11, v11
	v_cvt_f32_f16_e32 v15, v15
	v_cvt_f32_f16_e32 v26, v6
	v_cvt_f32_f16_e32 v27, v14
	v_add_f32_e32 v25, v25, v5
	v_mul_f32_e32 v5, v5, v5
	v_fma_mix_f32 v4, v4, v4, v5 op_sel_hi:[1,1,0]
	v_mul_f32_e32 v5, v7, v7
	v_add_f32_e32 v24, v24, v11
	v_mul_f32_e32 v11, v11, v11
	v_fma_mix_f32 v5, v6, v6, v5 op_sel_hi:[1,1,0]
	v_mul_f32_e32 v6, v15, v15
	v_add_f32_e32 v24, v24, v25
	v_add_f32_e32 v25, v26, v7
	v_add_f32_e32 v26, v27, v15
	v_fma_mix_f32 v10, v10, v10, v11 op_sel_hi:[1,1,0]
	v_fma_mix_f32 v6, v14, v14, v6 op_sel_hi:[1,1,0]
	v_add_f32_e32 v25, v25, v26
	v_add_f32_e32 v4, v10, v4
	v_add_f32_e32 v5, v5, v6
	v_add_f32_e32 v24, v24, v25
	v_add_f32_e32 v4, v4, v5
	v_add_f32_e32 v13, v13, v24
	v_add_f32_e32 v4, v12, v4
	ds_bpermute_b32 v5, v221, v13
	ds_bpermute_b32 v6, v221, v4
	v_cvt_pk_f16_f32 v2, v2, v3
	v_cvt_pk_f16_f32 v3, v8, v9
	ds_write_b128 v235, v[0:3] offset:64
	s_waitcnt lgkmcnt(2)
	v_add_f32_e32 v10, v13, v5
	s_waitcnt lgkmcnt(1)
	v_add_f32_e32 v11, v4, v6
	ds_bpermute_b32 v31, v237, v29
	ds_bpermute_b32 v12, v237, v10
	ds_bpermute_b32 v13, v237, v11
	ds_read_b128 v[0:3], v236
	ds_read_b128 v[4:7], v236 offset:1152
	v_add_f32_e32 v8, v28, v30
	s_waitcnt lgkmcnt(4)
	v_add_f32_e32 v9, v29, v31
	s_waitcnt lgkmcnt(3)
	v_add_f32_e32 v10, v10, v12
	s_waitcnt lgkmcnt(2)
	v_add_f32_e32 v11, v11, v13
	v_add_u32_e32 v12, 0x3c000, v144
	buffer_store_dwordx4 v[16:19], v12, s[24:27], 0 offen nt
	v_add_u32_e32 v12, 0x3f000, v144
	buffer_store_dwordx4 v[20:23], v12, s[24:27], 0 offen nt
	global_store_dwordx2 v[32:33], v[8:9], off offset:3072
	v_add_u32_e32 v8, 0x42000, v144
	s_waitcnt lgkmcnt(1)
	buffer_store_dwordx4 v[0:3], v8, s[24:27], 0 offen nt
	s_nop 1
	v_add_u32_e32 v0, 0x45000, v144
	s_waitcnt lgkmcnt(0)
	buffer_store_dwordx4 v[4:7], v0, s[24:27], 0 offen nt
	v_add_co_u32_e32 v0, vcc, 0x4000, v140
	s_nop 1
	v_addc_co_u32_e32 v1, vcc, 0, v141, vcc
	global_store_dwordx2 v[0:1], v[10:11], off offset:512
	s_mov_b32 s83, s81
	s_mov_b32 s84, s82
	s_mov_b64 s[40:41], s[0:1]
	s_mov_b64 s[38:39], s[8:9]
	s_mov_b64 vcc, s[6:7]
	s_cbranch_vccz .LBB8_12
	s_waitcnt vmcnt(0)
	s_cmpk_gt_u32 s44, 0xff
	s_cbranch_scc1 .LBB8_31
	s_barrier

.LBB8_32:
	s_endpgm
	s_endpgm
	s_endpgm
	s_endpgm
	s_endpgm
	s_endpgm
	s_endpgm
	s_endpgm
	s_endpgm
	s_endpgm
	.section	.rodata,"a",@progbits
	.p2align	6, 0x0
	.amdhsa_kernel _Z6k_gemmIN2pg6EpiResELi768EEvNS0_4GemmET_
		.amdhsa_group_segment_fixed_size 0
		.amdhsa_private_segment_fixed_size 0
		.amdhsa_kernarg_size 344
		.amdhsa_user_sgpr_count 2
		.amdhsa_user_sgpr_dispatch_ptr 0
		.amdhsa_user_sgpr_queue_ptr 0
		.amdhsa_user_sgpr_kernarg_segment_ptr 1
		.amdhsa_user_sgpr_dispatch_id 0
		.amdhsa_user_sgpr_kernarg_preload_length 0
		.amdhsa_user_sgpr_kernarg_preload_offset 0
		.amdhsa_user_sgpr_private_segment_size 0
		.amdhsa_uses_dynamic_stack 0
		.amdhsa_enable_private_segment 0
		.amdhsa_system_sgpr_workgroup_id_x 1
		.amdhsa_system_sgpr_workgroup_id_y 0
		.amdhsa_system_sgpr_workgroup_id_z 0
		.amdhsa_system_sgpr_workgroup_info 0
		.amdhsa_system_vgpr_workitem_id 0
		.amdhsa_next_free_vgpr 250
		.amdhsa_next_free_sgpr 92
		.amdhsa_accum_offset 252
		.amdhsa_reserve_vcc 1
		.amdhsa_float_round_mode_32 0
		.amdhsa_float_round_mode_16_64 0
		.amdhsa_float_denorm_mode_32 3
		.amdhsa_float_denorm_mode_16_64 3
		.amdhsa_dx10_clamp 1
		.amdhsa_ieee_mode 1
		.amdhsa_fp16_overflow 0
		.amdhsa_tg_split 0
		.amdhsa_exception_fp_ieee_invalid_op 0
		.amdhsa_exception_fp_denorm_src 0
		.amdhsa_exception_fp_ieee_div_zero 0
		.amdhsa_exception_fp_ieee_overflow 0
		.amdhsa_exception_fp_ieee_underflow 0
		.amdhsa_exception_fp_ieee_inexact 0
		.amdhsa_exception_int_div_zero 0
	.end_amdhsa_kernel

.LBB9_26:
	s_min_u32 s77, s47, 2
	s_lshl_b32 s34, s70, 8
	s_add_i32 s34, s34, s48
	v_or_b32_e32 v250, s34, v167
	v_ashrrev_i32_e32 v251, 31, v250
	v_lshl_add_u64 v[250:251], v[250:251], 3, s[12:13]
	s_lshl_b32 s35, s68, 8
	s_or_b32 s35, s35, s51
	v_or_b32_e32 v252, s35, v166
	v_ashrrev_i32_e32 v253, 31, v252
	v_lshl_add_u64 v[252:253], v[252:253], 2, s[14:15]
	global_load_dword v226, v[250:251], off offset:4
	global_load_dword v227, v[250:251], off offset:132
	global_load_dword v228, v[250:251], off offset:260
	global_load_dword v229, v[250:251], off offset:388
	global_load_dword v230, v[250:251], off offset:1028
	global_load_dword v231, v[250:251], off offset:1156
	global_load_dword v232, v[250:251], off offset:1284
	global_load_dword v233, v[250:251], off offset:1412
	global_load_dwordx4 v[234:237], v[252:253], off
	global_load_dwordx4 v[238:241], v[252:253], off offset:16
	global_load_dwordx4 v[242:245], v[252:253], off offset:128
	global_load_dwordx4 v[246:249], v[252:253], off offset:144
	s_add_u32 s28, s28, 0x30080
	s_addc_u32 s29, s29, 0
	s_add_u32 s71, s30, 0x100
	v_mov_b32_e32 v0, 0
	s_addc_u32 s72, s31, 0
	s_mov_b32 s73, -2
	v_mov_b32_e32 v1, v0
	v_mov_b32_e32 v2, v0
	v_mov_b32_e32 v3, v0
	v_mov_b32_e32 v4, v0
	v_mov_b32_e32 v5, v0
	v_mov_b32_e32 v6, v0
	v_mov_b32_e32 v7, v0
	v_mov_b32_e32 v12, v0
	v_mov_b32_e32 v13, v0
	v_mov_b32_e32 v14, v0
	v_mov_b32_e32 v15, v0
	v_mov_b32_e32 v20, v0
	v_mov_b32_e32 v21, v0
	v_mov_b32_e32 v22, v0
	v_mov_b32_e32 v23, v0
	v_mov_b32_e32 v28, v0
	v_mov_b32_e32 v29, v0
	v_mov_b32_e32 v30, v0
	v_mov_b32_e32 v31, v0
	v_mov_b32_e32 v36, v0
	v_mov_b32_e32 v37, v0
	v_mov_b32_e32 v38, v0
	v_mov_b32_e32 v39, v0
	v_mov_b32_e32 v44, v0
	v_mov_b32_e32 v45, v0
	v_mov_b32_e32 v46, v0
	v_mov_b32_e32 v47, v0
	v_mov_b32_e32 v52, v0
	v_mov_b32_e32 v53, v0
	v_mov_b32_e32 v54, v0
	v_mov_b32_e32 v55, v0
	v_mov_b32_e32 v8, v0
	v_mov_b32_e32 v9, v0
	v_mov_b32_e32 v10, v0
	v_mov_b32_e32 v11, v0
	v_mov_b32_e32 v16, v0
	v_mov_b32_e32 v17, v0
	v_mov_b32_e32 v18, v0
	v_mov_b32_e32 v19, v0
	v_mov_b32_e32 v24, v0
	v_mov_b32_e32 v25, v0
	v_mov_b32_e32 v26, v0
	v_mov_b32_e32 v27, v0
	v_mov_b32_e32 v32, v0
	v_mov_b32_e32 v33, v0
	v_mov_b32_e32 v34, v0
	v_mov_b32_e32 v35, v0
	v_mov_b32_e32 v40, v0
	v_mov_b32_e32 v41, v0
	v_mov_b32_e32 v42, v0
	v_mov_b32_e32 v43, v0
	v_mov_b32_e32 v48, v0
	v_mov_b32_e32 v49, v0
	v_mov_b32_e32 v50, v0
	v_mov_b32_e32 v51, v0
	v_mov_b32_e32 v56, v0
	v_mov_b32_e32 v57, v0
	v_mov_b32_e32 v58, v0
	v_mov_b32_e32 v59, v0
	v_mov_b32_e32 v60, v0
	v_mov_b32_e32 v61, v0
	v_mov_b32_e32 v62, v0
	v_mov_b32_e32 v63, v0
	v_mov_b32_e32 v64, v0
	v_mov_b32_e32 v65, v0
	v_mov_b32_e32 v66, v0
	v_mov_b32_e32 v67, v0
	v_mov_b32_e32 v68, v0
	v_mov_b32_e32 v69, v0
	v_mov_b32_e32 v70, v0
	v_mov_b32_e32 v71, v0
	v_mov_b32_e32 v76, v0
	v_mov_b32_e32 v77, v0
	v_mov_b32_e32 v78, v0
	v_mov_b32_e32 v79, v0
	v_mov_b32_e32 v84, v0
	v_mov_b32_e32 v85, v0
	v_mov_b32_e32 v86, v0
	v_mov_b32_e32 v87, v0
	v_mov_b32_e32 v92, v0
	v_mov_b32_e32 v93, v0
	v_mov_b32_e32 v94, v0
	v_mov_b32_e32 v95, v0
	v_mov_b32_e32 v100, v0
	v_mov_b32_e32 v101, v0
	v_mov_b32_e32 v102, v0
	v_mov_b32_e32 v103, v0
	v_mov_b32_e32 v112, v0
	v_mov_b32_e32 v113, v0
	v_mov_b32_e32 v114, v0
	v_mov_b32_e32 v115, v0
	v_mov_b32_e32 v116, v0
	v_mov_b32_e32 v117, v0
	v_mov_b32_e32 v118, v0
	v_mov_b32_e32 v119, v0
	v_mov_b32_e32 v72, v0
	v_mov_b32_e32 v73, v0
	v_mov_b32_e32 v74, v0
	v_mov_b32_e32 v75, v0
	v_mov_b32_e32 v80, v0
	v_mov_b32_e32 v81, v0
	v_mov_b32_e32 v82, v0
	v_mov_b32_e32 v83, v0
	v_mov_b32_e32 v88, v0
	v_mov_b32_e32 v89, v0
	v_mov_b32_e32 v90, v0
	v_mov_b32_e32 v91, v0
	v_mov_b32_e32 v96, v0
	v_mov_b32_e32 v97, v0
	v_mov_b32_e32 v98, v0
	v_mov_b32_e32 v99, v0
	v_mov_b32_e32 v104, v0
	v_mov_b32_e32 v105, v0
	v_mov_b32_e32 v106, v0
	v_mov_b32_e32 v107, v0
	v_mov_b32_e32 v108, v0
	v_mov_b32_e32 v109, v0
	v_mov_b32_e32 v110, v0
	v_mov_b32_e32 v111, v0
	v_mov_b32_e32 v120, v0
	v_mov_b32_e32 v121, v0
	v_mov_b32_e32 v122, v0
	v_mov_b32_e32 v123, v0
	v_mov_b32_e32 v124, v0
	v_mov_b32_e32 v125, v0
	v_mov_b32_e32 v126, v0
	v_mov_b32_e32 v127, v0
.LBB9_27:
	ds_read_b128 v[128:131], v172
	ds_read_b128 v[132:135], v172 offset:1024
	ds_read_b128 v[136:139], v172 offset:2048
	ds_read_b128 v[140:143], v172 offset:3072
	s_add_u32 s30, s28, 0xfffd0080
	s_addc_u32 s31, s29, -1
	s_cmp_eq_u32 s73, 8
	s_cselect_b32 s35, s9, s31
	s_cselect_b32 s34, s8, s30
	s_cselect_b32 s31, s1, s72
	s_cselect_b32 s30, s0, s71
	v_lshl_add_u64 v[202:203], s[28:29], 0, v[152:153]
	s_add_i32 m0, s43, 0xc000
	ds_read_b128 v[158:161], v173
	ds_read_b128 v[162:165], v173 offset:1024
	ds_read_b128 v[178:181], v173 offset:2048
	ds_read_b128 v[182:185], v173 offset:3072
	ds_read_b128 v[186:189], v173 offset:4096
	ds_read_b128 v[190:193], v173 offset:5120
	ds_read_b128 v[194:197], v173 offset:6144
	ds_read_b128 v[198:201], v173 offset:7168
	global_load_lds_dwordx4 v[202:203], off
	v_lshl_add_u64 v[202:203], s[28:29], 0, v[154:155]
	s_add_i32 m0, s43, 0xe000
	s_nop 0
	global_load_lds_dwordx4 v[202:203], off
	s_cmp_eq_u32 s77, 0
	s_cbranch_scc0 .Lvw_9_1_o
	s_waitcnt vmcnt(10)
.Lvw_9_1_j:
	s_waitcnt lgkmcnt(8)
	s_barrier
	s_waitcnt lgkmcnt(0)
	s_setprio 1
	s_waitcnt lgkmcnt(0)
	v_mfma_f32_16x16x32_f16 v[124:127], v[128:131], v[158:161], v[124:127]
	v_mfma_f32_16x16x32_f16 v[120:123], v[136:139], v[158:161], v[120:123]
	v_mfma_f32_16x16x32_f16 v[108:111], v[128:131], v[178:181], v[108:111]
	v_mfma_f32_16x16x32_f16 v[104:107], v[136:139], v[178:181], v[104:107]
	v_mfma_f32_16x16x32_f16 v[96:99], v[128:131], v[186:189], v[96:99]
	v_mfma_f32_16x16x32_f16 v[88:91], v[136:139], v[186:189], v[88:91]
	v_mfma_f32_16x16x32_f16 v[80:83], v[128:131], v[194:197], v[80:83]
	v_mfma_f32_16x16x32_f16 v[72:75], v[136:139], v[194:197], v[72:75]
	v_mfma_f32_16x16x32_f16 v[124:127], v[132:135], v[162:165], v[124:127]
	v_mfma_f32_16x16x32_f16 v[120:123], v[140:143], v[162:165], v[120:123]
	v_mfma_f32_16x16x32_f16 v[108:111], v[132:135], v[182:185], v[108:111]
	v_mfma_f32_16x16x32_f16 v[104:107], v[140:143], v[182:185], v[104:107]
	v_mfma_f32_16x16x32_f16 v[96:99], v[132:135], v[190:193], v[96:99]
	v_mfma_f32_16x16x32_f16 v[88:91], v[140:143], v[190:193], v[88:91]
	v_mfma_f32_16x16x32_f16 v[80:83], v[132:135], v[198:201], v[80:83]
	v_mfma_f32_16x16x32_f16 v[72:75], v[140:143], v[198:201], v[72:75]
	s_setprio 0
	s_barrier
	s_add_i32 s74, s65, s42
	v_lshl_add_u64 v[218:219], s[30:31], 0, v[146:147]
	s_mov_b32 m0, s74
	ds_read_b128 v[202:205], v174
	ds_read_b128 v[206:209], v174 offset:1024
	ds_read_b128 v[210:213], v174 offset:2048
	ds_read_b128 v[214:217], v174 offset:3072
	global_load_lds_dwordx4 v[218:219], off
	v_lshl_add_u64 v[220:221], s[30:31], 0, v[150:151]
	s_add_i32 m0, s74, 0x2000
	s_nop 0
	global_load_lds_dwordx4 v[220:221], off
	s_cmp_eq_u32 s77, 0
	s_cbranch_scc0 .Lvw_9_2_o
	s_waitcnt vmcnt(10)
.Lvw_9_2_j:
	s_barrier
	s_waitcnt lgkmcnt(0)
	s_setprio 1
	s_waitcnt lgkmcnt(0)
	v_mfma_f32_16x16x32_f16 v[116:119], v[202:205], v[158:161], v[116:119]
	v_mfma_f32_16x16x32_f16 v[112:115], v[210:213], v[158:161], v[112:115]
	v_mfma_f32_16x16x32_f16 v[100:103], v[202:205], v[178:181], v[100:103]
	v_mfma_f32_16x16x32_f16 v[92:95], v[210:213], v[178:181], v[92:95]
	v_mfma_f32_16x16x32_f16 v[84:87], v[202:205], v[186:189], v[84:87]
	v_mfma_f32_16x16x32_f16 v[76:79], v[210:213], v[186:189], v[76:79]
	v_mfma_f32_16x16x32_f16 v[68:71], v[202:205], v[194:197], v[68:71]
	v_mfma_f32_16x16x32_f16 v[64:67], v[210:213], v[194:197], v[64:67]
	v_mfma_f32_16x16x32_f16 v[116:119], v[206:209], v[162:165], v[116:119]
	v_mfma_f32_16x16x32_f16 v[112:115], v[214:217], v[162:165], v[112:115]
	v_mfma_f32_16x16x32_f16 v[100:103], v[206:209], v[182:185], v[100:103]
	v_mfma_f32_16x16x32_f16 v[92:95], v[214:217], v[182:185], v[92:95]
	v_mfma_f32_16x16x32_f16 v[84:87], v[206:209], v[190:193], v[84:87]
	v_mfma_f32_16x16x32_f16 v[76:79], v[214:217], v[190:193], v[76:79]
	v_mfma_f32_16x16x32_f16 v[68:71], v[206:209], v[198:201], v[68:71]
	v_mfma_f32_16x16x32_f16 v[64:67], v[214:217], v[198:201], v[64:67]
	s_setprio 0
	s_mov_b32 m0, s43
	v_lshl_add_u64 v[222:223], s[34:35], 0, v[144:145]
	s_barrier
	ds_read_b128 v[158:161], v173 offset:16384
	ds_read_b128 v[162:165], v173 offset:17408
	ds_read_b128 v[178:181], v173 offset:18432
	ds_read_b128 v[182:185], v173 offset:19456
	ds_read_b128 v[186:189], v173 offset:20480
	ds_read_b128 v[190:193], v173 offset:21504
	ds_read_b128 v[194:197], v173 offset:22528
	ds_read_b128 v[198:201], v173 offset:23552
	global_load_lds_dwordx4 v[222:223], off
	v_lshl_add_u64 v[224:225], s[34:35], 0, v[148:149]
	s_mov_b32 m0, s44
	s_nop 0
	global_load_lds_dwordx4 v[224:225], off
	s_barrier
	s_waitcnt lgkmcnt(0)
	s_setprio 1
	s_waitcnt lgkmcnt(0)
	v_mfma_f32_16x16x32_f16 v[60:63], v[128:131], v[158:161], v[60:63]
	v_mfma_f32_16x16x32_f16 v[56:59], v[136:139], v[158:161], v[56:59]
	v_mfma_f32_16x16x32_f16 v[48:51], v[128:131], v[178:181], v[48:51]
	v_mfma_f32_16x16x32_f16 v[40:43], v[136:139], v[178:181], v[40:43]
	v_mfma_f32_16x16x32_f16 v[32:35], v[128:131], v[186:189], v[32:35]
	v_mfma_f32_16x16x32_f16 v[24:27], v[136:139], v[186:189], v[24:27]
	v_mfma_f32_16x16x32_f16 v[16:19], v[128:131], v[194:197], v[16:19]
	v_mfma_f32_16x16x32_f16 v[8:11], v[136:139], v[194:197], v[8:11]
	v_mfma_f32_16x16x32_f16 v[60:63], v[132:135], v[162:165], v[60:63]
	v_mfma_f32_16x16x32_f16 v[56:59], v[140:143], v[162:165], v[56:59]
	v_mfma_f32_16x16x32_f16 v[48:51], v[132:135], v[182:185], v[48:51]
	v_mfma_f32_16x16x32_f16 v[40:43], v[140:143], v[182:185], v[40:43]
	v_mfma_f32_16x16x32_f16 v[32:35], v[132:135], v[190:193], v[32:35]
	v_mfma_f32_16x16x32_f16 v[24:27], v[140:143], v[190:193], v[24:27]
	v_mfma_f32_16x16x32_f16 v[16:19], v[132:135], v[198:201], v[16:19]
	v_mfma_f32_16x16x32_f16 v[8:11], v[140:143], v[198:201], v[8:11]
	s_setprio 0
	s_barrier
	s_add_u32 s74, s30, 0xc000
	s_addc_u32 s75, s31, 0
	s_add_i32 s76, s66, s42
	v_lshl_add_u64 v[128:129], s[74:75], 0, v[146:147]
	s_mov_b32 m0, s76
	s_nop 0
	global_load_lds_dwordx4 v[128:129], off
	v_lshl_add_u64 v[128:129], s[74:75], 0, v[150:151]
	s_add_i32 m0, s76, 0x2000
	s_nop 0
	global_load_lds_dwordx4 v[128:129], off
	s_cmp_eq_u32 s77, 0
	s_cbranch_scc0 .Lvw_9_4_o
	s_waitcnt vmcnt(10)
.Lvw_9_4_j:
	s_barrier
	s_setprio 1
	v_mfma_f32_16x16x32_f16 v[52:55], v[202:205], v[158:161], v[52:55]
	v_mfma_f32_16x16x32_f16 v[44:47], v[210:213], v[158:161], v[44:47]
	v_mfma_f32_16x16x32_f16 v[36:39], v[202:205], v[178:181], v[36:39]
	v_mfma_f32_16x16x32_f16 v[28:31], v[210:213], v[178:181], v[28:31]
	v_mfma_f32_16x16x32_f16 v[20:23], v[202:205], v[186:189], v[20:23]
	v_mfma_f32_16x16x32_f16 v[12:15], v[210:213], v[186:189], v[12:15]
	v_mfma_f32_16x16x32_f16 v[4:7], v[202:205], v[194:197], v[4:7]
	v_mfma_f32_16x16x32_f16 v[0:3], v[210:213], v[194:197], v[0:3]
	v_mfma_f32_16x16x32_f16 v[52:55], v[206:209], v[162:165], v[52:55]
	v_mfma_f32_16x16x32_f16 v[44:47], v[214:217], v[162:165], v[44:47]
	v_mfma_f32_16x16x32_f16 v[36:39], v[206:209], v[182:185], v[36:39]
	v_mfma_f32_16x16x32_f16 v[28:31], v[214:217], v[182:185], v[28:31]
	v_mfma_f32_16x16x32_f16 v[20:23], v[206:209], v[190:193], v[20:23]
	v_mfma_f32_16x16x32_f16 v[12:15], v[214:217], v[190:193], v[12:15]
	v_mfma_f32_16x16x32_f16 v[4:7], v[206:209], v[198:201], v[4:7]
	v_mfma_f32_16x16x32_f16 v[0:3], v[214:217], v[198:201], v[0:3]
	s_setprio 0
	s_add_i32 s74, 0, 0x18000
	v_add_u32_e32 v140, s74, v168
	s_barrier
	ds_read_b128 v[128:131], v140
	ds_read_b128 v[132:135], v140 offset:1024
	ds_read_b128 v[136:139], v140 offset:2048
	ds_read_b128 v[140:143], v140 offset:3072
	s_add_u32 s34, s34, 0x30000
	s_addc_u32 s35, s35, 0
	s_mov_b32 m0, s45
	v_lshl_add_u64 v[202:203], s[34:35], 0, v[144:145]
	ds_read_b128 v[158:161], v173 offset:32768
	ds_read_b128 v[162:165], v173 offset:33792
	ds_read_b128 v[178:181], v173 offset:34816
	ds_read_b128 v[182:185], v173 offset:35840
	ds_read_b128 v[186:189], v173 offset:36864
	ds_read_b128 v[190:193], v173 offset:37888
	ds_read_b128 v[194:197], v173 offset:38912
	ds_read_b128 v[198:201], v173 offset:39936
	global_load_lds_dwordx4 v[202:203], off
	v_lshl_add_u64 v[202:203], s[34:35], 0, v[148:149]
	s_mov_b32 m0, s46
	s_nop 0
	global_load_lds_dwordx4 v[202:203], off
	s_cmp_eq_u32 s77, 0
	s_cbranch_scc0 .Lvw_9_5_o
	s_waitcnt vmcnt(10)
.Lvw_9_5_j:
	s_waitcnt lgkmcnt(8)
	s_barrier
	s_waitcnt lgkmcnt(0)
	s_setprio 1
	s_waitcnt lgkmcnt(0)
	v_mfma_f32_16x16x32_f16 v[124:127], v[128:131], v[158:161], v[124:127]
	v_mfma_f32_16x16x32_f16 v[120:123], v[136:139], v[158:161], v[120:123]
	v_mfma_f32_16x16x32_f16 v[108:111], v[128:131], v[178:181], v[108:111]
	v_mfma_f32_16x16x32_f16 v[104:107], v[136:139], v[178:181], v[104:107]
	v_mfma_f32_16x16x32_f16 v[96:99], v[128:131], v[186:189], v[96:99]
	v_mfma_f32_16x16x32_f16 v[88:91], v[136:139], v[186:189], v[88:91]
	v_mfma_f32_16x16x32_f16 v[80:83], v[128:131], v[194:197], v[80:83]
	v_mfma_f32_16x16x32_f16 v[72:75], v[136:139], v[194:197], v[72:75]
	v_mfma_f32_16x16x32_f16 v[124:127], v[132:135], v[162:165], v[124:127]
	v_mfma_f32_16x16x32_f16 v[120:123], v[140:143], v[162:165], v[120:123]
	v_mfma_f32_16x16x32_f16 v[108:111], v[132:135], v[182:185], v[108:111]
	v_mfma_f32_16x16x32_f16 v[104:107], v[140:143], v[182:185], v[104:107]
	v_mfma_f32_16x16x32_f16 v[96:99], v[132:135], v[190:193], v[96:99]
	v_mfma_f32_16x16x32_f16 v[88:91], v[140:143], v[190:193], v[88:91]
	v_mfma_f32_16x16x32_f16 v[80:83], v[132:135], v[198:201], v[80:83]
	v_mfma_f32_16x16x32_f16 v[72:75], v[140:143], v[198:201], v[72:75]
	s_setprio 0
	s_barrier
	s_add_i32 s34, 0, 0x1c000
	s_add_i32 s35, s74, s42
	v_add_u32_e32 v177, s34, v168
	v_lshl_add_u64 v[218:219], v[218:219], 0, s[26:27]
	s_mov_b32 m0, s35
	ds_read_b128 v[202:205], v177
	ds_read_b128 v[206:209], v177 offset:1024
	ds_read_b128 v[210:213], v177 offset:2048
	ds_read_b128 v[214:217], v177 offset:3072
	global_load_lds_dwordx4 v[218:219], off
	v_lshl_add_u64 v[218:219], v[220:221], 0, s[26:27]
	s_add_i32 m0, s35, 0x2000
	s_nop 0
	global_load_lds_dwordx4 v[218:219], off
	s_waitcnt vmcnt(10)
	s_barrier
	s_waitcnt lgkmcnt(0)
	s_setprio 1
	s_waitcnt lgkmcnt(0)
	v_mfma_f32_16x16x32_f16 v[116:119], v[202:205], v[158:161], v[116:119]
	v_mfma_f32_16x16x32_f16 v[112:115], v[210:213], v[158:161], v[112:115]
	v_mfma_f32_16x16x32_f16 v[100:103], v[202:205], v[178:181], v[100:103]
	v_mfma_f32_16x16x32_f16 v[92:95], v[210:213], v[178:181], v[92:95]
	v_mfma_f32_16x16x32_f16 v[84:87], v[202:205], v[186:189], v[84:87]
	v_mfma_f32_16x16x32_f16 v[76:79], v[210:213], v[186:189], v[76:79]
	v_mfma_f32_16x16x32_f16 v[68:71], v[202:205], v[194:197], v[68:71]
	v_mfma_f32_16x16x32_f16 v[64:67], v[210:213], v[194:197], v[64:67]
	v_mfma_f32_16x16x32_f16 v[116:119], v[206:209], v[162:165], v[116:119]
	v_mfma_f32_16x16x32_f16 v[112:115], v[214:217], v[162:165], v[112:115]
	v_mfma_f32_16x16x32_f16 v[100:103], v[206:209], v[182:185], v[100:103]
	v_mfma_f32_16x16x32_f16 v[92:95], v[214:217], v[182:185], v[92:95]
	v_mfma_f32_16x16x32_f16 v[84:87], v[206:209], v[190:193], v[84:87]
	v_mfma_f32_16x16x32_f16 v[76:79], v[214:217], v[190:193], v[76:79]
	v_mfma_f32_16x16x32_f16 v[68:71], v[206:209], v[198:201], v[68:71]
	v_mfma_f32_16x16x32_f16 v[64:67], v[214:217], v[198:201], v[64:67]
	s_setprio 0
	s_mov_b32 m0, s49
	v_lshl_add_u64 v[218:219], v[222:223], 0, s[26:27]
	s_barrier
	ds_read_b128 v[158:161], v173 offset:49152
	ds_read_b128 v[162:165], v173 offset:50176
	ds_read_b128 v[178:181], v173 offset:51200
	ds_read_b128 v[182:185], v173 offset:52224
	ds_read_b128 v[186:189], v173 offset:53248
	ds_read_b128 v[190:193], v173 offset:54272
	ds_read_b128 v[194:197], v173 offset:55296
	ds_read_b128 v[198:201], v173 offset:56320
	global_load_lds_dwordx4 v[218:219], off
	v_lshl_add_u64 v[218:219], v[224:225], 0, s[26:27]
	s_mov_b32 m0, s50
	s_nop 0
	global_load_lds_dwordx4 v[218:219], off
	s_barrier
	s_waitcnt lgkmcnt(0)
	s_setprio 1
	s_waitcnt lgkmcnt(0)
	v_mfma_f32_16x16x32_f16 v[60:63], v[128:131], v[158:161], v[60:63]
	v_mfma_f32_16x16x32_f16 v[56:59], v[136:139], v[158:161], v[56:59]
	v_mfma_f32_16x16x32_f16 v[48:51], v[128:131], v[178:181], v[48:51]
	v_mfma_f32_16x16x32_f16 v[40:43], v[136:139], v[178:181], v[40:43]
	v_mfma_f32_16x16x32_f16 v[32:35], v[128:131], v[186:189], v[32:35]
	v_mfma_f32_16x16x32_f16 v[24:27], v[136:139], v[186:189], v[24:27]
	v_mfma_f32_16x16x32_f16 v[16:19], v[128:131], v[194:197], v[16:19]
	v_mfma_f32_16x16x32_f16 v[8:11], v[136:139], v[194:197], v[8:11]
	v_mfma_f32_16x16x32_f16 v[60:63], v[132:135], v[162:165], v[60:63]
	v_mfma_f32_16x16x32_f16 v[56:59], v[140:143], v[162:165], v[56:59]
	v_mfma_f32_16x16x32_f16 v[48:51], v[132:135], v[182:185], v[48:51]
	v_mfma_f32_16x16x32_f16 v[40:43], v[140:143], v[182:185], v[40:43]
	v_mfma_f32_16x16x32_f16 v[32:35], v[132:135], v[190:193], v[32:35]
	v_mfma_f32_16x16x32_f16 v[24:27], v[140:143], v[190:193], v[24:27]
	v_mfma_f32_16x16x32_f16 v[16:19], v[132:135], v[198:201], v[16:19]
	v_mfma_f32_16x16x32_f16 v[8:11], v[140:143], v[198:201], v[8:11]
	s_setprio 0
	s_barrier
	s_add_u32 s30, s30, 0xc080
	s_addc_u32 s31, s31, 0
	s_add_i32 s34, s34, s42
	v_lshl_add_u64 v[128:129], s[30:31], 0, v[146:147]
	s_mov_b32 m0, s34
	s_nop 0
	global_load_lds_dwordx4 v[128:129], off
	v_lshl_add_u64 v[128:129], s[30:31], 0, v[150:151]
	s_add_i32 m0, s34, 0x2000
	s_nop 0
	global_load_lds_dwordx4 v[128:129], off
	s_waitcnt vmcnt(10)
	s_barrier
	s_setprio 1
	v_mfma_f32_16x16x32_f16 v[52:55], v[202:205], v[158:161], v[52:55]
	v_mfma_f32_16x16x32_f16 v[44:47], v[210:213], v[158:161], v[44:47]
	v_mfma_f32_16x16x32_f16 v[36:39], v[202:205], v[178:181], v[36:39]
	v_mfma_f32_16x16x32_f16 v[28:31], v[210:213], v[178:181], v[28:31]
	v_mfma_f32_16x16x32_f16 v[20:23], v[202:205], v[186:189], v[20:23]
	v_mfma_f32_16x16x32_f16 v[12:15], v[210:213], v[186:189], v[12:15]
	v_mfma_f32_16x16x32_f16 v[4:7], v[202:205], v[194:197], v[4:7]
	v_mfma_f32_16x16x32_f16 v[0:3], v[210:213], v[194:197], v[0:3]
	v_mfma_f32_16x16x32_f16 v[52:55], v[206:209], v[162:165], v[52:55]
	v_mfma_f32_16x16x32_f16 v[44:47], v[214:217], v[162:165], v[44:47]
	v_mfma_f32_16x16x32_f16 v[36:39], v[206:209], v[182:185], v[36:39]
	v_mfma_f32_16x16x32_f16 v[28:31], v[214:217], v[182:185], v[28:31]
	v_mfma_f32_16x16x32_f16 v[20:23], v[206:209], v[190:193], v[20:23]
	v_mfma_f32_16x16x32_f16 v[12:15], v[214:217], v[190:193], v[12:15]
	v_mfma_f32_16x16x32_f16 v[4:7], v[206:209], v[198:201], v[4:7]
	v_mfma_f32_16x16x32_f16 v[0:3], v[214:217], v[198:201], v[0:3]
	s_setprio 0
	s_add_i32 s73, s73, 2
	s_add_u32 s28, s28, 0x100
	s_addc_u32 s29, s29, 0
	s_add_u32 s71, s71, 0x100
	s_addc_u32 s72, s72, 0
	s_mov_b32 s77, 0
	s_cmp_gt_u32 s73, 9
	s_barrier
	s_cbranch_scc0 .LBB9_27
	s_lshl_b32 s28, s70, 8
	s_add_i32 s28, s28, s48
	s_lshl_b32 s29, s68, 8
	s_or_b32 s29, s29, s51
	s_waitcnt vmcnt(6)
	v_pk_fma_f32 v[126:127], v[126:127], v[226:227], v[236:237] op_sel_hi:[1,0,1]
	v_pk_fma_f32 v[124:125], v[124:125], v[226:227], v[234:235] op_sel_hi:[1,0,1]
	v_pk_fma_f32 v[122:123], v[122:123], v[226:227], v[240:241] op_sel_hi:[1,0,1]
	v_pk_fma_f32 v[120:121], v[120:121], v[226:227], v[238:239] op_sel_hi:[1,0,1]
	v_cvt_pk_f16_f32 v124, v124, v125
	v_cvt_pk_f16_f32 v125, v126, v127
	v_cvt_pk_f16_f32 v126, v120, v121
	v_cvt_pk_f16_f32 v123, v122, v123
	v_pk_fma_f32 v[118:119], v[118:119], v[226:227], v[244:245] op_sel_hi:[1,0,1]
	v_pk_fma_f32 v[116:117], v[116:117], v[226:227], v[242:243] op_sel_hi:[1,0,1]
	v_pk_fma_f32 v[114:115], v[114:115], v[226:227], v[248:249] op_sel_hi:[1,0,1]
	v_pk_fma_f32 v[112:113], v[112:113], v[226:227], v[246:247] op_sel_hi:[1,0,1]
	v_pk_max_f16 v120, v124, 0
	v_pk_max_f16 v121, v125, 0
	v_pk_max_f16 v122, v126, 0
	v_pk_max_f16 v123, v123, 0
	v_cvt_pk_f16_f32 v116, v116, v117
	v_cvt_pk_f16_f32 v117, v118, v119
	v_cvt_pk_f16_f32 v118, v112, v113
	v_cvt_pk_f16_f32 v115, v114, v115
	v_pk_fma_f32 v[110:111], v[110:111], v[226:227], v[236:237] op_sel:[0,1,0]
	v_pk_fma_f32 v[108:109], v[108:109], v[226:227], v[234:235] op_sel:[0,1,0]
	v_pk_fma_f32 v[106:107], v[106:107], v[226:227], v[240:241] op_sel:[0,1,0]
	v_pk_fma_f32 v[104:105], v[104:105], v[226:227], v[238:239] op_sel:[0,1,0]
	v_pk_fma_f32 v[102:103], v[102:103], v[226:227], v[244:245] op_sel:[0,1,0]
	v_pk_fma_f32 v[100:101], v[100:101], v[226:227], v[242:243] op_sel:[0,1,0]
	v_pk_fma_f32 v[94:95], v[94:95], v[226:227], v[248:249] op_sel:[0,1,0]
	v_pk_fma_f32 v[92:93], v[92:93], v[226:227], v[246:247] op_sel:[0,1,0]
	ds_write_b128 v175, v[120:123]
	v_or_b32_e32 v120, s28, v169
	v_pk_max_f16 v112, v116, 0
	v_pk_max_f16 v113, v117, 0
	v_pk_max_f16 v114, v118, 0
	v_pk_max_f16 v115, v115, 0
	v_cvt_pk_f16_f32 v108, v108, v109
	v_cvt_pk_f16_f32 v109, v110, v111
	v_cvt_pk_f16_f32 v110, v104, v105
	v_cvt_pk_f16_f32 v107, v106, v107
	v_cvt_pk_f16_f32 v100, v100, v101
	v_cvt_pk_f16_f32 v101, v102, v103
	v_cvt_pk_f16_f32 v102, v92, v93
	v_cvt_pk_f16_f32 v95, v94, v95
	ds_write_b128 v175, v[112:115] offset:64
	v_mul_lo_u32 v116, v120, s10
	v_pk_max_f16 v104, v108, 0
	v_pk_max_f16 v105, v109, 0
	v_pk_max_f16 v106, v110, 0
	v_pk_max_f16 v107, v107, 0
	v_pk_max_f16 v92, v100, 0
	v_pk_max_f16 v93, v101, 0
	v_pk_max_f16 v94, v102, 0
	v_pk_max_f16 v95, v95, 0
	ds_read_b128 v[112:115], v176
	v_add_u32_e32 v120, s29, v116
	ds_read_b128 v[116:119], v176 offset:1152
	ds_write_b128 v175, v[104:107]
	ds_write_b128 v175, v[92:95] offset:64
	ds_read_b128 v[92:95], v176
	ds_read_b128 v[100:103], v176 offset:1152
	v_lshlrev_b32_e32 v121, 1, v120
	v_add_u32_e32 v122, v121, v170
	v_add_u32_e32 v104, s55, v121
	s_waitcnt lgkmcnt(0)
	buffer_store_dwordx4 v[112:115], v122, s[20:23], 0 offen nt
	v_add_u32_e32 v105, v104, v170
	v_pk_fma_f32 v[90:91], v[90:91], v[228:229], v[240:241] op_sel_hi:[1,0,1]
	v_add_u32_e32 v112, v121, v171
	buffer_store_dwordx4 v[116:119], v112, s[20:23], 0 offen nt
	buffer_store_dwordx4 v[92:95], v105, s[20:23], 0 offen nt
	v_pk_fma_f32 v[88:89], v[88:89], v[228:229], v[238:239] op_sel_hi:[1,0,1]
	v_pk_fma_f32 v[86:87], v[86:87], v[228:229], v[244:245] op_sel_hi:[1,0,1]
	v_pk_fma_f32 v[92:93], v[98:99], v[228:229], v[236:237] op_sel_hi:[1,0,1]
	v_pk_fma_f32 v[94:95], v[96:97], v[228:229], v[234:235] op_sel_hi:[1,0,1]
	v_pk_fma_f32 v[84:85], v[84:85], v[228:229], v[242:243] op_sel_hi:[1,0,1]
	v_pk_fma_f32 v[78:79], v[78:79], v[228:229], v[248:249] op_sel_hi:[1,0,1]
	v_pk_fma_f32 v[76:77], v[76:77], v[228:229], v[246:247] op_sel_hi:[1,0,1]
	v_cvt_pk_f16_f32 v94, v94, v95
	v_cvt_pk_f16_f32 v92, v92, v93
	v_cvt_pk_f16_f32 v93, v88, v89
	v_cvt_pk_f16_f32 v91, v90, v91
	v_cvt_pk_f16_f32 v84, v84, v85
	v_cvt_pk_f16_f32 v85, v86, v87
	v_cvt_pk_f16_f32 v86, v76, v77
	v_cvt_pk_f16_f32 v79, v78, v79
	v_pk_max_f16 v88, v94, 0
	v_pk_max_f16 v89, v92, 0
	v_pk_max_f16 v90, v93, 0
	v_pk_max_f16 v91, v91, 0
	v_pk_max_f16 v76, v84, 0
	v_pk_max_f16 v77, v85, 0
	v_pk_max_f16 v78, v86, 0
	v_pk_max_f16 v79, v79, 0
	ds_write_b128 v175, v[88:91]
	ds_write_b128 v175, v[76:79] offset:64
	ds_read_b128 v[76:79], v176
	ds_read_b128 v[84:87], v176 offset:1152
	v_add_u32_e32 v88, s55, v104
	v_add_u32_e32 v105, v104, v171
	v_add_u32_e32 v89, v88, v170
	buffer_store_dwordx4 v[100:103], v105, s[20:23], 0 offen nt
	s_waitcnt lgkmcnt(1)
	buffer_store_dwordx4 v[76:79], v89, s[20:23], 0 offen nt
	v_pk_fma_f32 v[74:75], v[74:75], v[228:229], v[240:241] op_sel:[0,1,0]
	v_pk_fma_f32 v[72:73], v[72:73], v[228:229], v[238:239] op_sel:[0,1,0]
	v_add_u32_e32 v76, v88, v171
	s_waitcnt lgkmcnt(0)
	buffer_store_dwordx4 v[84:87], v76, s[20:23], 0 offen nt
	v_pk_fma_f32 v[76:77], v[82:83], v[228:229], v[236:237] op_sel:[0,1,0]
	v_pk_fma_f32 v[78:79], v[80:81], v[228:229], v[234:235] op_sel:[0,1,0]
	v_pk_fma_f32 v[70:71], v[70:71], v[228:229], v[244:245] op_sel:[0,1,0]
	v_pk_fma_f32 v[68:69], v[68:69], v[228:229], v[242:243] op_sel:[0,1,0]
	v_pk_fma_f32 v[66:67], v[66:67], v[228:229], v[248:249] op_sel:[0,1,0]
	v_pk_fma_f32 v[64:65], v[64:65], v[228:229], v[246:247] op_sel:[0,1,0]
	v_cvt_pk_f16_f32 v78, v78, v79
	v_cvt_pk_f16_f32 v76, v76, v77
	v_cvt_pk_f16_f32 v77, v72, v73
	v_cvt_pk_f16_f32 v75, v74, v75
	v_cvt_pk_f16_f32 v68, v68, v69
	v_cvt_pk_f16_f32 v69, v70, v71
	v_cvt_pk_f16_f32 v70, v64, v65
	v_cvt_pk_f16_f32 v67, v66, v67
	v_pk_fma_f32 v[62:63], v[62:63], v[230:231], v[236:237] op_sel_hi:[1,0,1]
	v_pk_fma_f32 v[60:61], v[60:61], v[230:231], v[234:235] op_sel_hi:[1,0,1]
	v_pk_fma_f32 v[58:59], v[58:59], v[230:231], v[240:241] op_sel_hi:[1,0,1]
	v_pk_fma_f32 v[56:57], v[56:57], v[230:231], v[238:239] op_sel_hi:[1,0,1]
	v_pk_fma_f32 v[54:55], v[54:55], v[230:231], v[244:245] op_sel_hi:[1,0,1]
	v_pk_fma_f32 v[52:53], v[52:53], v[230:231], v[242:243] op_sel_hi:[1,0,1]
	v_pk_fma_f32 v[46:47], v[46:47], v[230:231], v[248:249] op_sel_hi:[1,0,1]
	v_pk_fma_f32 v[44:45], v[44:45], v[230:231], v[246:247] op_sel_hi:[1,0,1]
	v_pk_max_f16 v72, v78, 0
	v_pk_max_f16 v73, v76, 0
	v_pk_max_f16 v74, v77, 0
	v_pk_max_f16 v75, v75, 0
	v_pk_max_f16 v64, v68, 0
	v_pk_max_f16 v65, v69, 0
	v_pk_max_f16 v66, v70, 0
	v_pk_max_f16 v67, v67, 0
	v_cvt_pk_f16_f32 v60, v60, v61
	v_cvt_pk_f16_f32 v61, v62, v63
	v_cvt_pk_f16_f32 v62, v56, v57
	v_cvt_pk_f16_f32 v59, v58, v59
	v_cvt_pk_f16_f32 v52, v52, v53
	v_cvt_pk_f16_f32 v53, v54, v55
	v_cvt_pk_f16_f32 v54, v44, v45
	v_cvt_pk_f16_f32 v47, v46, v47
	ds_write_b128 v175, v[72:75]
	ds_write_b128 v175, v[64:67] offset:64
	v_pk_max_f16 v56, v60, 0
	v_pk_max_f16 v57, v61, 0
	v_pk_max_f16 v58, v62, 0
	v_pk_max_f16 v59, v59, 0
	v_pk_max_f16 v44, v52, 0
	v_pk_max_f16 v45, v53, 0
	v_pk_max_f16 v46, v54, 0
	v_pk_max_f16 v47, v47, 0
	ds_read_b128 v[64:67], v176
	ds_read_b128 v[68:71], v176 offset:1152
	ds_write_b128 v175, v[56:59]
	ds_write_b128 v175, v[44:47] offset:64
	ds_read_b128 v[44:47], v176
	ds_read_b128 v[52:55], v176 offset:1152
	v_add_u32_e32 v72, s56, v120
	v_lshlrev_b32_e32 v73, 1, v72
	v_add_u32_e32 v74, v73, v170
	v_add_u32_e32 v56, s62, v88
	s_waitcnt lgkmcnt(5)
	buffer_store_dwordx4 v[64:67], v74, s[20:23], 0 offen nt
	v_add_u32_e32 v57, v56, v170
	v_pk_fma_f32 v[42:43], v[42:43], v[230:231], v[240:241] op_sel:[0,1,0]
	v_add_u32_e32 v64, v73, v171
	s_waitcnt lgkmcnt(4)
	buffer_store_dwordx4 v[68:71], v64, s[20:23], 0 offen nt
	s_waitcnt lgkmcnt(1)
	buffer_store_dwordx4 v[44:47], v57, s[20:23], 0 offen nt
	v_pk_fma_f32 v[40:41], v[40:41], v[230:231], v[238:239] op_sel:[0,1,0]
	v_pk_fma_f32 v[38:39], v[38:39], v[230:231], v[244:245] op_sel:[0,1,0]
	v_add_u32_e32 v44, v56, v171
	s_waitcnt lgkmcnt(0)
	buffer_store_dwordx4 v[52:55], v44, s[20:23], 0 offen nt
	v_pk_fma_f32 v[44:45], v[50:51], v[230:231], v[236:237] op_sel:[0,1,0]
	v_pk_fma_f32 v[46:47], v[48:49], v[230:231], v[234:235] op_sel:[0,1,0]
	v_pk_fma_f32 v[36:37], v[36:37], v[230:231], v[242:243] op_sel:[0,1,0]
	v_pk_fma_f32 v[30:31], v[30:31], v[230:231], v[248:249] op_sel:[0,1,0]
	v_pk_fma_f32 v[28:29], v[28:29], v[230:231], v[246:247] op_sel:[0,1,0]
	v_cvt_pk_f16_f32 v46, v46, v47
	v_cvt_pk_f16_f32 v44, v44, v45
	v_cvt_pk_f16_f32 v45, v40, v41
	v_cvt_pk_f16_f32 v43, v42, v43
	v_cvt_pk_f16_f32 v36, v36, v37
	v_cvt_pk_f16_f32 v37, v38, v39
	v_cvt_pk_f16_f32 v38, v28, v29
	v_cvt_pk_f16_f32 v31, v30, v31
	v_pk_max_f16 v40, v46, 0
	v_pk_max_f16 v41, v44, 0
	v_pk_max_f16 v42, v45, 0
	v_pk_max_f16 v43, v43, 0
	v_pk_max_f16 v28, v36, 0
	v_pk_max_f16 v29, v37, 0
	v_pk_max_f16 v30, v38, 0
	v_pk_max_f16 v31, v31, 0
	ds_write_b128 v175, v[40:43]
	ds_write_b128 v175, v[28:31] offset:64
	ds_read_b128 v[28:31], v176
	ds_read_b128 v[36:39], v176 offset:1152
	v_add_u32_e32 v40, s63, v72
	v_lshlrev_b32_e32 v41, 1, v40
	v_add_u32_e32 v42, v41, v170
	s_waitcnt lgkmcnt(1)
	buffer_store_dwordx4 v[28:31], v42, s[20:23], 0 offen nt
	v_pk_fma_f32 v[26:27], v[26:27], v[232:233], v[240:241] op_sel_hi:[1,0,1]
	v_pk_fma_f32 v[24:25], v[24:25], v[232:233], v[238:239] op_sel_hi:[1,0,1]
	v_add_u32_e32 v28, v41, v171
	s_waitcnt lgkmcnt(0)
	buffer_store_dwordx4 v[36:39], v28, s[20:23], 0 offen nt
	v_pk_fma_f32 v[28:29], v[34:35], v[232:233], v[236:237] op_sel_hi:[1,0,1]
	v_pk_fma_f32 v[30:31], v[32:33], v[232:233], v[234:235] op_sel_hi:[1,0,1]
	v_pk_fma_f32 v[22:23], v[22:23], v[232:233], v[244:245] op_sel_hi:[1,0,1]
	v_pk_fma_f32 v[20:21], v[20:21], v[232:233], v[242:243] op_sel_hi:[1,0,1]
	v_pk_fma_f32 v[14:15], v[14:15], v[232:233], v[248:249] op_sel_hi:[1,0,1]
	v_pk_fma_f32 v[12:13], v[12:13], v[232:233], v[246:247] op_sel_hi:[1,0,1]
	v_cvt_pk_f16_f32 v30, v30, v31
	v_cvt_pk_f16_f32 v28, v28, v29
	v_cvt_pk_f16_f32 v29, v24, v25
	v_cvt_pk_f16_f32 v27, v26, v27
	v_cvt_pk_f16_f32 v20, v20, v21
	v_cvt_pk_f16_f32 v21, v22, v23
	v_cvt_pk_f16_f32 v22, v12, v13
	v_cvt_pk_f16_f32 v15, v14, v15
	v_pk_max_f16 v24, v30, 0
	v_pk_max_f16 v25, v28, 0
	v_pk_max_f16 v26, v29, 0
	v_pk_max_f16 v27, v27, 0
	v_pk_max_f16 v12, v20, 0
	v_pk_max_f16 v13, v21, 0
	v_pk_max_f16 v14, v22, 0
	v_pk_max_f16 v15, v15, 0
	ds_write_b128 v175, v[24:27]
	ds_write_b128 v175, v[12:15] offset:64
	ds_read_b128 v[12:15], v176
	ds_read_b128 v[20:23], v176 offset:1152
	v_add_u32_e32 v24, s64, v40
	v_lshlrev_b32_e32 v25, 1, v24
	v_add_u32_e32 v26, v25, v170
	s_waitcnt lgkmcnt(1)
	buffer_store_dwordx4 v[12:15], v26, s[20:23], 0 offen nt
	v_pk_fma_f32 v[10:11], v[10:11], v[232:233], v[240:241] op_sel:[0,1,0]
	v_pk_fma_f32 v[8:9], v[8:9], v[232:233], v[238:239] op_sel:[0,1,0]
	v_pk_fma_f32 v[12:13], v[18:19], v[232:233], v[236:237] op_sel:[0,1,0]
	v_pk_fma_f32 v[14:15], v[16:17], v[232:233], v[234:235] op_sel:[0,1,0]
	v_pk_fma_f32 v[6:7], v[6:7], v[232:233], v[244:245] op_sel:[0,1,0]
	v_pk_fma_f32 v[4:5], v[4:5], v[232:233], v[242:243] op_sel:[0,1,0]
	v_pk_fma_f32 v[2:3], v[2:3], v[232:233], v[248:249] op_sel:[0,1,0]
	v_pk_fma_f32 v[0:1], v[0:1], v[232:233], v[246:247] op_sel:[0,1,0]
	v_cvt_pk_f16_f32 v14, v14, v15
	v_cvt_pk_f16_f32 v12, v12, v13
	v_cvt_pk_f16_f32 v13, v8, v9
	v_cvt_pk_f16_f32 v11, v10, v11
	v_cvt_pk_f16_f32 v4, v4, v5
	v_cvt_pk_f16_f32 v5, v6, v7
	v_cvt_pk_f16_f32 v6, v0, v1
	v_cvt_pk_f16_f32 v3, v2, v3
	v_pk_max_f16 v8, v14, 0
	v_pk_max_f16 v9, v12, 0
	v_pk_max_f16 v10, v13, 0
	v_pk_max_f16 v11, v11, 0
	v_pk_max_f16 v0, v4, 0
	v_pk_max_f16 v1, v5, 0
	v_pk_max_f16 v2, v6, 0
	v_pk_max_f16 v3, v3, 0
	ds_write_b128 v175, v[8:11]
	ds_write_b128 v175, v[0:3] offset:64
	ds_read_b128 v[0:3], v176
	ds_read_b128 v[4:7], v176 offset:1152
	v_add_lshl_u32 v8, v24, s64, 1
	v_add_u32_e32 v25, v25, v171
	v_add_u32_e32 v9, v8, v170
	s_waitcnt lgkmcnt(4)
	buffer_store_dwordx4 v[20:23], v25, s[20:23], 0 offen nt
	s_waitcnt lgkmcnt(1)
	buffer_store_dwordx4 v[0:3], v9, s[20:23], 0 offen nt
	s_mov_b32 s68, s67
	s_mov_b32 s70, s69
	v_add_u32_e32 v0, v8, v171
	s_mov_b64 s[30:31], s[0:1]
	s_mov_b64 s[28:29], s[8:9]
	s_mov_b64 vcc, s[6:7]
	s_waitcnt lgkmcnt(0)
	buffer_store_dwordx4 v[4:7], v0, s[20:23], 0 offen nt
	s_cbranch_vccz .LBB9_12
	s_waitcnt vmcnt(0)
	s_cmpk_gt_u32 s36, 0xff
	s_cbranch_scc1 .LBB9_31
	s_barrier

.Lvw_9_4_t0:
	s_waitcnt vmcnt(22)
	s_branch .Lvw_9_4_j
	s_endpgm
	s_endpgm
	s_endpgm
	s_endpgm
	s_endpgm
	s_endpgm
	s_endpgm
	s_endpgm
	s_endpgm
	s_endpgm
	s_endpgm
	s_endpgm
	s_endpgm
	s_endpgm
	s_endpgm
	s_endpgm
	s_endpgm
	s_endpgm

	.amdhsa_kernel _Z6k_gemmIN2pg6EpiLinILi1EEELi768EEvNS0_4GemmET_
		.amdhsa_group_segment_fixed_size 0
		.amdhsa_private_segment_fixed_size 0
		.amdhsa_kernarg_size 320
		.amdhsa_user_sgpr_count 2
		.amdhsa_user_sgpr_dispatch_ptr 0
		.amdhsa_user_sgpr_queue_ptr 0
		.amdhsa_user_sgpr_kernarg_segment_ptr 1
		.amdhsa_user_sgpr_dispatch_id 0
		.amdhsa_user_sgpr_kernarg_preload_length 0
		.amdhsa_user_sgpr_kernarg_preload_offset 0
		.amdhsa_user_sgpr_private_segment_size 0
		.amdhsa_uses_dynamic_stack 0
		.amdhsa_enable_private_segment 0
		.amdhsa_system_sgpr_workgroup_id_x 1
		.amdhsa_system_sgpr_workgroup_id_y 0
		.amdhsa_system_sgpr_workgroup_id_z 0
		.amdhsa_system_sgpr_workgroup_info 0
		.amdhsa_system_vgpr_workitem_id 0
		.amdhsa_next_free_vgpr 254
		.amdhsa_next_free_sgpr 78
		.amdhsa_accum_offset 256
		.amdhsa_reserve_vcc 1
		.amdhsa_float_round_mode_32 0
		.amdhsa_float_round_mode_16_64 0
		.amdhsa_float_denorm_mode_32 3
		.amdhsa_float_denorm_mode_16_64 3
		.amdhsa_dx10_clamp 1
		.amdhsa_ieee_mode 1
		.amdhsa_fp16_overflow 0
		.amdhsa_tg_split 0
		.amdhsa_exception_fp_ieee_invalid_op 0
		.amdhsa_exception_fp_denorm_src 0
		.amdhsa_exception_fp_ieee_div_zero 0
		.amdhsa_exception_fp_ieee_overflow 0
		.amdhsa_exception_fp_ieee_underflow 0
		.amdhsa_exception_fp_ieee_inexact 0
		.amdhsa_exception_int_div_zero 0
	.end_amdhsa_kernel

.LBB10_26:
	s_cmp_eq_u32 s80, 1
	s_cselect_b32 s91, 0, 2
	s_add_u32 s38, s38, 0xc0080
	s_addc_u32 s39, s39, 0
	s_add_u32 s85, s40, 0x100
	v_mov_b32_e32 v0, 0
	s_addc_u32 s86, s41, 0
	s_mov_b32 s87, -2
	v_mov_b32_e32 v1, v0
	v_mov_b32_e32 v2, v0
	v_mov_b32_e32 v3, v0
	v_mov_b32_e32 v4, v0
	v_mov_b32_e32 v5, v0
	v_mov_b32_e32 v6, v0
	v_mov_b32_e32 v7, v0
	v_mov_b32_e32 v16, v0
	v_mov_b32_e32 v17, v0
	v_mov_b32_e32 v18, v0
	v_mov_b32_e32 v19, v0
	v_mov_b32_e32 v20, v0
	v_mov_b32_e32 v21, v0
	v_mov_b32_e32 v22, v0
	v_mov_b32_e32 v23, v0
	v_mov_b32_e32 v32, v0
	v_mov_b32_e32 v33, v0
	v_mov_b32_e32 v34, v0
	v_mov_b32_e32 v35, v0
	v_mov_b32_e32 v36, v0
	v_mov_b32_e32 v37, v0
	v_mov_b32_e32 v38, v0
	v_mov_b32_e32 v39, v0
	v_mov_b32_e32 v48, v0
	v_mov_b32_e32 v49, v0
	v_mov_b32_e32 v50, v0
	v_mov_b32_e32 v51, v0
	v_mov_b32_e32 v52, v0
	v_mov_b32_e32 v53, v0
	v_mov_b32_e32 v54, v0
	v_mov_b32_e32 v55, v0
	v_mov_b32_e32 v8, v0
	v_mov_b32_e32 v9, v0
	v_mov_b32_e32 v10, v0
	v_mov_b32_e32 v11, v0
	v_mov_b32_e32 v12, v0
	v_mov_b32_e32 v13, v0
	v_mov_b32_e32 v14, v0
	v_mov_b32_e32 v15, v0
	v_mov_b32_e32 v24, v0
	v_mov_b32_e32 v25, v0
	v_mov_b32_e32 v26, v0
	v_mov_b32_e32 v27, v0
	v_mov_b32_e32 v28, v0
	v_mov_b32_e32 v29, v0
	v_mov_b32_e32 v30, v0
	v_mov_b32_e32 v31, v0
	v_mov_b32_e32 v40, v0
	v_mov_b32_e32 v41, v0
	v_mov_b32_e32 v42, v0
	v_mov_b32_e32 v43, v0
	v_mov_b32_e32 v44, v0
	v_mov_b32_e32 v45, v0
	v_mov_b32_e32 v46, v0
	v_mov_b32_e32 v47, v0
	v_mov_b32_e32 v56, v0
	v_mov_b32_e32 v57, v0
	v_mov_b32_e32 v58, v0
	v_mov_b32_e32 v59, v0
	v_mov_b32_e32 v60, v0
	v_mov_b32_e32 v61, v0
	v_mov_b32_e32 v62, v0
	v_mov_b32_e32 v63, v0
	v_mov_b32_e32 v64, v0
	v_mov_b32_e32 v65, v0
	v_mov_b32_e32 v66, v0
	v_mov_b32_e32 v67, v0
	v_mov_b32_e32 v68, v0
	v_mov_b32_e32 v69, v0
	v_mov_b32_e32 v70, v0
	v_mov_b32_e32 v71, v0
	v_mov_b32_e32 v96, v0
	v_mov_b32_e32 v97, v0
	v_mov_b32_e32 v98, v0
	v_mov_b32_e32 v99, v0
	v_mov_b32_e32 v100, v0
	v_mov_b32_e32 v101, v0
	v_mov_b32_e32 v102, v0
	v_mov_b32_e32 v103, v0
	v_mov_b32_e32 v112, v0
	v_mov_b32_e32 v113, v0
	v_mov_b32_e32 v114, v0
	v_mov_b32_e32 v115, v0
	v_mov_b32_e32 v116, v0
	v_mov_b32_e32 v117, v0
	v_mov_b32_e32 v118, v0
	v_mov_b32_e32 v119, v0
	v_mov_b32_e32 v128, v0
	v_mov_b32_e32 v129, v0
	v_mov_b32_e32 v130, v0
	v_mov_b32_e32 v131, v0
	v_mov_b32_e32 v132, v0
	v_mov_b32_e32 v133, v0
	v_mov_b32_e32 v134, v0
	v_mov_b32_e32 v135, v0
	v_mov_b32_e32 v76, v0
	v_mov_b32_e32 v77, v0
	v_mov_b32_e32 v78, v0
	v_mov_b32_e32 v79, v0
	v_mov_b32_e32 v84, v0
	v_mov_b32_e32 v85, v0
	v_mov_b32_e32 v86, v0
	v_mov_b32_e32 v87, v0
	v_mov_b32_e32 v104, v0
	v_mov_b32_e32 v105, v0
	v_mov_b32_e32 v106, v0
	v_mov_b32_e32 v107, v0
	v_mov_b32_e32 v108, v0
	v_mov_b32_e32 v109, v0
	v_mov_b32_e32 v110, v0
	v_mov_b32_e32 v111, v0
	v_mov_b32_e32 v120, v0
	v_mov_b32_e32 v121, v0
	v_mov_b32_e32 v122, v0
	v_mov_b32_e32 v123, v0
	v_mov_b32_e32 v124, v0
	v_mov_b32_e32 v125, v0
	v_mov_b32_e32 v126, v0
	v_mov_b32_e32 v127, v0
	v_mov_b32_e32 v140, v0
	v_mov_b32_e32 v141, v0
	v_mov_b32_e32 v142, v0
	v_mov_b32_e32 v143, v0
	v_mov_b32_e32 v144, v0
	v_mov_b32_e32 v145, v0
	v_mov_b32_e32 v146, v0
	v_mov_b32_e32 v147, v0
.LBB10_27:
	ds_read_b128 v[72:75], v231
	ds_read_b128 v[80:83], v231 offset:1024
	ds_read_b128 v[88:91], v231 offset:2048
	ds_read_b128 v[92:95], v231 offset:3072
	s_add_u32 s40, s38, 0xfff40080
	s_addc_u32 s41, s39, -1
	s_cmp_eq_u32 s87, 44
	s_cselect_b32 s43, s9, s41
	s_cselect_b32 s42, s8, s40
	s_cselect_b32 s41, s1, s86
	s_cselect_b32 s40, s0, s85
	v_lshl_add_u64 v[190:191], s[38:39], 0, v[184:185]
	s_add_i32 m0, s51, 0xc000
	ds_read_b128 v[136:139], v232
	ds_read_b128 v[148:151], v232 offset:1024
	ds_read_b128 v[152:155], v232 offset:2048
	ds_read_b128 v[156:159], v232 offset:3072
	ds_read_b128 v[160:163], v232 offset:4096
	ds_read_b128 v[164:167], v232 offset:5120
	ds_read_b128 v[168:171], v232 offset:6144
	ds_read_b128 v[172:175], v232 offset:7168
	global_load_lds_dwordx4 v[190:191], off
	v_lshl_add_u64 v[190:191], s[38:39], 0, v[186:187]
	s_add_i32 m0, s51, 0xe000
	s_nop 0
	global_load_lds_dwordx4 v[190:191], off
	s_cmp_eq_u32 s91, 0
	s_cbranch_scc0 .Lvw_10_1_j
	s_waitcnt vmcnt(10)
.Lvw_10_1_j:
	s_waitcnt lgkmcnt(8)
	s_barrier
	s_waitcnt lgkmcnt(0)
	s_setprio 1
	s_waitcnt lgkmcnt(0)
	v_mfma_f32_16x16x32_f16 v[144:147], v[72:75], v[136:139], v[144:147]
	v_mfma_f32_16x16x32_f16 v[140:143], v[88:91], v[136:139], v[140:143]
	v_mfma_f32_16x16x32_f16 v[124:127], v[72:75], v[152:155], v[124:127]
	v_mfma_f32_16x16x32_f16 v[120:123], v[88:91], v[152:155], v[120:123]
	v_mfma_f32_16x16x32_f16 v[108:111], v[72:75], v[160:163], v[108:111]
	v_mfma_f32_16x16x32_f16 v[104:107], v[88:91], v[160:163], v[104:107]
	v_mfma_f32_16x16x32_f16 v[84:87], v[72:75], v[168:171], v[84:87]
	v_mfma_f32_16x16x32_f16 v[76:79], v[88:91], v[168:171], v[76:79]
	v_mfma_f32_16x16x32_f16 v[144:147], v[80:83], v[148:151], v[144:147]
	v_mfma_f32_16x16x32_f16 v[140:143], v[92:95], v[148:151], v[140:143]
	v_mfma_f32_16x16x32_f16 v[124:127], v[80:83], v[156:159], v[124:127]
	v_mfma_f32_16x16x32_f16 v[120:123], v[92:95], v[156:159], v[120:123]
	v_mfma_f32_16x16x32_f16 v[108:111], v[80:83], v[164:167], v[108:111]
	v_mfma_f32_16x16x32_f16 v[104:107], v[92:95], v[164:167], v[104:107]
	v_mfma_f32_16x16x32_f16 v[84:87], v[80:83], v[172:175], v[84:87]
	v_mfma_f32_16x16x32_f16 v[76:79], v[92:95], v[172:175], v[76:79]
	s_setprio 0
	s_barrier
	s_add_i32 s88, s69, s50
	v_lshl_add_u64 v[206:207], s[40:41], 0, v[178:179]
	s_mov_b32 m0, s88
	ds_read_b128 v[190:193], v233
	ds_read_b128 v[194:197], v233 offset:1024
	ds_read_b128 v[198:201], v233 offset:2048
	ds_read_b128 v[202:205], v233 offset:3072
	global_load_lds_dwordx4 v[206:207], off
	v_lshl_add_u64 v[208:209], s[40:41], 0, v[182:183]
	s_add_i32 m0, s88, 0x2000
	s_nop 0
	global_load_lds_dwordx4 v[208:209], off
	s_cmp_eq_u32 s91, 0
	s_cbranch_scc0 .Lvw_10_2_j
	s_waitcnt vmcnt(10)
.Lvw_10_2_j:
	s_barrier
	s_waitcnt lgkmcnt(0)
	s_setprio 1
	s_waitcnt lgkmcnt(0)
	v_mfma_f32_16x16x32_f16 v[132:135], v[190:193], v[136:139], v[132:135]
	v_mfma_f32_16x16x32_f16 v[128:131], v[198:201], v[136:139], v[128:131]
	v_mfma_f32_16x16x32_f16 v[116:119], v[190:193], v[152:155], v[116:119]
	v_mfma_f32_16x16x32_f16 v[112:115], v[198:201], v[152:155], v[112:115]
	v_mfma_f32_16x16x32_f16 v[100:103], v[190:193], v[160:163], v[100:103]
	v_mfma_f32_16x16x32_f16 v[96:99], v[198:201], v[160:163], v[96:99]
	v_mfma_f32_16x16x32_f16 v[68:71], v[190:193], v[168:171], v[68:71]
	v_mfma_f32_16x16x32_f16 v[64:67], v[198:201], v[168:171], v[64:67]
	v_mfma_f32_16x16x32_f16 v[132:135], v[194:197], v[148:151], v[132:135]
	v_mfma_f32_16x16x32_f16 v[128:131], v[202:205], v[148:151], v[128:131]
	v_mfma_f32_16x16x32_f16 v[116:119], v[194:197], v[156:159], v[116:119]
	v_mfma_f32_16x16x32_f16 v[112:115], v[202:205], v[156:159], v[112:115]
	v_mfma_f32_16x16x32_f16 v[100:103], v[194:197], v[164:167], v[100:103]
	v_mfma_f32_16x16x32_f16 v[96:99], v[202:205], v[164:167], v[96:99]
	v_mfma_f32_16x16x32_f16 v[68:71], v[194:197], v[172:175], v[68:71]
	v_mfma_f32_16x16x32_f16 v[64:67], v[202:205], v[172:175], v[64:67]
	s_setprio 0
	s_mov_b32 m0, s51
	v_lshl_add_u64 v[210:211], s[42:43], 0, v[176:177]
	s_barrier
	ds_read_b128 v[136:139], v232 offset:16384
	ds_read_b128 v[148:151], v232 offset:17408
	ds_read_b128 v[152:155], v232 offset:18432
	ds_read_b128 v[156:159], v232 offset:19456
	ds_read_b128 v[160:163], v232 offset:20480
	ds_read_b128 v[164:167], v232 offset:21504
	ds_read_b128 v[168:171], v232 offset:22528
	ds_read_b128 v[172:175], v232 offset:23552
	global_load_lds_dwordx4 v[210:211], off
	v_lshl_add_u64 v[212:213], s[42:43], 0, v[180:181]
	s_mov_b32 m0, s52
	s_nop 0
	global_load_lds_dwordx4 v[212:213], off
	s_barrier
	s_waitcnt lgkmcnt(0)
	s_setprio 1
	s_waitcnt lgkmcnt(0)
	v_mfma_f32_16x16x32_f16 v[60:63], v[72:75], v[136:139], v[60:63]
	v_mfma_f32_16x16x32_f16 v[56:59], v[88:91], v[136:139], v[56:59]
	v_mfma_f32_16x16x32_f16 v[44:47], v[72:75], v[152:155], v[44:47]
	v_mfma_f32_16x16x32_f16 v[40:43], v[88:91], v[152:155], v[40:43]
	v_mfma_f32_16x16x32_f16 v[28:31], v[72:75], v[160:163], v[28:31]
	v_mfma_f32_16x16x32_f16 v[24:27], v[88:91], v[160:163], v[24:27]
	v_mfma_f32_16x16x32_f16 v[12:15], v[72:75], v[168:171], v[12:15]
	v_mfma_f32_16x16x32_f16 v[8:11], v[88:91], v[168:171], v[8:11]
	v_mfma_f32_16x16x32_f16 v[60:63], v[80:83], v[148:151], v[60:63]
	v_mfma_f32_16x16x32_f16 v[56:59], v[92:95], v[148:151], v[56:59]
	v_mfma_f32_16x16x32_f16 v[44:47], v[80:83], v[156:159], v[44:47]
	v_mfma_f32_16x16x32_f16 v[40:43], v[92:95], v[156:159], v[40:43]
	v_mfma_f32_16x16x32_f16 v[28:31], v[80:83], v[164:167], v[28:31]
	v_mfma_f32_16x16x32_f16 v[24:27], v[92:95], v[164:167], v[24:27]
	v_mfma_f32_16x16x32_f16 v[12:15], v[80:83], v[172:175], v[12:15]
	v_mfma_f32_16x16x32_f16 v[8:11], v[92:95], v[172:175], v[8:11]
	s_setprio 0
	s_barrier
	s_add_u32 s88, s40, 0x30000
	s_addc_u32 s89, s41, 0
	s_add_i32 s90, s70, s50
	v_lshl_add_u64 v[72:73], s[88:89], 0, v[178:179]
	s_mov_b32 m0, s90
	s_nop 0
	global_load_lds_dwordx4 v[72:73], off
	v_lshl_add_u64 v[72:73], s[88:89], 0, v[182:183]
	s_add_i32 m0, s90, 0x2000
	s_nop 0
	global_load_lds_dwordx4 v[72:73], off
	s_cmp_eq_u32 s91, 0
	s_cbranch_scc0 .Lvw_10_4_j
	s_waitcnt vmcnt(10)
.Lvw_10_4_j:
	s_barrier
	s_setprio 1
	v_mfma_f32_16x16x32_f16 v[52:55], v[190:193], v[136:139], v[52:55]
	v_mfma_f32_16x16x32_f16 v[48:51], v[198:201], v[136:139], v[48:51]
	v_mfma_f32_16x16x32_f16 v[36:39], v[190:193], v[152:155], v[36:39]
	v_mfma_f32_16x16x32_f16 v[32:35], v[198:201], v[152:155], v[32:35]
	v_mfma_f32_16x16x32_f16 v[20:23], v[190:193], v[160:163], v[20:23]
	v_mfma_f32_16x16x32_f16 v[16:19], v[198:201], v[160:163], v[16:19]
	v_mfma_f32_16x16x32_f16 v[4:7], v[190:193], v[168:171], v[4:7]
	v_mfma_f32_16x16x32_f16 v[0:3], v[198:201], v[168:171], v[0:3]
	v_mfma_f32_16x16x32_f16 v[52:55], v[194:197], v[148:151], v[52:55]
	v_mfma_f32_16x16x32_f16 v[48:51], v[202:205], v[148:151], v[48:51]
	v_mfma_f32_16x16x32_f16 v[36:39], v[194:197], v[156:159], v[36:39]
	v_mfma_f32_16x16x32_f16 v[32:35], v[202:205], v[156:159], v[32:35]
	v_mfma_f32_16x16x32_f16 v[20:23], v[194:197], v[164:167], v[20:23]
	v_mfma_f32_16x16x32_f16 v[16:19], v[202:205], v[164:167], v[16:19]
	v_mfma_f32_16x16x32_f16 v[4:7], v[194:197], v[172:175], v[4:7]
	v_mfma_f32_16x16x32_f16 v[0:3], v[202:205], v[172:175], v[0:3]
	s_setprio 0
	s_add_i32 s88, 0, 0x18000
	v_add_u32_e32 v92, s88, v228
	s_barrier
	ds_read_b128 v[72:75], v92
	ds_read_b128 v[80:83], v92 offset:1024
	ds_read_b128 v[88:91], v92 offset:2048
	ds_read_b128 v[92:95], v92 offset:3072
	s_add_u32 s42, s42, 0xc0000
	s_addc_u32 s43, s43, 0
	s_mov_b32 m0, s53
	v_lshl_add_u64 v[190:191], s[42:43], 0, v[176:177]
	ds_read_b128 v[136:139], v232 offset:32768
	ds_read_b128 v[148:151], v232 offset:33792
	ds_read_b128 v[152:155], v232 offset:34816
	ds_read_b128 v[156:159], v232 offset:35840
	ds_read_b128 v[160:163], v232 offset:36864
	ds_read_b128 v[164:167], v232 offset:37888
	ds_read_b128 v[168:171], v232 offset:38912
	ds_read_b128 v[172:175], v232 offset:39936
	global_load_lds_dwordx4 v[190:191], off
	v_lshl_add_u64 v[190:191], s[42:43], 0, v[180:181]
	s_mov_b32 m0, s54
	s_nop 0
	global_load_lds_dwordx4 v[190:191], off
	s_cmp_eq_u32 s91, 0
	s_cbranch_scc0 .Lvw_10_5_j
	s_waitcnt vmcnt(10)
.Lvw_10_5_j:
	s_waitcnt lgkmcnt(8)
	s_barrier
	s_waitcnt lgkmcnt(0)
	s_setprio 1
	s_waitcnt lgkmcnt(0)
	v_mfma_f32_16x16x32_f16 v[144:147], v[72:75], v[136:139], v[144:147]
	v_mfma_f32_16x16x32_f16 v[140:143], v[88:91], v[136:139], v[140:143]
	v_mfma_f32_16x16x32_f16 v[124:127], v[72:75], v[152:155], v[124:127]
	v_mfma_f32_16x16x32_f16 v[120:123], v[88:91], v[152:155], v[120:123]
	v_mfma_f32_16x16x32_f16 v[108:111], v[72:75], v[160:163], v[108:111]
	v_mfma_f32_16x16x32_f16 v[104:107], v[88:91], v[160:163], v[104:107]
	v_mfma_f32_16x16x32_f16 v[84:87], v[72:75], v[168:171], v[84:87]
	v_mfma_f32_16x16x32_f16 v[76:79], v[88:91], v[168:171], v[76:79]
	v_mfma_f32_16x16x32_f16 v[144:147], v[80:83], v[148:151], v[144:147]
	v_mfma_f32_16x16x32_f16 v[140:143], v[92:95], v[148:151], v[140:143]
	v_mfma_f32_16x16x32_f16 v[124:127], v[80:83], v[156:159], v[124:127]
	v_mfma_f32_16x16x32_f16 v[120:123], v[92:95], v[156:159], v[120:123]
	v_mfma_f32_16x16x32_f16 v[108:111], v[80:83], v[164:167], v[108:111]
	v_mfma_f32_16x16x32_f16 v[104:107], v[92:95], v[164:167], v[104:107]
	v_mfma_f32_16x16x32_f16 v[84:87], v[80:83], v[172:175], v[84:87]
	v_mfma_f32_16x16x32_f16 v[76:79], v[92:95], v[172:175], v[76:79]
	s_setprio 0
	s_barrier
	s_add_i32 s42, 0, 0x1c000
	s_add_i32 s43, s88, s50
	v_add_u32_e32 v202, s42, v228
	v_lshl_add_u64 v[206:207], v[206:207], 0, s[36:37]
	s_mov_b32 m0, s43
	ds_read_b128 v[190:193], v202
	ds_read_b128 v[194:197], v202 offset:1024
	ds_read_b128 v[198:201], v202 offset:2048
	ds_read_b128 v[202:205], v202 offset:3072
	global_load_lds_dwordx4 v[206:207], off
	v_lshl_add_u64 v[206:207], v[208:209], 0, s[36:37]
	s_add_i32 m0, s43, 0x2000
	s_nop 0
	global_load_lds_dwordx4 v[206:207], off
	s_waitcnt vmcnt(10)
	s_barrier
	s_waitcnt lgkmcnt(0)
	s_setprio 1
	s_waitcnt lgkmcnt(0)
	v_mfma_f32_16x16x32_f16 v[132:135], v[190:193], v[136:139], v[132:135]
	v_mfma_f32_16x16x32_f16 v[128:131], v[198:201], v[136:139], v[128:131]
	v_mfma_f32_16x16x32_f16 v[116:119], v[190:193], v[152:155], v[116:119]
	v_mfma_f32_16x16x32_f16 v[112:115], v[198:201], v[152:155], v[112:115]
	v_mfma_f32_16x16x32_f16 v[100:103], v[190:193], v[160:163], v[100:103]
	v_mfma_f32_16x16x32_f16 v[96:99], v[198:201], v[160:163], v[96:99]
	v_mfma_f32_16x16x32_f16 v[68:71], v[190:193], v[168:171], v[68:71]
	v_mfma_f32_16x16x32_f16 v[64:67], v[198:201], v[168:171], v[64:67]
	v_mfma_f32_16x16x32_f16 v[132:135], v[194:197], v[148:151], v[132:135]
	v_mfma_f32_16x16x32_f16 v[128:131], v[202:205], v[148:151], v[128:131]
	v_mfma_f32_16x16x32_f16 v[116:119], v[194:197], v[156:159], v[116:119]
	v_mfma_f32_16x16x32_f16 v[112:115], v[202:205], v[156:159], v[112:115]
	v_mfma_f32_16x16x32_f16 v[100:103], v[194:197], v[164:167], v[100:103]
	v_mfma_f32_16x16x32_f16 v[96:99], v[202:205], v[164:167], v[96:99]
	v_mfma_f32_16x16x32_f16 v[68:71], v[194:197], v[172:175], v[68:71]
	v_mfma_f32_16x16x32_f16 v[64:67], v[202:205], v[172:175], v[64:67]
	s_setprio 0
	s_mov_b32 m0, s58
	v_lshl_add_u64 v[206:207], v[210:211], 0, s[36:37]
	s_barrier
	ds_read_b128 v[136:139], v232 offset:49152
	ds_read_b128 v[148:151], v232 offset:50176
	ds_read_b128 v[152:155], v232 offset:51200
	ds_read_b128 v[156:159], v232 offset:52224
	ds_read_b128 v[160:163], v232 offset:53248
	ds_read_b128 v[164:167], v232 offset:54272
	ds_read_b128 v[168:171], v232 offset:55296
	ds_read_b128 v[172:175], v232 offset:56320
	global_load_lds_dwordx4 v[206:207], off
	v_lshl_add_u64 v[206:207], v[212:213], 0, s[36:37]
	s_mov_b32 m0, s59
	s_nop 0
	global_load_lds_dwordx4 v[206:207], off
	s_barrier
	s_waitcnt lgkmcnt(0)
	s_setprio 1
	s_waitcnt lgkmcnt(0)
	v_mfma_f32_16x16x32_f16 v[60:63], v[72:75], v[136:139], v[60:63]
	v_mfma_f32_16x16x32_f16 v[56:59], v[88:91], v[136:139], v[56:59]
	v_mfma_f32_16x16x32_f16 v[44:47], v[72:75], v[152:155], v[44:47]
	v_mfma_f32_16x16x32_f16 v[40:43], v[88:91], v[152:155], v[40:43]
	v_mfma_f32_16x16x32_f16 v[28:31], v[72:75], v[160:163], v[28:31]
	v_mfma_f32_16x16x32_f16 v[24:27], v[88:91], v[160:163], v[24:27]
	v_mfma_f32_16x16x32_f16 v[12:15], v[72:75], v[168:171], v[12:15]
	v_mfma_f32_16x16x32_f16 v[8:11], v[88:91], v[168:171], v[8:11]
	v_mfma_f32_16x16x32_f16 v[60:63], v[80:83], v[148:151], v[60:63]
	v_mfma_f32_16x16x32_f16 v[56:59], v[92:95], v[148:151], v[56:59]
	v_mfma_f32_16x16x32_f16 v[44:47], v[80:83], v[156:159], v[44:47]
	v_mfma_f32_16x16x32_f16 v[40:43], v[92:95], v[156:159], v[40:43]
	v_mfma_f32_16x16x32_f16 v[28:31], v[80:83], v[164:167], v[28:31]
	v_mfma_f32_16x16x32_f16 v[24:27], v[92:95], v[164:167], v[24:27]
	v_mfma_f32_16x16x32_f16 v[12:15], v[80:83], v[172:175], v[12:15]
	v_mfma_f32_16x16x32_f16 v[8:11], v[92:95], v[172:175], v[8:11]
	s_setprio 0
	s_barrier
	s_add_u32 s40, s40, 0x30080
	s_addc_u32 s41, s41, 0
	s_add_i32 s42, s42, s50
	v_lshl_add_u64 v[72:73], s[40:41], 0, v[178:179]
	s_mov_b32 m0, s42
	s_nop 0
	global_load_lds_dwordx4 v[72:73], off
	v_lshl_add_u64 v[72:73], s[40:41], 0, v[182:183]
	s_add_i32 m0, s42, 0x2000
	s_nop 0
	global_load_lds_dwordx4 v[72:73], off
	s_waitcnt vmcnt(10)
	s_barrier
	s_setprio 1
	v_mfma_f32_16x16x32_f16 v[52:55], v[190:193], v[136:139], v[52:55]
	v_mfma_f32_16x16x32_f16 v[48:51], v[198:201], v[136:139], v[48:51]
	v_mfma_f32_16x16x32_f16 v[36:39], v[190:193], v[152:155], v[36:39]
	v_mfma_f32_16x16x32_f16 v[32:35], v[198:201], v[152:155], v[32:35]
	v_mfma_f32_16x16x32_f16 v[20:23], v[190:193], v[160:163], v[20:23]
	v_mfma_f32_16x16x32_f16 v[16:19], v[198:201], v[160:163], v[16:19]
	v_mfma_f32_16x16x32_f16 v[4:7], v[190:193], v[168:171], v[4:7]
	v_mfma_f32_16x16x32_f16 v[0:3], v[198:201], v[168:171], v[0:3]
	v_mfma_f32_16x16x32_f16 v[52:55], v[194:197], v[148:151], v[52:55]
	v_mfma_f32_16x16x32_f16 v[48:51], v[202:205], v[148:151], v[48:51]
	v_mfma_f32_16x16x32_f16 v[36:39], v[194:197], v[156:159], v[36:39]
	v_mfma_f32_16x16x32_f16 v[32:35], v[202:205], v[156:159], v[32:35]
	v_mfma_f32_16x16x32_f16 v[20:23], v[194:197], v[164:167], v[20:23]
	v_mfma_f32_16x16x32_f16 v[16:19], v[202:205], v[164:167], v[16:19]
	v_mfma_f32_16x16x32_f16 v[4:7], v[194:197], v[172:175], v[4:7]
	v_mfma_f32_16x16x32_f16 v[0:3], v[202:205], v[172:175], v[0:3]
	s_setprio 0
	s_add_i32 s87, s87, 2
	s_add_u32 s38, s38, 0x100
	s_addc_u32 s39, s39, 0
	s_add_u32 s85, s85, 0x100
	s_addc_u32 s86, s86, 0
	s_mov_b32 s91, 0
	s_cmp_gt_u32 s87, 45
	s_barrier
	s_cbranch_scc0 .LBB10_27
	s_lshl_b32 s38, s84, 8
	s_lshl_b32 s39, s83, 8
	s_add_i32 s38, s38, s57
	s_or_b32 s39, s39, s60
	v_or_b32_e32 v72, s39, v226
	v_or_b32_e32 v220, s38, v227
	v_mov_b64_e32 v[74:75], s[10:11]
	v_mad_i64_i32 v[74:75], s[40:41], v220, s71, v[74:75]
	v_ashrrev_i32_e32 v73, 31, v72
	v_lshl_add_u64 v[214:215], v[72:73], 1, v[74:75]
	v_add_co_u32_e32 v74, vcc, 0x6000, v214
	global_load_dwordx4 v[172:175], v[214:215], off nt
	global_load_dwordx4 v[168:171], v[214:215], off offset:64 nt
	v_addc_co_u32_e32 v75, vcc, 0, v215, vcc
	global_load_dwordx4 v[164:167], v[74:75], off nt
	global_load_dwordx4 v[160:163], v[74:75], off offset:64 nt
	v_add_co_u32_e32 v74, vcc, 0xc000, v214
	v_ashrrev_i32_e32 v221, 31, v220
	s_nop 0
	v_addc_co_u32_e32 v75, vcc, 0, v215, vcc
	global_load_dwordx4 v[156:159], v[74:75], off nt
	global_load_dwordx4 v[152:155], v[74:75], off offset:64 nt
	v_add_co_u32_e32 v74, vcc, s56, v214
	v_lshlrev_b64 v[72:73], 2, v[72:73]
	s_nop 0
	v_addc_co_u32_e32 v75, vcc, 0, v215, vcc
	global_load_dwordx4 v[148:151], v[74:75], off nt
	global_load_dwordx4 v[136:139], v[74:75], off offset:64 nt
	v_lshl_add_u64 v[74:75], v[220:221], 3, s[12:13]
	v_lshl_add_u64 v[238:239], s[14:15], 0, v[72:73]
	global_load_dwordx2 v[224:225], v[74:75], off
	global_load_dwordx2 v[222:223], v[74:75], off offset:128
	global_load_dwordx2 v[218:219], v[74:75], off offset:256
	global_load_dwordx2 v[216:217], v[74:75], off offset:384
	global_load_dwordx2 v[212:213], v[74:75], off offset:1024
	global_load_dwordx2 v[210:211], v[74:75], off offset:1152
	global_load_dwordx2 v[196:197], v[74:75], off offset:1280
	global_load_dwordx2 v[190:191], v[74:75], off offset:1408
	v_lshl_add_u64 v[242:243], s[16:17], 0, v[72:73]
	v_lshl_add_u64 v[246:247], s[18:19], 0, v[72:73]
	global_load_dwordx4 v[88:91], v[238:239], off offset:16
	global_load_dwordx4 v[92:95], v[238:239], off
	global_load_dwordx4 v[72:75], v[242:243], off offset:16
	global_load_dwordx4 v[80:83], v[242:243], off
	global_load_dwordx4 v[192:195], v[246:247], off offset:16
	global_load_dwordx4 v[198:201], v[246:247], off
	v_or_b32_e32 v221, s38, v229
	v_mul_lo_u32 v221, v221, s72
	v_and_b32_e32 v237, 64, v234
	v_add_u32_e32 v237, 64, v237
	s_lshl_b32 s38, s83, 2
	s_waitcnt vmcnt(0)
	v_pk_add_f32 v[202:203], v[74:75], v[194:195]
	v_pk_add_f32 v[206:207], v[82:83], v[200:201]
	v_pk_add_f32 v[208:209], v[80:81], v[198:199]
	v_pk_add_f32 v[204:205], v[72:73], v[192:193]
	global_load_dwordx4 v[72:75], v[238:239], off offset:144
	global_load_dwordx4 v[80:83], v[238:239], off offset:128
	s_nop 0
	global_load_dwordx4 v[238:241], v[242:243], off offset:144
	global_load_dwordx4 v[192:195], v[242:243], off offset:128
	s_nop 0
	global_load_dwordx4 v[242:245], v[246:247], off offset:144
	s_nop 0
	global_load_dwordx4 v[246:249], v[246:247], off offset:128
	v_pk_add_f32 v[146:147], v[146:147], v[206:207]
	v_pk_add_f32 v[144:145], v[144:145], v[208:209]
	v_pk_add_f32 v[142:143], v[142:143], v[202:203]
	v_pk_add_f32 v[140:141], v[140:141], v[204:205]
	v_pk_add_f32 v[126:127], v[126:127], v[206:207]
	v_pk_add_f32 v[124:125], v[124:125], v[208:209]
	v_pk_add_f32 v[122:123], v[122:123], v[202:203]
	v_pk_add_f32 v[120:121], v[120:121], v[204:205]
	s_waitcnt vmcnt(0)
	v_pk_add_f32 v[198:199], v[194:195], v[248:249]
	v_pk_add_f32 v[194:195], v[238:239], v[242:243]
	v_add_u32_e32 v238, s39, v221
	v_xor_b32_e32 v221, 16, v234
	v_cmp_lt_i32_e32 vcc, v221, v237
	v_xor_b32_e32 v239, 32, v234
	v_pk_add_f32 v[200:201], v[192:193], v[246:247]
	v_cndmask_b32_e32 v221, v234, v221, vcc
	v_cmp_lt_i32_e32 vcc, v239, v237
	v_pk_add_f32 v[192:193], v[240:241], v[244:245]
	v_cvt_f32_f16_e32 v240, v172
	v_cndmask_b32_e32 v237, v234, v239, vcc
	v_cvt_f32_f16_sdwa v239, v172 dst_sel:DWORD dst_unused:UNUSED_PAD src0_sel:WORD_1
	v_cvt_f32_f16_sdwa v241, v173 dst_sel:DWORD dst_unused:UNUSED_PAD src0_sel:WORD_1
	v_cvt_f32_f16_e32 v172, v173
	v_cvt_f32_f16_sdwa v242, v174 dst_sel:DWORD dst_unused:UNUSED_PAD src0_sel:WORD_1
	v_cvt_f32_f16_e32 v243, v174
	v_cvt_f32_f16_sdwa v244, v175 dst_sel:DWORD dst_unused:UNUSED_PAD src0_sel:WORD_1
	v_cvt_f32_f16_e32 v245, v175
	v_sub_f32_e32 v172, v172, v224
	v_sub_f32_e32 v173, v241, v224
	v_sub_f32_e32 v174, v240, v224
	v_sub_f32_e32 v175, v239, v224
	v_pk_mul_f32 v[174:175], v[224:225], v[174:175] op_sel:[1,0]
	v_pk_mul_f32 v[172:173], v[224:225], v[172:173] op_sel:[1,0]
	v_pk_fma_f32 v[144:145], v[174:175], v[92:93], v[144:145]
	v_pk_fma_f32 v[146:147], v[172:173], v[94:95], v[146:147]
	v_sub_f32_e32 v172, v245, v224
	v_sub_f32_e32 v173, v244, v224
	v_sub_f32_e32 v174, v243, v224
	v_sub_f32_e32 v175, v242, v224
	v_pk_mul_f32 v[174:175], v[224:225], v[174:175] op_sel:[1,0]
	v_pk_mul_f32 v[172:173], v[224:225], v[172:173] op_sel:[1,0]
	v_pk_add_f32 v[134:135], v[134:135], v[198:199]
	v_pk_fma_f32 v[172:173], v[172:173], v[90:91], v[142:143]
	v_pk_fma_f32 v[142:143], v[174:175], v[88:89], v[140:141]
	v_cvt_f16_f32_e32 v174, v144
	v_cvt_f16_f32_e32 v175, v145
	v_cvt_pk_f16_f32 v140, v144, v145
	v_cvt_f16_f32_e32 v144, v146
	v_cvt_f16_f32_e32 v145, v147
	v_cvt_pk_f16_f32 v141, v146, v147
	v_cvt_f16_f32_e32 v146, v142
	v_cvt_f16_f32_e32 v147, v143
	v_cvt_f16_f32_e32 v239, v172
	v_cvt_f16_f32_e32 v240, v173
	v_cvt_pk_f16_f32 v142, v142, v143
	v_cvt_pk_f16_f32 v143, v172, v173
	ds_write_b128 v235, v[140:143]
	v_cvt_f32_f16_e32 v140, v174
	v_cvt_f32_f16_e32 v141, v175
	v_cvt_f32_f16_e32 v142, v144
	v_cvt_f32_f16_e32 v143, v145
	v_cvt_f32_f16_e32 v145, v146
	v_cvt_f32_f16_e32 v147, v147
	v_cvt_f32_f16_e32 v172, v239
	v_cvt_f32_f16_e32 v173, v240
	v_add_f32_e32 v140, v140, v141
	v_add_f32_e32 v142, v142, v143
	v_add_f32_e32 v140, v140, v142
	v_add_f32_e32 v142, v145, v147
	v_add_f32_e32 v145, v172, v173
	v_add_f32_e32 v142, v142, v145
	v_add_f32_e32 v140, v140, v142
	v_add_f32_e32 v145, 0, v140
	v_mul_f32_e32 v140, v141, v141
	v_mul_f32_e32 v141, v143, v143
	v_fma_mix_f32 v140, v174, v174, v140 op_sel_hi:[1,1,0]
	v_fma_mix_f32 v141, v144, v144, v141 op_sel_hi:[1,1,0]
	v_mul_f32_e32 v142, v173, v173
	v_add_f32_e32 v140, v140, v141
	v_mul_f32_e32 v141, v147, v147
	v_fma_mix_f32 v141, v146, v146, v141 op_sel_hi:[1,1,0]
	v_fma_mix_f32 v142, v239, v239, v142 op_sel_hi:[1,1,0]
	v_cvt_f32_f16_sdwa v143, v168 dst_sel:DWORD dst_unused:UNUSED_PAD src0_sel:WORD_1
	v_add_f32_e32 v141, v141, v142
	v_add_f32_e32 v144, v140, v141
	v_cvt_f32_f16_e32 v142, v168
	v_cvt_f32_f16_sdwa v141, v169 dst_sel:DWORD dst_unused:UNUSED_PAD src0_sel:WORD_1
	v_cvt_f32_f16_e32 v140, v169
	v_cvt_f32_f16_sdwa v146, v170 dst_sel:DWORD dst_unused:UNUSED_PAD src0_sel:WORD_1
	v_cvt_f32_f16_e32 v147, v170
	v_cvt_f32_f16_sdwa v168, v171 dst_sel:DWORD dst_unused:UNUSED_PAD src0_sel:WORD_1
	v_cvt_f32_f16_e32 v169, v171
	v_sub_f32_e32 v140, v140, v224
	v_sub_f32_e32 v141, v141, v224
	v_sub_f32_e32 v142, v142, v224
	v_sub_f32_e32 v143, v143, v224
	v_pk_add_f32 v[132:133], v[132:133], v[200:201]
	v_pk_mul_f32 v[142:143], v[224:225], v[142:143] op_sel:[1,0]
	v_pk_mul_f32 v[140:141], v[224:225], v[140:141] op_sel:[1,0]
	v_pk_fma_f32 v[132:133], v[142:143], v[80:81], v[132:133]
	v_pk_fma_f32 v[134:135], v[140:141], v[82:83], v[134:135]
	v_sub_f32_e32 v140, v169, v224
	v_sub_f32_e32 v141, v168, v224
	v_sub_f32_e32 v142, v147, v224
	v_sub_f32_e32 v143, v146, v224
	v_pk_add_f32 v[130:131], v[130:131], v[192:193]
	v_pk_add_f32 v[128:129], v[128:129], v[194:195]
	v_pk_mul_f32 v[142:143], v[224:225], v[142:143] op_sel:[1,0]
	v_pk_mul_f32 v[140:141], v[224:225], v[140:141] op_sel:[1,0]
	v_lshlrev_b32_e32 v221, 2, v221
	v_pk_fma_f32 v[140:141], v[140:141], v[74:75], v[130:131]
	v_pk_fma_f32 v[130:131], v[142:143], v[72:73], v[128:129]
	v_cvt_f16_f32_e32 v142, v132
	v_cvt_f16_f32_e32 v143, v133
	v_cvt_pk_f16_f32 v128, v132, v133
	v_cvt_f16_f32_e32 v132, v134
	v_cvt_f16_f32_e32 v133, v135
	v_cvt_pk_f16_f32 v129, v134, v135
	v_cvt_f16_f32_e32 v134, v130
	v_cvt_f16_f32_e32 v135, v131
	v_cvt_f16_f32_e32 v146, v140
	v_cvt_f16_f32_e32 v147, v141
	v_cvt_pk_f16_f32 v130, v130, v131
	v_cvt_pk_f16_f32 v131, v140, v141
	ds_write_b128 v235, v[128:131] offset:64
	v_cvt_f32_f16_e32 v128, v142
	v_cvt_f32_f16_e32 v129, v143
	v_cvt_f32_f16_e32 v130, v132
	v_cvt_f32_f16_e32 v131, v133
	v_cvt_f32_f16_e32 v133, v134
	v_cvt_f32_f16_e32 v135, v135
	v_cvt_f32_f16_e32 v140, v146
	v_cvt_f32_f16_e32 v141, v147
	v_add_f32_e32 v128, v128, v129
	v_add_f32_e32 v130, v130, v131
	v_add_f32_e32 v128, v128, v130
	v_add_f32_e32 v130, v133, v135
	v_add_f32_e32 v133, v140, v141
	v_add_f32_e32 v130, v130, v133
	v_add_f32_e32 v128, v128, v130
	v_add_f32_e32 v140, v145, v128
	v_mul_f32_e32 v128, v129, v129
	v_mul_f32_e32 v129, v131, v131
	v_fma_mix_f32 v128, v142, v142, v128 op_sel_hi:[1,1,0]
	v_fma_mix_f32 v129, v132, v132, v129 op_sel_hi:[1,1,0]
	v_mul_f32_e32 v130, v141, v141
	v_add_f32_e32 v128, v128, v129
	v_mul_f32_e32 v129, v135, v135
	ds_bpermute_b32 v142, v221, v140
	v_fma_mix_f32 v129, v134, v134, v129 op_sel_hi:[1,1,0]
	v_fma_mix_f32 v130, v146, v146, v130 op_sel_hi:[1,1,0]
	v_lshlrev_b32_e32 v237, 2, v237
	v_add_f32_e32 v129, v129, v130
	v_add_f32_e32 v128, v128, v129
	v_add_f32_e32 v141, v144, v128
	s_waitcnt lgkmcnt(0)
	v_add_f32_e32 v140, v140, v142
	ds_bpermute_b32 v142, v221, v141
	v_cvt_f32_f16_sdwa v145, v164 dst_sel:DWORD dst_unused:UNUSED_PAD src0_sel:WORD_1
	v_cvt_f32_f16_e32 v144, v164
	v_cvt_f32_f16_sdwa v146, v166 dst_sel:DWORD dst_unused:UNUSED_PAD src0_sel:WORD_1
	v_cvt_f32_f16_e32 v147, v166
	s_waitcnt lgkmcnt(0)
	v_add_f32_e32 v141, v141, v142
	ds_bpermute_b32 v142, v237, v140
	v_cvt_f32_f16_sdwa v164, v167 dst_sel:DWORD dst_unused:UNUSED_PAD src0_sel:WORD_1
	v_sub_f32_e32 v144, v144, v222
	v_sub_f32_e32 v145, v145, v222
	v_pk_mul_f32 v[144:145], v[222:223], v[144:145] op_sel:[1,0]
	s_waitcnt lgkmcnt(0)
	v_add_f32_e32 v142, v140, v142
	ds_bpermute_b32 v140, v237, v141
	v_pk_fma_f32 v[124:125], v[144:145], v[92:93], v[124:125]
	v_sub_f32_e32 v144, v147, v222
	v_sub_f32_e32 v145, v146, v222
	v_pk_mul_f32 v[144:145], v[222:223], v[144:145] op_sel:[1,0]
	s_waitcnt lgkmcnt(0)
	v_add_f32_e32 v143, v141, v140
	v_cvt_f32_f16_sdwa v141, v165 dst_sel:DWORD dst_unused:UNUSED_PAD src0_sel:WORD_1
	v_cvt_f32_f16_e32 v140, v165
	v_cvt_f32_f16_e32 v165, v167
	ds_read_b128 v[132:135], v236
	ds_read_b128 v[128:131], v236 offset:1152
	v_sub_f32_e32 v141, v141, v222
	v_sub_f32_e32 v140, v140, v222
	v_pk_mul_f32 v[140:141], v[222:223], v[140:141] op_sel:[1,0]
	v_pk_add_f32 v[118:119], v[118:119], v[198:199]
	v_pk_fma_f32 v[126:127], v[140:141], v[94:95], v[126:127]
	v_sub_f32_e32 v140, v165, v222
	v_sub_f32_e32 v141, v164, v222
	v_pk_mul_f32 v[140:141], v[222:223], v[140:141] op_sel:[1,0]
	v_pk_add_f32 v[116:117], v[116:117], v[200:201]
	v_pk_fma_f32 v[140:141], v[140:141], v[90:91], v[122:123]
	v_pk_fma_f32 v[122:123], v[144:145], v[88:89], v[120:121]
	v_cvt_f16_f32_e32 v144, v124
	v_cvt_f16_f32_e32 v145, v125
	v_cvt_pk_f16_f32 v120, v124, v125
	v_cvt_f16_f32_e32 v124, v126
	v_cvt_f16_f32_e32 v125, v127
	v_cvt_pk_f16_f32 v121, v126, v127
	v_cvt_f16_f32_e32 v126, v122
	v_cvt_f16_f32_e32 v127, v123
	v_cvt_f16_f32_e32 v146, v140
	v_cvt_f16_f32_e32 v147, v141
	v_cvt_pk_f16_f32 v122, v122, v123
	v_cvt_pk_f16_f32 v123, v140, v141
	ds_write_b128 v235, v[120:123]
	v_cvt_f32_f16_e32 v120, v144
	v_cvt_f32_f16_e32 v121, v145
	v_cvt_f32_f16_e32 v122, v124
	v_cvt_f32_f16_e32 v123, v125
	v_cvt_f32_f16_e32 v125, v126
	v_cvt_f32_f16_e32 v127, v127
	v_cvt_f32_f16_e32 v140, v146
	v_cvt_f32_f16_e32 v141, v147
	v_add_f32_e32 v120, v120, v121
	v_add_f32_e32 v122, v122, v123
	v_add_f32_e32 v120, v120, v122
	v_add_f32_e32 v122, v125, v127
	v_add_f32_e32 v125, v140, v141
	v_add_f32_e32 v122, v122, v125
	v_add_f32_e32 v120, v120, v122
	v_add_f32_e32 v125, 0, v120
	v_mul_f32_e32 v120, v121, v121
	v_mul_f32_e32 v121, v123, v123
	v_fma_mix_f32 v120, v144, v144, v120 op_sel_hi:[1,1,0]
	v_fma_mix_f32 v121, v124, v124, v121 op_sel_hi:[1,1,0]
	v_mul_f32_e32 v122, v141, v141
	v_add_f32_e32 v120, v120, v121
	v_mul_f32_e32 v121, v127, v127
	v_fma_mix_f32 v121, v126, v126, v121 op_sel_hi:[1,1,0]
	v_fma_mix_f32 v122, v146, v146, v122 op_sel_hi:[1,1,0]
	v_cvt_f32_f16_sdwa v123, v160 dst_sel:DWORD dst_unused:UNUSED_PAD src0_sel:WORD_1
	v_add_f32_e32 v121, v121, v122
	v_add_f32_e32 v124, v120, v121
	v_cvt_f32_f16_e32 v122, v160
	v_cvt_f32_f16_sdwa v121, v161 dst_sel:DWORD dst_unused:UNUSED_PAD src0_sel:WORD_1
	v_cvt_f32_f16_e32 v120, v161
	v_cvt_f32_f16_sdwa v126, v162 dst_sel:DWORD dst_unused:UNUSED_PAD src0_sel:WORD_1
	v_cvt_f32_f16_e32 v127, v162
	v_cvt_f32_f16_sdwa v140, v163 dst_sel:DWORD dst_unused:UNUSED_PAD src0_sel:WORD_1
	v_cvt_f32_f16_e32 v141, v163
	v_sub_f32_e32 v120, v120, v222
	v_sub_f32_e32 v121, v121, v222
	v_sub_f32_e32 v122, v122, v222
	v_sub_f32_e32 v123, v123, v222
	v_pk_mul_f32 v[122:123], v[222:223], v[122:123] op_sel:[1,0]
	v_pk_mul_f32 v[120:121], v[222:223], v[120:121] op_sel:[1,0]
	v_pk_fma_f32 v[116:117], v[122:123], v[80:81], v[116:117]
	v_pk_fma_f32 v[118:119], v[120:121], v[82:83], v[118:119]
	v_sub_f32_e32 v120, v141, v222
	v_sub_f32_e32 v121, v140, v222
	v_sub_f32_e32 v122, v127, v222
	v_sub_f32_e32 v123, v126, v222
	v_pk_add_f32 v[114:115], v[114:115], v[192:193]
	v_pk_add_f32 v[112:113], v[112:113], v[194:195]
	v_pk_mul_f32 v[122:123], v[222:223], v[122:123] op_sel:[1,0]
	v_pk_mul_f32 v[120:121], v[222:223], v[120:121] op_sel:[1,0]
	s_ashr_i32 s39, s38, 31
	v_pk_fma_f32 v[120:121], v[120:121], v[74:75], v[114:115]
	v_pk_fma_f32 v[114:115], v[122:123], v[72:73], v[112:113]
	v_cvt_f16_f32_e32 v122, v116
	v_cvt_f16_f32_e32 v123, v117
	v_cvt_pk_f16_f32 v112, v116, v117
	v_cvt_f16_f32_e32 v116, v118
	v_cvt_f16_f32_e32 v117, v119
	v_cvt_pk_f16_f32 v113, v118, v119
	v_cvt_f16_f32_e32 v118, v114
	v_cvt_f16_f32_e32 v119, v115
	v_cvt_f16_f32_e32 v126, v120
	v_cvt_f16_f32_e32 v127, v121
	v_cvt_pk_f16_f32 v114, v114, v115
	v_cvt_pk_f16_f32 v115, v120, v121
	ds_write_b128 v235, v[112:115] offset:64
	v_cvt_f32_f16_e32 v112, v122
	v_cvt_f32_f16_e32 v113, v123
	v_cvt_f32_f16_e32 v114, v116
	v_cvt_f32_f16_e32 v115, v117
	v_cvt_f32_f16_e32 v117, v118
	v_cvt_f32_f16_e32 v119, v119
	v_cvt_f32_f16_e32 v120, v126
	v_cvt_f32_f16_e32 v121, v127
	v_add_f32_e32 v112, v112, v113
	v_add_f32_e32 v114, v114, v115
	v_add_f32_e32 v112, v112, v114
	v_add_f32_e32 v114, v117, v119
	v_add_f32_e32 v117, v120, v121
	v_add_f32_e32 v114, v114, v117
	v_add_f32_e32 v112, v112, v114
	v_mul_f32_e32 v113, v113, v113
	v_mul_f32_e32 v114, v115, v115
	v_fma_mix_f32 v113, v122, v122, v113 op_sel_hi:[1,1,0]
	v_fma_mix_f32 v114, v116, v116, v114 op_sel_hi:[1,1,0]
	v_mul_f32_e32 v115, v121, v121
	v_add_f32_e32 v113, v113, v114
	v_mul_f32_e32 v114, v119, v119
	v_fma_mix_f32 v114, v118, v118, v114 op_sel_hi:[1,1,0]
	v_fma_mix_f32 v115, v126, v126, v115 op_sel_hi:[1,1,0]
	v_add_f32_e32 v112, v125, v112
	v_add_f32_e32 v114, v114, v115
	v_add_f32_e32 v113, v113, v114
	ds_bpermute_b32 v114, v221, v112
	v_add_f32_e32 v113, v124, v113
	ds_read_b128 v[160:163], v236
	ds_read_b128 v[164:167], v236 offset:1152
	s_waitcnt lgkmcnt(2)
	v_add_f32_e32 v112, v112, v114
	ds_bpermute_b32 v114, v221, v113
	s_waitcnt lgkmcnt(0)
	v_add_f32_e32 v113, v113, v114
	ds_bpermute_b32 v114, v237, v112
	s_waitcnt lgkmcnt(0)
	v_add_f32_e32 v146, v112, v114
	ds_bpermute_b32 v112, v237, v113
	s_waitcnt lgkmcnt(0)
	v_add_f32_e32 v147, v113, v112
	v_mov_b64_e32 v[112:113], s[28:29]
	v_mad_i64_i32 v[112:113], s[40:41], v220, s73, v[112:113]
	v_lshl_add_u64 v[140:141], s[38:39], 3, v[112:113]
	v_add_co_u32_e32 v112, vcc, s74, v214
	v_lshl_or_b32 v144, v238, 1, v230
	s_nop 0
	v_addc_co_u32_e32 v113, vcc, 0, v215, vcc
	global_load_dwordx4 v[124:127], v[112:113], off nt
	global_load_dwordx4 v[120:123], v[112:113], off offset:64 nt
	v_add_co_u32_e32 v112, vcc, s75, v214
	v_lshl_add_u64 v[140:141], v[140:141], 0, s[34:35]
	s_nop 0
	v_addc_co_u32_e32 v113, vcc, 0, v215, vcc
	global_load_dwordx4 v[116:119], v[112:113], off nt
	s_nop 0
	global_load_dwordx4 v[112:115], v[112:113], off offset:64 nt
	s_nop 0
	buffer_store_dwordx4 v[132:135], v144, s[24:27], 0 offen nt
	s_nop 1
	v_add_u32_e32 v132, 0x3000, v144
	buffer_store_dwordx4 v[128:131], v132, s[24:27], 0 offen nt
	global_store_dwordx2 v[140:141], v[142:143], off
	s_nop 0
	v_add_u32_e32 v128, 0x6000, v144
	buffer_store_dwordx4 v[160:163], v128, s[24:27], 0 offen nt
	v_add_u32_e32 v128, 0x9000, v144
	buffer_store_dwordx4 v[164:167], v128, s[24:27], 0 offen nt
	global_store_dwordx2 v[140:141], v[146:147], off offset:1536
	v_cvt_f32_f16_sdwa v131, v156 dst_sel:DWORD dst_unused:UNUSED_PAD src0_sel:WORD_1
	v_cvt_f32_f16_e32 v130, v156
	v_cvt_f32_f16_sdwa v129, v157 dst_sel:DWORD dst_unused:UNUSED_PAD src0_sel:WORD_1
	v_cvt_f32_f16_e32 v128, v157
	v_cvt_f32_f16_sdwa v132, v158 dst_sel:DWORD dst_unused:UNUSED_PAD src0_sel:WORD_1
	v_cvt_f32_f16_e32 v133, v158
	v_cvt_f32_f16_sdwa v134, v159 dst_sel:DWORD dst_unused:UNUSED_PAD src0_sel:WORD_1
	v_cvt_f32_f16_e32 v135, v159
	v_sub_f32_e32 v128, v128, v218
	v_sub_f32_e32 v129, v129, v218
	v_sub_f32_e32 v130, v130, v218
	v_sub_f32_e32 v131, v131, v218
	v_pk_add_f32 v[110:111], v[110:111], v[206:207]
	v_pk_add_f32 v[108:109], v[108:109], v[208:209]
	v_pk_mul_f32 v[130:131], v[218:219], v[130:131] op_sel:[1,0]
	v_pk_mul_f32 v[128:129], v[218:219], v[128:129] op_sel:[1,0]
	v_pk_fma_f32 v[108:109], v[130:131], v[92:93], v[108:109]
	v_pk_fma_f32 v[110:111], v[128:129], v[94:95], v[110:111]
	v_sub_f32_e32 v128, v135, v218
	v_sub_f32_e32 v129, v134, v218
	v_sub_f32_e32 v130, v133, v218
	v_sub_f32_e32 v131, v132, v218
	v_pk_add_f32 v[106:107], v[106:107], v[202:203]
	v_pk_add_f32 v[104:105], v[104:105], v[204:205]
	v_pk_mul_f32 v[130:131], v[218:219], v[130:131] op_sel:[1,0]
	v_pk_mul_f32 v[128:129], v[218:219], v[128:129] op_sel:[1,0]
	v_pk_add_f32 v[102:103], v[102:103], v[198:199]
	v_pk_fma_f32 v[128:129], v[128:129], v[90:91], v[106:107]
	v_pk_fma_f32 v[106:107], v[130:131], v[88:89], v[104:105]
	v_cvt_f16_f32_e32 v130, v108
	v_cvt_f16_f32_e32 v131, v109
	v_cvt_pk_f16_f32 v104, v108, v109
	v_cvt_f16_f32_e32 v108, v110
	v_cvt_f16_f32_e32 v109, v111
	v_cvt_pk_f16_f32 v105, v110, v111
	v_cvt_f16_f32_e32 v110, v106
	v_cvt_f16_f32_e32 v111, v107
	v_cvt_f16_f32_e32 v132, v128
	v_cvt_f16_f32_e32 v133, v129
	v_cvt_pk_f16_f32 v106, v106, v107
	v_cvt_pk_f16_f32 v107, v128, v129
	ds_write_b128 v235, v[104:107]
	v_cvt_f32_f16_e32 v104, v130
	v_cvt_f32_f16_e32 v105, v131
	v_cvt_f32_f16_e32 v106, v108
	v_cvt_f32_f16_e32 v107, v109
	v_cvt_f32_f16_e32 v109, v110
	v_cvt_f32_f16_e32 v111, v111
	v_cvt_f32_f16_e32 v128, v132
	v_cvt_f32_f16_e32 v129, v133
	v_add_f32_e32 v104, v104, v105
	v_add_f32_e32 v106, v106, v107
	v_add_f32_e32 v104, v104, v106
	v_add_f32_e32 v106, v109, v111
	v_add_f32_e32 v109, v128, v129
	v_add_f32_e32 v106, v106, v109
	v_add_f32_e32 v104, v104, v106
	v_add_f32_e32 v109, 0, v104
	v_mul_f32_e32 v104, v105, v105
	v_mul_f32_e32 v105, v107, v107
	v_fma_mix_f32 v104, v130, v130, v104 op_sel_hi:[1,1,0]
	v_fma_mix_f32 v105, v108, v108, v105 op_sel_hi:[1,1,0]
	v_mul_f32_e32 v106, v129, v129
	v_add_f32_e32 v104, v104, v105
	v_mul_f32_e32 v105, v111, v111
	v_fma_mix_f32 v105, v110, v110, v105 op_sel_hi:[1,1,0]
	v_fma_mix_f32 v106, v132, v132, v106 op_sel_hi:[1,1,0]
	v_cvt_f32_f16_sdwa v107, v152 dst_sel:DWORD dst_unused:UNUSED_PAD src0_sel:WORD_1
	v_add_f32_e32 v105, v105, v106
	v_add_f32_e32 v108, v104, v105
	v_cvt_f32_f16_e32 v106, v152
	v_cvt_f32_f16_sdwa v105, v153 dst_sel:DWORD dst_unused:UNUSED_PAD src0_sel:WORD_1
	v_cvt_f32_f16_e32 v104, v153
	v_cvt_f32_f16_sdwa v110, v154 dst_sel:DWORD dst_unused:UNUSED_PAD src0_sel:WORD_1
	v_cvt_f32_f16_e32 v111, v154
	v_cvt_f32_f16_sdwa v128, v155 dst_sel:DWORD dst_unused:UNUSED_PAD src0_sel:WORD_1
	v_cvt_f32_f16_e32 v129, v155
	v_sub_f32_e32 v104, v104, v218
	v_sub_f32_e32 v105, v105, v218
	v_sub_f32_e32 v106, v106, v218
	v_sub_f32_e32 v107, v107, v218
	v_pk_add_f32 v[100:101], v[100:101], v[200:201]
	v_pk_mul_f32 v[106:107], v[218:219], v[106:107] op_sel:[1,0]
	v_pk_mul_f32 v[104:105], v[218:219], v[104:105] op_sel:[1,0]
	v_pk_fma_f32 v[100:101], v[106:107], v[80:81], v[100:101]
	v_pk_fma_f32 v[102:103], v[104:105], v[82:83], v[102:103]
	v_sub_f32_e32 v104, v129, v218
	v_sub_f32_e32 v105, v128, v218
	v_sub_f32_e32 v106, v111, v218
	v_sub_f32_e32 v107, v110, v218
	v_pk_add_f32 v[98:99], v[98:99], v[192:193]
	v_pk_add_f32 v[96:97], v[96:97], v[194:195]
	v_pk_mul_f32 v[106:107], v[218:219], v[106:107] op_sel:[1,0]
	v_pk_mul_f32 v[104:105], v[218:219], v[104:105] op_sel:[1,0]
	v_pk_add_f32 v[86:87], v[86:87], v[206:207]
	v_pk_fma_f32 v[104:105], v[104:105], v[74:75], v[98:99]
	v_pk_fma_f32 v[98:99], v[106:107], v[72:73], v[96:97]
	v_cvt_f16_f32_e32 v106, v100
	v_cvt_f16_f32_e32 v107, v101
	v_cvt_pk_f16_f32 v96, v100, v101
	v_cvt_f16_f32_e32 v100, v102
	v_cvt_f16_f32_e32 v101, v103
	v_cvt_pk_f16_f32 v97, v102, v103
	v_cvt_f16_f32_e32 v103, v99
	v_cvt_f16_f32_e32 v111, v105
	v_cvt_f16_f32_e32 v102, v98
	v_cvt_f16_f32_e32 v110, v104
	v_cvt_pk_f16_f32 v98, v98, v99
	v_cvt_pk_f16_f32 v99, v104, v105
	v_cvt_f32_f16_e32 v105, v107
	v_cvt_f32_f16_e32 v107, v100
	v_cvt_f32_f16_e32 v101, v101
	v_cvt_f32_f16_e32 v103, v103
	v_cvt_f32_f16_e32 v104, v106
	v_cvt_f32_f16_e32 v111, v111
	v_cvt_f32_f16_e32 v128, v102
	v_cvt_f32_f16_e32 v129, v110
	v_add_f32_e32 v107, v107, v101
	v_mul_f32_e32 v101, v101, v101
	v_fma_mix_f32 v100, v100, v100, v101 op_sel_hi:[1,1,0]
	v_mul_f32_e32 v101, v103, v103
	v_add_f32_e32 v104, v104, v105
	v_mul_f32_e32 v105, v105, v105
	v_fma_mix_f32 v101, v102, v102, v101 op_sel_hi:[1,1,0]
	v_mul_f32_e32 v102, v111, v111
	v_add_f32_e32 v104, v104, v107
	v_add_f32_e32 v107, v128, v103
	v_add_f32_e32 v128, v129, v111
	v_fma_mix_f32 v105, v106, v106, v105 op_sel_hi:[1,1,0]
	v_fma_mix_f32 v102, v110, v110, v102 op_sel_hi:[1,1,0]
	v_add_f32_e32 v107, v107, v128
	v_add_f32_e32 v100, v105, v100
	v_add_f32_e32 v101, v101, v102
	v_add_f32_e32 v104, v104, v107
	v_add_f32_e32 v100, v100, v101
	v_add_f32_e32 v104, v109, v104
	v_add_f32_e32 v105, v108, v100
	ds_bpermute_b32 v106, v221, v104
	ds_bpermute_b32 v107, v221, v105
	v_cvt_f32_f16_sdwa v108, v150 dst_sel:DWORD dst_unused:UNUSED_PAD src0_sel:WORD_1
	v_cvt_f32_f16_e32 v109, v150
	v_cvt_f32_f16_sdwa v110, v151 dst_sel:DWORD dst_unused:UNUSED_PAD src0_sel:WORD_1
	s_waitcnt lgkmcnt(1)
	v_add_f32_e32 v128, v104, v106
	s_waitcnt lgkmcnt(0)
	v_add_f32_e32 v129, v105, v107
	v_cvt_f32_f16_sdwa v107, v148 dst_sel:DWORD dst_unused:UNUSED_PAD src0_sel:WORD_1
	v_cvt_f32_f16_e32 v106, v148
	v_cvt_f32_f16_sdwa v105, v149 dst_sel:DWORD dst_unused:UNUSED_PAD src0_sel:WORD_1
	v_cvt_f32_f16_e32 v104, v149
	v_cvt_f32_f16_e32 v111, v151
	v_sub_f32_e32 v106, v106, v216
	v_sub_f32_e32 v105, v105, v216
	v_sub_f32_e32 v104, v104, v216
	v_sub_f32_e32 v107, v107, v216
	v_pk_add_f32 v[84:85], v[84:85], v[208:209]
	v_pk_mul_f32 v[106:107], v[216:217], v[106:107] op_sel:[1,0]
	v_pk_mul_f32 v[104:105], v[216:217], v[104:105] op_sel:[1,0]
	v_pk_fma_f32 v[84:85], v[106:107], v[92:93], v[84:85]
	v_pk_fma_f32 v[86:87], v[104:105], v[94:95], v[86:87]
	v_sub_f32_e32 v104, v111, v216
	v_sub_f32_e32 v105, v110, v216
	v_sub_f32_e32 v106, v109, v216
	v_sub_f32_e32 v107, v108, v216
	v_pk_add_f32 v[78:79], v[78:79], v[202:203]
	v_pk_add_f32 v[76:77], v[76:77], v[204:205]
	v_pk_mul_f32 v[106:107], v[216:217], v[106:107] op_sel:[1,0]
	v_pk_mul_f32 v[104:105], v[216:217], v[104:105] op_sel:[1,0]
	ds_write_b128 v235, v[96:99] offset:64
	v_pk_fma_f32 v[104:105], v[104:105], v[90:91], v[78:79]
	v_pk_fma_f32 v[78:79], v[106:107], v[88:89], v[76:77]
	v_cvt_f16_f32_e32 v106, v84
	v_cvt_f16_f32_e32 v107, v85
	v_cvt_pk_f16_f32 v76, v84, v85
	v_cvt_f16_f32_e32 v84, v86
	v_cvt_f16_f32_e32 v85, v87
	v_cvt_pk_f16_f32 v77, v86, v87
	v_cvt_f16_f32_e32 v86, v78
	v_cvt_f16_f32_e32 v87, v79
	v_cvt_f16_f32_e32 v108, v104
	v_cvt_f16_f32_e32 v109, v105
	v_cvt_pk_f16_f32 v78, v78, v79
	v_cvt_pk_f16_f32 v79, v104, v105
	ds_read_b128 v[96:99], v236
	ds_read_b128 v[100:103], v236 offset:1152
	ds_write_b128 v235, v[76:79]
	v_cvt_f32_f16_e32 v76, v106
	v_cvt_f32_f16_e32 v77, v107
	v_cvt_f32_f16_e32 v78, v84
	v_cvt_f32_f16_e32 v79, v85
	v_cvt_f32_f16_e32 v85, v86
	v_cvt_f32_f16_e32 v87, v87
	v_cvt_f32_f16_e32 v104, v108
	v_cvt_f32_f16_e32 v105, v109
	v_add_f32_e32 v76, v76, v77
	v_add_f32_e32 v78, v78, v79
	v_add_f32_e32 v76, v76, v78
	v_add_f32_e32 v78, v85, v87
	v_add_f32_e32 v85, v104, v105
	v_add_f32_e32 v78, v78, v85
	v_add_f32_e32 v76, v76, v78
	v_add_f32_e32 v85, 0, v76
	v_mul_f32_e32 v76, v77, v77
	v_mul_f32_e32 v77, v79, v79
	v_fma_mix_f32 v76, v106, v106, v76 op_sel_hi:[1,1,0]
	v_fma_mix_f32 v77, v84, v84, v77 op_sel_hi:[1,1,0]
	v_mul_f32_e32 v78, v105, v105
	v_add_f32_e32 v76, v76, v77
	v_mul_f32_e32 v77, v87, v87
	v_fma_mix_f32 v77, v86, v86, v77 op_sel_hi:[1,1,0]
	v_fma_mix_f32 v78, v108, v108, v78 op_sel_hi:[1,1,0]
	v_cvt_f32_f16_sdwa v79, v136 dst_sel:DWORD dst_unused:UNUSED_PAD src0_sel:WORD_1
	v_add_f32_e32 v77, v77, v78
	v_add_f32_e32 v84, v76, v77
	v_cvt_f32_f16_e32 v78, v136
	v_cvt_f32_f16_sdwa v77, v137 dst_sel:DWORD dst_unused:UNUSED_PAD src0_sel:WORD_1
	v_cvt_f32_f16_e32 v76, v137
	v_cvt_f32_f16_sdwa v86, v138 dst_sel:DWORD dst_unused:UNUSED_PAD src0_sel:WORD_1
	v_cvt_f32_f16_e32 v87, v138
	v_cvt_f32_f16_sdwa v104, v139 dst_sel:DWORD dst_unused:UNUSED_PAD src0_sel:WORD_1
	v_cvt_f32_f16_e32 v105, v139
	v_sub_f32_e32 v76, v76, v216
	v_sub_f32_e32 v77, v77, v216
	v_sub_f32_e32 v78, v78, v216
	v_sub_f32_e32 v79, v79, v216
	v_pk_add_f32 v[70:71], v[70:71], v[198:199]
	v_pk_add_f32 v[68:69], v[68:69], v[200:201]
	v_pk_mul_f32 v[78:79], v[216:217], v[78:79] op_sel:[1,0]
	v_pk_mul_f32 v[76:77], v[216:217], v[76:77] op_sel:[1,0]
	v_pk_fma_f32 v[68:69], v[78:79], v[80:81], v[68:69]
	v_pk_fma_f32 v[70:71], v[76:77], v[82:83], v[70:71]
	v_sub_f32_e32 v76, v105, v216
	v_sub_f32_e32 v77, v104, v216
	v_sub_f32_e32 v78, v87, v216
	v_sub_f32_e32 v79, v86, v216
	v_pk_add_f32 v[66:67], v[66:67], v[192:193]
	v_pk_add_f32 v[64:65], v[64:65], v[194:195]
	v_pk_mul_f32 v[78:79], v[216:217], v[78:79] op_sel:[1,0]
	v_pk_mul_f32 v[76:77], v[216:217], v[76:77] op_sel:[1,0]
	ds_bpermute_b32 v130, v237, v128
	v_pk_fma_f32 v[76:77], v[76:77], v[74:75], v[66:67]
	v_pk_fma_f32 v[66:67], v[78:79], v[72:73], v[64:65]
	v_cvt_f16_f32_e32 v78, v68
	v_cvt_f16_f32_e32 v79, v69
	v_cvt_pk_f16_f32 v64, v68, v69
	v_cvt_f16_f32_e32 v68, v70
	v_cvt_f16_f32_e32 v69, v71
	v_cvt_pk_f16_f32 v65, v70, v71
	v_cvt_f16_f32_e32 v71, v67
	v_cvt_f16_f32_e32 v87, v77
	v_cvt_f16_f32_e32 v70, v66
	v_cvt_f16_f32_e32 v86, v76
	v_cvt_f32_f16_e32 v105, v68
	v_cvt_f32_f16_e32 v69, v69
	v_cvt_f32_f16_e32 v71, v71
	v_cvt_f32_f16_e32 v104, v78
	v_cvt_f32_f16_e32 v79, v79
	v_cvt_f32_f16_e32 v87, v87
	v_cvt_f32_f16_e32 v106, v70
	v_cvt_f32_f16_e32 v107, v86
	v_add_f32_e32 v105, v105, v69
	v_mul_f32_e32 v69, v69, v69
	v_fma_mix_f32 v68, v68, v68, v69 op_sel_hi:[1,1,0]
	v_mul_f32_e32 v69, v71, v71
	v_add_f32_e32 v104, v104, v79
	v_mul_f32_e32 v79, v79, v79
	v_fma_mix_f32 v69, v70, v70, v69 op_sel_hi:[1,1,0]
	v_mul_f32_e32 v70, v87, v87
	v_add_f32_e32 v104, v104, v105
	v_add_f32_e32 v105, v106, v71
	v_add_f32_e32 v106, v107, v87
	v_fma_mix_f32 v78, v78, v78, v79 op_sel_hi:[1,1,0]
	v_fma_mix_f32 v70, v86, v86, v70 op_sel_hi:[1,1,0]
	v_add_f32_e32 v105, v105, v106
	v_add_f32_e32 v68, v78, v68
	v_add_f32_e32 v69, v69, v70
	v_add_f32_e32 v104, v104, v105
	v_add_f32_e32 v68, v68, v69
	v_add_f32_e32 v85, v85, v104
	v_add_f32_e32 v68, v84, v68
	ds_bpermute_b32 v69, v221, v85
	ds_bpermute_b32 v70, v221, v68
	v_cvt_pk_f16_f32 v66, v66, v67
	v_cvt_pk_f16_f32 v67, v76, v77
	ds_write_b128 v235, v[64:67] offset:64
	s_waitcnt lgkmcnt(2)
	v_add_f32_e32 v64, v85, v69
	s_waitcnt lgkmcnt(1)
	v_add_f32_e32 v65, v68, v70
	ds_bpermute_b32 v131, v237, v129
	ds_bpermute_b32 v66, v237, v64
	ds_bpermute_b32 v67, v237, v65
	ds_read_b128 v[104:107], v236
	ds_read_b128 v[108:111], v236 offset:1152
	v_add_f32_e32 v128, v128, v130
	s_waitcnt lgkmcnt(4)
	v_add_f32_e32 v129, v129, v131
	s_waitcnt lgkmcnt(3)
	v_add_f32_e32 v130, v64, v66
	s_waitcnt lgkmcnt(2)
	v_add_f32_e32 v131, v65, v67
	v_add_co_u32_e32 v64, vcc, s77, v214
	s_nop 1
	v_addc_co_u32_e32 v65, vcc, 0, v215, vcc
	global_load_dwordx4 v[84:87], v[64:65], off nt
	global_load_dwordx4 v[76:79], v[64:65], off offset:64 nt
	v_add_co_u32_e32 v64, vcc, s78, v214
	s_nop 1
	v_addc_co_u32_e32 v65, vcc, 0, v215, vcc
	global_load_dwordx4 v[68:71], v[64:65], off nt
	s_nop 0
	global_load_dwordx4 v[64:67], v[64:65], off offset:64 nt
	v_add_u32_e32 v132, 0xc000, v144
	buffer_store_dwordx4 v[96:99], v132, s[24:27], 0 offen nt
	s_nop 1
	v_add_u32_e32 v96, 0xf000, v144
	buffer_store_dwordx4 v[100:103], v96, s[24:27], 0 offen nt
	v_add_u32_e32 v96, 0x12000, v144
	global_store_dwordx2 v[140:141], v[128:129], off offset:3072
	s_waitcnt lgkmcnt(1)
	buffer_store_dwordx4 v[104:107], v96, s[24:27], 0 offen nt
	v_add_u32_e32 v96, 0x15000, v144
	s_waitcnt lgkmcnt(0)
	buffer_store_dwordx4 v[108:111], v96, s[24:27], 0 offen nt
	v_add_co_u32_e32 v96, vcc, s79, v140
	s_nop 1
	v_addc_co_u32_e32 v97, vcc, 0, v141, vcc
	global_store_dwordx2 v[96:97], v[130:131], off offset:512
	s_waitcnt vmcnt(19)
	v_cvt_f32_f16_sdwa v99, v124 dst_sel:DWORD dst_unused:UNUSED_PAD src0_sel:WORD_1
	v_cvt_f32_f16_e32 v98, v124
	v_cvt_f32_f16_sdwa v97, v125 dst_sel:DWORD dst_unused:UNUSED_PAD src0_sel:WORD_1
	v_cvt_f32_f16_e32 v96, v125
	v_cvt_f32_f16_sdwa v100, v126 dst_sel:DWORD dst_unused:UNUSED_PAD src0_sel:WORD_1
	v_cvt_f32_f16_e32 v101, v126
	v_cvt_f32_f16_sdwa v102, v127 dst_sel:DWORD dst_unused:UNUSED_PAD src0_sel:WORD_1
	v_cvt_f32_f16_e32 v103, v127
	v_sub_f32_e32 v96, v96, v212
	v_sub_f32_e32 v97, v97, v212
	v_sub_f32_e32 v98, v98, v212
	v_sub_f32_e32 v99, v99, v212
	v_pk_add_f32 v[62:63], v[62:63], v[206:207]
	v_pk_add_f32 v[60:61], v[60:61], v[208:209]
	v_pk_mul_f32 v[98:99], v[212:213], v[98:99] op_sel:[1,0]
	v_pk_mul_f32 v[96:97], v[212:213], v[96:97] op_sel:[1,0]
	v_pk_fma_f32 v[60:61], v[92:93], v[98:99], v[60:61]
	v_pk_fma_f32 v[62:63], v[94:95], v[96:97], v[62:63]
	v_sub_f32_e32 v96, v103, v212
	v_sub_f32_e32 v97, v102, v212
	v_sub_f32_e32 v98, v101, v212
	v_sub_f32_e32 v99, v100, v212
	v_pk_add_f32 v[58:59], v[58:59], v[202:203]
	v_pk_add_f32 v[56:57], v[56:57], v[204:205]
	v_pk_mul_f32 v[98:99], v[212:213], v[98:99] op_sel:[1,0]
	v_pk_mul_f32 v[96:97], v[212:213], v[96:97] op_sel:[1,0]
	v_pk_add_f32 v[54:55], v[54:55], v[198:199]
	v_pk_fma_f32 v[96:97], v[90:91], v[96:97], v[58:59]
	v_pk_fma_f32 v[58:59], v[88:89], v[98:99], v[56:57]
	v_cvt_f16_f32_e32 v98, v60
	v_cvt_f16_f32_e32 v99, v61
	v_cvt_pk_f16_f32 v56, v60, v61
	v_cvt_f16_f32_e32 v60, v62
	v_cvt_f16_f32_e32 v61, v63
	v_cvt_pk_f16_f32 v57, v62, v63
	v_cvt_f16_f32_e32 v62, v58
	v_cvt_f16_f32_e32 v63, v59
	v_cvt_f16_f32_e32 v100, v96
	v_cvt_f16_f32_e32 v101, v97
	v_cvt_pk_f16_f32 v58, v58, v59
	v_cvt_pk_f16_f32 v59, v96, v97
	ds_write_b128 v235, v[56:59]
	v_cvt_f32_f16_e32 v56, v98
	v_cvt_f32_f16_e32 v57, v99
	v_cvt_f32_f16_e32 v58, v60
	v_cvt_f32_f16_e32 v59, v61
	v_cvt_f32_f16_e32 v61, v62
	v_cvt_f32_f16_e32 v63, v63
	v_cvt_f32_f16_e32 v96, v100
	v_cvt_f32_f16_e32 v97, v101
	v_add_f32_e32 v56, v56, v57
	v_add_f32_e32 v58, v58, v59
	v_add_f32_e32 v56, v56, v58
	v_add_f32_e32 v58, v61, v63
	v_add_f32_e32 v61, v96, v97
	v_add_f32_e32 v58, v58, v61
	v_add_f32_e32 v56, v56, v58
	v_add_f32_e32 v61, 0, v56
	v_mul_f32_e32 v56, v57, v57
	v_mul_f32_e32 v57, v59, v59
	v_fma_mix_f32 v56, v98, v98, v56 op_sel_hi:[1,1,0]
	v_fma_mix_f32 v57, v60, v60, v57 op_sel_hi:[1,1,0]
	v_mul_f32_e32 v58, v97, v97
	v_add_f32_e32 v56, v56, v57
	v_mul_f32_e32 v57, v63, v63
	v_fma_mix_f32 v57, v62, v62, v57 op_sel_hi:[1,1,0]
	v_fma_mix_f32 v58, v100, v100, v58 op_sel_hi:[1,1,0]
	s_waitcnt vmcnt(18)
	v_cvt_f32_f16_sdwa v59, v120 dst_sel:DWORD dst_unused:UNUSED_PAD src0_sel:WORD_1
	v_add_f32_e32 v57, v57, v58
	v_add_f32_e32 v60, v56, v57
	v_cvt_f32_f16_e32 v58, v120
	v_cvt_f32_f16_sdwa v57, v121 dst_sel:DWORD dst_unused:UNUSED_PAD src0_sel:WORD_1
	v_cvt_f32_f16_e32 v56, v121
	v_cvt_f32_f16_sdwa v62, v122 dst_sel:DWORD dst_unused:UNUSED_PAD src0_sel:WORD_1
	v_cvt_f32_f16_e32 v63, v122
	v_cvt_f32_f16_sdwa v96, v123 dst_sel:DWORD dst_unused:UNUSED_PAD src0_sel:WORD_1
	v_cvt_f32_f16_e32 v97, v123
	v_sub_f32_e32 v56, v56, v212
	v_sub_f32_e32 v57, v57, v212
	v_sub_f32_e32 v58, v58, v212
	v_sub_f32_e32 v59, v59, v212
	v_pk_add_f32 v[52:53], v[52:53], v[200:201]
	v_pk_mul_f32 v[58:59], v[212:213], v[58:59] op_sel:[1,0]
	v_pk_mul_f32 v[56:57], v[212:213], v[56:57] op_sel:[1,0]
	v_pk_fma_f32 v[52:53], v[80:81], v[58:59], v[52:53]
	v_pk_fma_f32 v[54:55], v[82:83], v[56:57], v[54:55]
	v_sub_f32_e32 v56, v97, v212
	v_sub_f32_e32 v57, v96, v212
	v_sub_f32_e32 v58, v63, v212
	v_sub_f32_e32 v59, v62, v212
	v_pk_add_f32 v[50:51], v[50:51], v[192:193]
	v_pk_add_f32 v[48:49], v[48:49], v[194:195]
	v_pk_mul_f32 v[58:59], v[212:213], v[58:59] op_sel:[1,0]
	v_pk_mul_f32 v[56:57], v[212:213], v[56:57] op_sel:[1,0]
	s_waitcnt vmcnt(17)
	v_cvt_f32_f16_sdwa v98, v119 dst_sel:DWORD dst_unused:UNUSED_PAD src0_sel:WORD_1
	v_pk_fma_f32 v[56:57], v[74:75], v[56:57], v[50:51]
	v_pk_fma_f32 v[50:51], v[72:73], v[58:59], v[48:49]
	v_cvt_f16_f32_e32 v58, v52
	v_cvt_f16_f32_e32 v59, v53
	v_cvt_pk_f16_f32 v48, v52, v53
	v_cvt_f16_f32_e32 v52, v54
	v_cvt_f16_f32_e32 v53, v55
	v_cvt_pk_f16_f32 v49, v54, v55
	v_cvt_f16_f32_e32 v55, v51
	v_cvt_f16_f32_e32 v63, v57
	v_cvt_f16_f32_e32 v54, v50
	v_cvt_f16_f32_e32 v62, v56
	v_cvt_pk_f16_f32 v50, v50, v51
	v_cvt_pk_f16_f32 v51, v56, v57
	v_cvt_f32_f16_e32 v57, v59
	v_cvt_f32_f16_e32 v59, v52
	v_cvt_f32_f16_e32 v53, v53
	v_cvt_f32_f16_e32 v55, v55
	v_cvt_f32_f16_e32 v56, v58
	v_cvt_f32_f16_e32 v63, v63
	v_cvt_f32_f16_e32 v96, v54
	v_cvt_f32_f16_e32 v97, v62
	v_add_f32_e32 v59, v59, v53
	v_mul_f32_e32 v53, v53, v53
	v_fma_mix_f32 v52, v52, v52, v53 op_sel_hi:[1,1,0]
	v_mul_f32_e32 v53, v55, v55
	v_add_f32_e32 v56, v56, v57
	v_mul_f32_e32 v57, v57, v57
	v_fma_mix_f32 v53, v54, v54, v53 op_sel_hi:[1,1,0]
	v_mul_f32_e32 v54, v63, v63
	v_add_f32_e32 v56, v56, v59
	v_add_f32_e32 v59, v96, v55
	v_add_f32_e32 v96, v97, v63
	v_fma_mix_f32 v57, v58, v58, v57 op_sel_hi:[1,1,0]
	v_fma_mix_f32 v54, v62, v62, v54 op_sel_hi:[1,1,0]
	v_add_f32_e32 v59, v59, v96
	v_add_f32_e32 v52, v57, v52
	v_add_f32_e32 v53, v53, v54
	v_add_f32_e32 v56, v56, v59
	v_add_f32_e32 v52, v52, v53
	v_add_f32_e32 v56, v61, v56
	v_add_f32_e32 v57, v60, v52
	ds_bpermute_b32 v58, v221, v56
	ds_bpermute_b32 v59, v221, v57
	v_cvt_f32_f16_sdwa v96, v118 dst_sel:DWORD dst_unused:UNUSED_PAD src0_sel:WORD_1
	v_cvt_f32_f16_e32 v97, v118
	v_cvt_f32_f16_e32 v99, v119
	s_waitcnt lgkmcnt(1)
	v_add_f32_e32 v60, v56, v58
	s_waitcnt lgkmcnt(0)
	v_add_f32_e32 v61, v57, v59
	v_cvt_f32_f16_sdwa v59, v116 dst_sel:DWORD dst_unused:UNUSED_PAD src0_sel:WORD_1
	v_cvt_f32_f16_e32 v58, v116
	v_cvt_f32_f16_sdwa v57, v117 dst_sel:DWORD dst_unused:UNUSED_PAD src0_sel:WORD_1
	v_cvt_f32_f16_e32 v56, v117
	v_sub_f32_e32 v59, v59, v210
	v_sub_f32_e32 v58, v58, v210
	v_sub_f32_e32 v57, v57, v210
	v_sub_f32_e32 v56, v56, v210
	v_pk_add_f32 v[46:47], v[46:47], v[206:207]
	v_pk_add_f32 v[44:45], v[44:45], v[208:209]
	v_pk_mul_f32 v[58:59], v[210:211], v[58:59] op_sel:[1,0]
	v_pk_mul_f32 v[56:57], v[210:211], v[56:57] op_sel:[1,0]
	v_pk_fma_f32 v[44:45], v[92:93], v[58:59], v[44:45]
	v_pk_fma_f32 v[46:47], v[94:95], v[56:57], v[46:47]
	v_sub_f32_e32 v56, v99, v210
	v_sub_f32_e32 v57, v98, v210
	v_sub_f32_e32 v58, v97, v210
	v_sub_f32_e32 v59, v96, v210
	v_pk_add_f32 v[42:43], v[42:43], v[202:203]
	v_pk_add_f32 v[40:41], v[40:41], v[204:205]
	v_pk_mul_f32 v[58:59], v[210:211], v[58:59] op_sel:[1,0]
	v_pk_mul_f32 v[56:57], v[210:211], v[56:57] op_sel:[1,0]
	ds_write_b128 v235, v[48:51] offset:64
	v_pk_fma_f32 v[56:57], v[90:91], v[56:57], v[42:43]
	v_pk_fma_f32 v[42:43], v[88:89], v[58:59], v[40:41]
	v_cvt_f16_f32_e32 v58, v44
	v_cvt_f16_f32_e32 v59, v45
	v_cvt_pk_f16_f32 v40, v44, v45
	v_cvt_f16_f32_e32 v44, v46
	v_cvt_f16_f32_e32 v45, v47
	v_cvt_pk_f16_f32 v41, v46, v47
	v_cvt_f16_f32_e32 v46, v42
	v_cvt_f16_f32_e32 v47, v43
	v_cvt_f16_f32_e32 v96, v56
	v_cvt_f16_f32_e32 v97, v57
	v_cvt_pk_f16_f32 v42, v42, v43
	v_cvt_pk_f16_f32 v43, v56, v57
	ds_read_b128 v[48:51], v236
	ds_read_b128 v[52:55], v236 offset:1152
	ds_write_b128 v235, v[40:43]
	v_cvt_f32_f16_e32 v40, v58
	v_cvt_f32_f16_e32 v41, v59
	v_cvt_f32_f16_e32 v42, v44
	v_cvt_f32_f16_e32 v43, v45
	v_cvt_f32_f16_e32 v45, v46
	v_cvt_f32_f16_e32 v47, v47
	v_cvt_f32_f16_e32 v56, v96
	v_cvt_f32_f16_e32 v57, v97
	v_add_f32_e32 v40, v40, v41
	v_add_f32_e32 v42, v42, v43
	v_add_f32_e32 v40, v40, v42
	v_add_f32_e32 v42, v45, v47
	v_add_f32_e32 v45, v56, v57
	v_add_f32_e32 v42, v42, v45
	v_add_f32_e32 v40, v40, v42
	v_add_f32_e32 v45, 0, v40
	v_mul_f32_e32 v40, v41, v41
	v_mul_f32_e32 v41, v43, v43
	v_fma_mix_f32 v40, v58, v58, v40 op_sel_hi:[1,1,0]
	v_fma_mix_f32 v41, v44, v44, v41 op_sel_hi:[1,1,0]
	v_mul_f32_e32 v42, v57, v57
	v_add_f32_e32 v40, v40, v41
	v_mul_f32_e32 v41, v47, v47
	v_fma_mix_f32 v41, v46, v46, v41 op_sel_hi:[1,1,0]
	v_fma_mix_f32 v42, v96, v96, v42 op_sel_hi:[1,1,0]
	s_waitcnt vmcnt(16)
	v_cvt_f32_f16_sdwa v43, v112 dst_sel:DWORD dst_unused:UNUSED_PAD src0_sel:WORD_1
	v_add_f32_e32 v41, v41, v42
	v_add_f32_e32 v44, v40, v41
	v_cvt_f32_f16_e32 v42, v112
	v_cvt_f32_f16_sdwa v41, v113 dst_sel:DWORD dst_unused:UNUSED_PAD src0_sel:WORD_1
	v_cvt_f32_f16_e32 v40, v113
	v_cvt_f32_f16_sdwa v46, v114 dst_sel:DWORD dst_unused:UNUSED_PAD src0_sel:WORD_1
	v_cvt_f32_f16_e32 v47, v114
	v_cvt_f32_f16_sdwa v56, v115 dst_sel:DWORD dst_unused:UNUSED_PAD src0_sel:WORD_1
	v_cvt_f32_f16_e32 v57, v115
	v_sub_f32_e32 v40, v40, v210
	v_sub_f32_e32 v41, v41, v210
	v_sub_f32_e32 v42, v42, v210
	v_sub_f32_e32 v43, v43, v210
	v_pk_add_f32 v[38:39], v[38:39], v[198:199]
	v_pk_add_f32 v[36:37], v[36:37], v[200:201]
	v_pk_mul_f32 v[42:43], v[210:211], v[42:43] op_sel:[1,0]
	v_pk_mul_f32 v[40:41], v[210:211], v[40:41] op_sel:[1,0]
	v_pk_fma_f32 v[36:37], v[80:81], v[42:43], v[36:37]
	v_pk_fma_f32 v[38:39], v[82:83], v[40:41], v[38:39]
	v_sub_f32_e32 v40, v57, v210
	v_sub_f32_e32 v41, v56, v210
	v_sub_f32_e32 v42, v47, v210
	v_sub_f32_e32 v43, v46, v210
	v_pk_add_f32 v[34:35], v[34:35], v[192:193]
	v_pk_add_f32 v[32:33], v[32:33], v[194:195]
	v_pk_mul_f32 v[42:43], v[210:211], v[42:43] op_sel:[1,0]
	v_pk_mul_f32 v[40:41], v[210:211], v[40:41] op_sel:[1,0]
	ds_bpermute_b32 v62, v237, v60
	v_pk_fma_f32 v[40:41], v[74:75], v[40:41], v[34:35]
	v_pk_fma_f32 v[34:35], v[72:73], v[42:43], v[32:33]
	v_cvt_f16_f32_e32 v42, v36
	v_cvt_f16_f32_e32 v43, v37
	v_cvt_pk_f16_f32 v32, v36, v37
	v_cvt_f16_f32_e32 v36, v38
	v_cvt_f16_f32_e32 v37, v39
	v_cvt_pk_f16_f32 v33, v38, v39
	v_cvt_f16_f32_e32 v39, v35
	v_cvt_f16_f32_e32 v47, v41
	v_cvt_f16_f32_e32 v38, v34
	v_cvt_f16_f32_e32 v46, v40
	v_cvt_f32_f16_e32 v57, v36
	v_cvt_f32_f16_e32 v37, v37
	v_cvt_f32_f16_e32 v39, v39
	v_cvt_f32_f16_e32 v56, v42
	v_cvt_f32_f16_e32 v43, v43
	v_cvt_f32_f16_e32 v47, v47
	v_cvt_f32_f16_e32 v58, v38
	v_cvt_f32_f16_e32 v59, v46
	v_add_f32_e32 v57, v57, v37
	v_mul_f32_e32 v37, v37, v37
	v_fma_mix_f32 v36, v36, v36, v37 op_sel_hi:[1,1,0]
	v_mul_f32_e32 v37, v39, v39
	v_add_f32_e32 v56, v56, v43
	v_mul_f32_e32 v43, v43, v43
	v_fma_mix_f32 v37, v38, v38, v37 op_sel_hi:[1,1,0]
	v_mul_f32_e32 v38, v47, v47
	v_add_f32_e32 v56, v56, v57
	v_add_f32_e32 v57, v58, v39
	v_add_f32_e32 v58, v59, v47
	v_fma_mix_f32 v42, v42, v42, v43 op_sel_hi:[1,1,0]
	v_fma_mix_f32 v38, v46, v46, v38 op_sel_hi:[1,1,0]
	v_add_f32_e32 v57, v57, v58
	v_add_f32_e32 v36, v42, v36
	v_add_f32_e32 v37, v37, v38
	v_add_f32_e32 v56, v56, v57
	v_add_f32_e32 v36, v36, v37
	v_add_f32_e32 v45, v45, v56
	v_add_f32_e32 v36, v44, v36
	ds_bpermute_b32 v37, v221, v45
	ds_bpermute_b32 v38, v221, v36
	v_cvt_pk_f16_f32 v34, v34, v35
	v_cvt_pk_f16_f32 v35, v40, v41
	ds_write_b128 v235, v[32:35] offset:64
	s_waitcnt lgkmcnt(2)
	v_add_f32_e32 v32, v45, v37
	s_waitcnt lgkmcnt(1)
	v_add_f32_e32 v33, v36, v38
	ds_bpermute_b32 v63, v237, v61
	ds_bpermute_b32 v44, v237, v32
	ds_bpermute_b32 v45, v237, v33
	ds_read_b128 v[34:37], v236
	ds_read_b128 v[38:41], v236 offset:1152
	v_add_f32_e32 v42, v60, v62
	s_waitcnt lgkmcnt(4)
	v_add_f32_e32 v43, v61, v63
	s_waitcnt lgkmcnt(3)
	v_add_f32_e32 v44, v32, v44
	s_waitcnt lgkmcnt(2)
	v_add_f32_e32 v45, v33, v45
	v_add_u32_e32 v32, 0x30000, v144
	buffer_store_dwordx4 v[48:51], v32, s[24:27], 0 offen nt
	v_add_u32_e32 v32, 0x33000, v144
	buffer_store_dwordx4 v[52:55], v32, s[24:27], 0 offen nt
	v_add_co_u32_e32 v32, vcc, s76, v140
	s_nop 1
	v_addc_co_u32_e32 v33, vcc, 0, v141, vcc
	global_store_dwordx2 v[32:33], v[42:43], off
	v_add_u32_e32 v42, 0x36000, v144
	s_waitcnt lgkmcnt(1)
	buffer_store_dwordx4 v[34:37], v42, s[24:27], 0 offen nt
	s_nop 1
	v_add_u32_e32 v34, 0x39000, v144
	s_waitcnt lgkmcnt(0)
	buffer_store_dwordx4 v[38:41], v34, s[24:27], 0 offen nt
	global_store_dwordx2 v[32:33], v[44:45], off offset:1536
	s_waitcnt vmcnt(15)
	v_cvt_f32_f16_sdwa v37, v84 dst_sel:DWORD dst_unused:UNUSED_PAD src0_sel:WORD_1
	v_cvt_f32_f16_e32 v36, v84
	v_cvt_f32_f16_sdwa v35, v85 dst_sel:DWORD dst_unused:UNUSED_PAD src0_sel:WORD_1
	v_cvt_f32_f16_e32 v34, v85
	v_cvt_f32_f16_sdwa v38, v86 dst_sel:DWORD dst_unused:UNUSED_PAD src0_sel:WORD_1
	v_cvt_f32_f16_e32 v39, v86
	v_cvt_f32_f16_sdwa v40, v87 dst_sel:DWORD dst_unused:UNUSED_PAD src0_sel:WORD_1
	v_cvt_f32_f16_e32 v41, v87
	v_sub_f32_e32 v34, v34, v196
	v_sub_f32_e32 v35, v35, v196
	v_sub_f32_e32 v36, v36, v196
	v_sub_f32_e32 v37, v37, v196
	v_pk_add_f32 v[30:31], v[30:31], v[206:207]
	v_pk_add_f32 v[28:29], v[28:29], v[208:209]
	v_pk_mul_f32 v[36:37], v[196:197], v[36:37] op_sel:[1,0]
	v_pk_mul_f32 v[34:35], v[196:197], v[34:35] op_sel:[1,0]
	v_pk_fma_f32 v[28:29], v[92:93], v[36:37], v[28:29]
	v_pk_fma_f32 v[30:31], v[94:95], v[34:35], v[30:31]
	v_sub_f32_e32 v34, v41, v196
	v_sub_f32_e32 v35, v40, v196
	v_sub_f32_e32 v36, v39, v196
	v_sub_f32_e32 v37, v38, v196
	v_pk_add_f32 v[26:27], v[26:27], v[202:203]
	v_pk_add_f32 v[24:25], v[24:25], v[204:205]
	v_pk_mul_f32 v[36:37], v[196:197], v[36:37] op_sel:[1,0]
	v_pk_mul_f32 v[34:35], v[196:197], v[34:35] op_sel:[1,0]
	v_pk_add_f32 v[22:23], v[22:23], v[198:199]
	v_pk_fma_f32 v[34:35], v[90:91], v[34:35], v[26:27]
	v_pk_fma_f32 v[26:27], v[88:89], v[36:37], v[24:25]
	v_cvt_f16_f32_e32 v36, v28
	v_cvt_f16_f32_e32 v37, v29
	v_cvt_pk_f16_f32 v24, v28, v29
	v_cvt_f16_f32_e32 v28, v30
	v_cvt_f16_f32_e32 v29, v31
	v_cvt_pk_f16_f32 v25, v30, v31
	v_cvt_f16_f32_e32 v30, v26
	v_cvt_f16_f32_e32 v31, v27
	v_cvt_f16_f32_e32 v38, v34
	v_cvt_f16_f32_e32 v39, v35
	v_cvt_pk_f16_f32 v26, v26, v27
	v_cvt_pk_f16_f32 v27, v34, v35
	ds_write_b128 v235, v[24:27]
	v_cvt_f32_f16_e32 v24, v36
	v_cvt_f32_f16_e32 v25, v37
	v_cvt_f32_f16_e32 v26, v28
	v_cvt_f32_f16_e32 v27, v29
	v_cvt_f32_f16_e32 v29, v30
	v_cvt_f32_f16_e32 v31, v31
	v_cvt_f32_f16_e32 v34, v38
	v_cvt_f32_f16_e32 v35, v39
	v_add_f32_e32 v24, v24, v25
	v_add_f32_e32 v26, v26, v27
	v_add_f32_e32 v24, v24, v26
	v_add_f32_e32 v26, v29, v31
	v_add_f32_e32 v29, v34, v35
	v_add_f32_e32 v26, v26, v29
	v_add_f32_e32 v24, v24, v26
	v_add_f32_e32 v29, 0, v24
	v_mul_f32_e32 v24, v25, v25
	v_mul_f32_e32 v25, v27, v27
	v_fma_mix_f32 v24, v36, v36, v24 op_sel_hi:[1,1,0]
	v_fma_mix_f32 v25, v28, v28, v25 op_sel_hi:[1,1,0]
	v_mul_f32_e32 v26, v35, v35
	v_add_f32_e32 v24, v24, v25
	v_mul_f32_e32 v25, v31, v31
	v_fma_mix_f32 v25, v30, v30, v25 op_sel_hi:[1,1,0]
	v_fma_mix_f32 v26, v38, v38, v26 op_sel_hi:[1,1,0]
	s_waitcnt vmcnt(14)
	v_cvt_f32_f16_sdwa v27, v76 dst_sel:DWORD dst_unused:UNUSED_PAD src0_sel:WORD_1
	v_add_f32_e32 v25, v25, v26
	v_add_f32_e32 v28, v24, v25
	v_cvt_f32_f16_e32 v26, v76
	v_cvt_f32_f16_sdwa v25, v77 dst_sel:DWORD dst_unused:UNUSED_PAD src0_sel:WORD_1
	v_cvt_f32_f16_e32 v24, v77
	v_cvt_f32_f16_sdwa v30, v78 dst_sel:DWORD dst_unused:UNUSED_PAD src0_sel:WORD_1
	v_cvt_f32_f16_e32 v31, v78
	v_cvt_f32_f16_sdwa v34, v79 dst_sel:DWORD dst_unused:UNUSED_PAD src0_sel:WORD_1
	v_cvt_f32_f16_e32 v35, v79
	v_sub_f32_e32 v24, v24, v196
	v_sub_f32_e32 v25, v25, v196
	v_sub_f32_e32 v26, v26, v196
	v_sub_f32_e32 v27, v27, v196
	v_pk_add_f32 v[20:21], v[20:21], v[200:201]
	v_pk_mul_f32 v[26:27], v[196:197], v[26:27] op_sel:[1,0]
	v_pk_mul_f32 v[24:25], v[196:197], v[24:25] op_sel:[1,0]
	v_pk_fma_f32 v[20:21], v[80:81], v[26:27], v[20:21]
	v_pk_fma_f32 v[22:23], v[82:83], v[24:25], v[22:23]
	v_sub_f32_e32 v24, v35, v196
	v_sub_f32_e32 v25, v34, v196
	v_sub_f32_e32 v26, v31, v196
	v_sub_f32_e32 v27, v30, v196
	v_pk_add_f32 v[18:19], v[18:19], v[192:193]
	v_pk_add_f32 v[16:17], v[16:17], v[194:195]
	v_pk_mul_f32 v[26:27], v[196:197], v[26:27] op_sel:[1,0]
	v_pk_mul_f32 v[24:25], v[196:197], v[24:25] op_sel:[1,0]
	s_waitcnt vmcnt(13)
	v_cvt_f32_f16_sdwa v36, v71 dst_sel:DWORD dst_unused:UNUSED_PAD src0_sel:WORD_1
	v_pk_fma_f32 v[24:25], v[74:75], v[24:25], v[18:19]
	v_pk_fma_f32 v[18:19], v[72:73], v[26:27], v[16:17]
	v_cvt_f16_f32_e32 v26, v20
	v_cvt_f16_f32_e32 v27, v21
	v_cvt_pk_f16_f32 v16, v20, v21
	v_cvt_f16_f32_e32 v20, v22
	v_cvt_f16_f32_e32 v21, v23
	v_cvt_pk_f16_f32 v17, v22, v23
	v_cvt_f16_f32_e32 v23, v19
	v_cvt_f16_f32_e32 v31, v25
	v_cvt_f16_f32_e32 v22, v18
	v_cvt_f16_f32_e32 v30, v24
	v_cvt_pk_f16_f32 v18, v18, v19
	v_cvt_pk_f16_f32 v19, v24, v25
	v_cvt_f32_f16_e32 v25, v27
	v_cvt_f32_f16_e32 v27, v20
	v_cvt_f32_f16_e32 v21, v21
	v_cvt_f32_f16_e32 v23, v23
	v_cvt_f32_f16_e32 v24, v26
	v_cvt_f32_f16_e32 v31, v31
	v_cvt_f32_f16_e32 v34, v22
	v_cvt_f32_f16_e32 v35, v30
	v_add_f32_e32 v27, v27, v21
	v_mul_f32_e32 v21, v21, v21
	v_fma_mix_f32 v20, v20, v20, v21 op_sel_hi:[1,1,0]
	v_mul_f32_e32 v21, v23, v23
	v_add_f32_e32 v24, v24, v25
	v_mul_f32_e32 v25, v25, v25
	v_fma_mix_f32 v21, v22, v22, v21 op_sel_hi:[1,1,0]
	v_mul_f32_e32 v22, v31, v31
	v_add_f32_e32 v24, v24, v27
	v_add_f32_e32 v27, v34, v23
	v_add_f32_e32 v34, v35, v31
	v_fma_mix_f32 v25, v26, v26, v25 op_sel_hi:[1,1,0]
	v_fma_mix_f32 v22, v30, v30, v22 op_sel_hi:[1,1,0]
	v_add_f32_e32 v27, v27, v34
	v_add_f32_e32 v20, v25, v20
	v_add_f32_e32 v21, v21, v22
	v_add_f32_e32 v24, v24, v27
	v_add_f32_e32 v20, v20, v21
	v_add_f32_e32 v24, v29, v24
	v_add_f32_e32 v25, v28, v20
	ds_bpermute_b32 v26, v221, v24
	ds_bpermute_b32 v27, v221, v25
	v_cvt_f32_f16_sdwa v34, v70 dst_sel:DWORD dst_unused:UNUSED_PAD src0_sel:WORD_1
	v_cvt_f32_f16_e32 v35, v70
	v_cvt_f32_f16_e32 v37, v71
	s_waitcnt lgkmcnt(1)
	v_add_f32_e32 v28, v24, v26
	s_waitcnt lgkmcnt(0)
	v_add_f32_e32 v29, v25, v27
	v_cvt_f32_f16_sdwa v27, v68 dst_sel:DWORD dst_unused:UNUSED_PAD src0_sel:WORD_1
	v_cvt_f32_f16_e32 v26, v68
	v_cvt_f32_f16_sdwa v25, v69 dst_sel:DWORD dst_unused:UNUSED_PAD src0_sel:WORD_1
	v_cvt_f32_f16_e32 v24, v69
	v_sub_f32_e32 v27, v27, v190
	v_sub_f32_e32 v26, v26, v190
	v_sub_f32_e32 v25, v25, v190
	v_sub_f32_e32 v24, v24, v190
	v_pk_add_f32 v[14:15], v[14:15], v[206:207]
	v_pk_add_f32 v[12:13], v[12:13], v[208:209]
	v_pk_mul_f32 v[26:27], v[190:191], v[26:27] op_sel:[1,0]
	v_pk_mul_f32 v[24:25], v[190:191], v[24:25] op_sel:[1,0]
	v_pk_fma_f32 v[12:13], v[92:93], v[26:27], v[12:13]
	v_pk_fma_f32 v[14:15], v[94:95], v[24:25], v[14:15]
	v_sub_f32_e32 v24, v37, v190
	v_sub_f32_e32 v25, v36, v190
	v_sub_f32_e32 v26, v35, v190
	v_sub_f32_e32 v27, v34, v190
	v_pk_add_f32 v[10:11], v[10:11], v[202:203]
	v_pk_add_f32 v[8:9], v[8:9], v[204:205]
	v_pk_mul_f32 v[26:27], v[190:191], v[26:27] op_sel:[1,0]
	v_pk_mul_f32 v[24:25], v[190:191], v[24:25] op_sel:[1,0]
	ds_write_b128 v235, v[16:19] offset:64
	v_pk_fma_f32 v[24:25], v[90:91], v[24:25], v[10:11]
	v_pk_fma_f32 v[10:11], v[88:89], v[26:27], v[8:9]
	v_cvt_f16_f32_e32 v26, v12
	v_cvt_f16_f32_e32 v27, v13
	v_cvt_pk_f16_f32 v8, v12, v13
	v_cvt_f16_f32_e32 v12, v14
	v_cvt_f16_f32_e32 v13, v15
	v_cvt_pk_f16_f32 v9, v14, v15
	v_cvt_f16_f32_e32 v14, v10
	v_cvt_f16_f32_e32 v15, v11
	v_cvt_f16_f32_e32 v34, v24
	v_cvt_f16_f32_e32 v35, v25
	v_cvt_pk_f16_f32 v10, v10, v11
	v_cvt_pk_f16_f32 v11, v24, v25
	ds_read_b128 v[16:19], v236
	ds_read_b128 v[20:23], v236 offset:1152
	ds_write_b128 v235, v[8:11]
	v_cvt_f32_f16_e32 v8, v26
	v_cvt_f32_f16_e32 v9, v27
	v_cvt_f32_f16_e32 v10, v12
	v_cvt_f32_f16_e32 v11, v13
	v_cvt_f32_f16_e32 v13, v14
	v_cvt_f32_f16_e32 v15, v15
	v_cvt_f32_f16_e32 v24, v34
	v_cvt_f32_f16_e32 v25, v35
	v_add_f32_e32 v8, v8, v9
	v_add_f32_e32 v10, v10, v11
	v_add_f32_e32 v8, v8, v10
	v_add_f32_e32 v10, v13, v15
	v_add_f32_e32 v13, v24, v25
	v_add_f32_e32 v10, v10, v13
	v_add_f32_e32 v8, v8, v10
	v_add_f32_e32 v13, 0, v8
	v_mul_f32_e32 v8, v9, v9
	v_mul_f32_e32 v9, v11, v11
	v_fma_mix_f32 v8, v26, v26, v8 op_sel_hi:[1,1,0]
	v_fma_mix_f32 v9, v12, v12, v9 op_sel_hi:[1,1,0]
	v_mul_f32_e32 v10, v25, v25
	v_add_f32_e32 v8, v8, v9
	v_mul_f32_e32 v9, v15, v15
	v_fma_mix_f32 v9, v14, v14, v9 op_sel_hi:[1,1,0]
	v_fma_mix_f32 v10, v34, v34, v10 op_sel_hi:[1,1,0]
	s_waitcnt vmcnt(12)
	v_cvt_f32_f16_sdwa v11, v64 dst_sel:DWORD dst_unused:UNUSED_PAD src0_sel:WORD_1
	v_add_f32_e32 v9, v9, v10
	v_add_f32_e32 v12, v8, v9
	v_cvt_f32_f16_e32 v10, v64
	v_cvt_f32_f16_sdwa v9, v65 dst_sel:DWORD dst_unused:UNUSED_PAD src0_sel:WORD_1
	v_cvt_f32_f16_e32 v8, v65
	v_cvt_f32_f16_sdwa v14, v66 dst_sel:DWORD dst_unused:UNUSED_PAD src0_sel:WORD_1
	v_cvt_f32_f16_e32 v15, v66
	v_cvt_f32_f16_sdwa v24, v67 dst_sel:DWORD dst_unused:UNUSED_PAD src0_sel:WORD_1
	v_cvt_f32_f16_e32 v25, v67
	v_sub_f32_e32 v8, v8, v190
	v_sub_f32_e32 v9, v9, v190
	v_sub_f32_e32 v10, v10, v190
	v_sub_f32_e32 v11, v11, v190
	v_pk_add_f32 v[6:7], v[6:7], v[198:199]
	v_pk_add_f32 v[4:5], v[4:5], v[200:201]
	v_pk_mul_f32 v[10:11], v[190:191], v[10:11] op_sel:[1,0]
	v_pk_mul_f32 v[8:9], v[190:191], v[8:9] op_sel:[1,0]
	v_pk_fma_f32 v[4:5], v[80:81], v[10:11], v[4:5]
	v_pk_fma_f32 v[6:7], v[82:83], v[8:9], v[6:7]
	v_sub_f32_e32 v8, v25, v190
	v_sub_f32_e32 v9, v24, v190
	v_sub_f32_e32 v10, v15, v190
	v_sub_f32_e32 v11, v14, v190
	v_pk_add_f32 v[2:3], v[2:3], v[192:193]
	v_pk_add_f32 v[0:1], v[0:1], v[194:195]
	v_pk_mul_f32 v[10:11], v[190:191], v[10:11] op_sel:[1,0]
	v_pk_mul_f32 v[8:9], v[190:191], v[8:9] op_sel:[1,0]
	ds_bpermute_b32 v30, v237, v28
	v_pk_fma_f32 v[8:9], v[74:75], v[8:9], v[2:3]
	v_pk_fma_f32 v[2:3], v[72:73], v[10:11], v[0:1]
	v_cvt_f16_f32_e32 v10, v4
	v_cvt_f16_f32_e32 v11, v5
	v_cvt_pk_f16_f32 v0, v4, v5
	v_cvt_f16_f32_e32 v4, v6
	v_cvt_f16_f32_e32 v5, v7
	v_cvt_pk_f16_f32 v1, v6, v7
	v_cvt_f16_f32_e32 v7, v3
	v_cvt_f16_f32_e32 v15, v9
	v_cvt_f16_f32_e32 v6, v2
	v_cvt_f16_f32_e32 v14, v8
	v_cvt_f32_f16_e32 v25, v4
	v_cvt_f32_f16_e32 v5, v5
	v_cvt_f32_f16_e32 v7, v7
	v_cvt_f32_f16_e32 v24, v10
	v_cvt_f32_f16_e32 v11, v11
	v_cvt_f32_f16_e32 v15, v15
	v_cvt_f32_f16_e32 v26, v6
	v_cvt_f32_f16_e32 v27, v14
	v_add_f32_e32 v25, v25, v5
	v_mul_f32_e32 v5, v5, v5
	v_fma_mix_f32 v4, v4, v4, v5 op_sel_hi:[1,1,0]
	v_mul_f32_e32 v5, v7, v7
	v_add_f32_e32 v24, v24, v11
	v_mul_f32_e32 v11, v11, v11
	v_fma_mix_f32 v5, v6, v6, v5 op_sel_hi:[1,1,0]
	v_mul_f32_e32 v6, v15, v15
	v_add_f32_e32 v24, v24, v25
	v_add_f32_e32 v25, v26, v7
	v_add_f32_e32 v26, v27, v15
	v_fma_mix_f32 v10, v10, v10, v11 op_sel_hi:[1,1,0]
	v_fma_mix_f32 v6, v14, v14, v6 op_sel_hi:[1,1,0]
	v_add_f32_e32 v25, v25, v26
	v_add_f32_e32 v4, v10, v4
	v_add_f32_e32 v5, v5, v6
	v_add_f32_e32 v24, v24, v25
	v_add_f32_e32 v4, v4, v5
	v_add_f32_e32 v13, v13, v24
	v_add_f32_e32 v4, v12, v4
	ds_bpermute_b32 v5, v221, v13
	ds_bpermute_b32 v6, v221, v4
	v_cvt_pk_f16_f32 v2, v2, v3
	v_cvt_pk_f16_f32 v3, v8, v9
	ds_write_b128 v235, v[0:3] offset:64
	s_waitcnt lgkmcnt(2)
	v_add_f32_e32 v10, v13, v5
	s_waitcnt lgkmcnt(1)
	v_add_f32_e32 v11, v4, v6
	ds_bpermute_b32 v31, v237, v29
	ds_bpermute_b32 v12, v237, v10
	ds_bpermute_b32 v13, v237, v11
	ds_read_b128 v[0:3], v236
	ds_read_b128 v[4:7], v236 offset:1152
	v_add_f32_e32 v8, v28, v30
	s_waitcnt lgkmcnt(4)
	v_add_f32_e32 v9, v29, v31
	s_waitcnt lgkmcnt(3)
	v_add_f32_e32 v10, v10, v12
	s_waitcnt lgkmcnt(2)
	v_add_f32_e32 v11, v11, v13
	v_add_u32_e32 v12, 0x3c000, v144
	buffer_store_dwordx4 v[16:19], v12, s[24:27], 0 offen nt
	v_add_u32_e32 v12, 0x3f000, v144
	buffer_store_dwordx4 v[20:23], v12, s[24:27], 0 offen nt
	global_store_dwordx2 v[32:33], v[8:9], off offset:3072
	v_add_u32_e32 v8, 0x42000, v144
	s_waitcnt lgkmcnt(1)
	buffer_store_dwordx4 v[0:3], v8, s[24:27], 0 offen nt
	s_nop 1
	v_add_u32_e32 v0, 0x45000, v144
	s_waitcnt lgkmcnt(0)
	buffer_store_dwordx4 v[4:7], v0, s[24:27], 0 offen nt
	v_add_co_u32_e32 v0, vcc, 0x4000, v140
	s_nop 1
	v_addc_co_u32_e32 v1, vcc, 0, v141, vcc
	global_store_dwordx2 v[0:1], v[10:11], off offset:512
	s_mov_b32 s83, s81
	s_mov_b32 s84, s82
	s_mov_b64 s[40:41], s[0:1]
	s_mov_b64 s[38:39], s[8:9]
	s_mov_b64 vcc, s[6:7]
	s_cbranch_vccz .LBB10_12
	s_waitcnt vmcnt(0)
	s_cmpk_gt_u32 s44, 0xff
	s_cbranch_scc1 .LBB10_31
	s_barrier

.LBB10_32:
	s_endpgm
	s_endpgm
	s_endpgm
	s_endpgm
	s_endpgm
	s_endpgm
	s_endpgm
	s_endpgm
	s_endpgm
	s_endpgm
	.section	.rodata,"a",@progbits
	.p2align	6, 0x0
	.amdhsa_kernel _Z6k_gemmIN2pg6EpiResELi3072EEvNS0_4GemmET_
		.amdhsa_group_segment_fixed_size 0
		.amdhsa_private_segment_fixed_size 0
		.amdhsa_kernarg_size 344
		.amdhsa_user_sgpr_count 2
		.amdhsa_user_sgpr_dispatch_ptr 0
		.amdhsa_user_sgpr_queue_ptr 0
		.amdhsa_user_sgpr_kernarg_segment_ptr 1
		.amdhsa_user_sgpr_dispatch_id 0
		.amdhsa_user_sgpr_kernarg_preload_length 0
		.amdhsa_user_sgpr_kernarg_preload_offset 0
		.amdhsa_user_sgpr_private_segment_size 0
		.amdhsa_uses_dynamic_stack 0
		.amdhsa_enable_private_segment 0
		.amdhsa_system_sgpr_workgroup_id_x 1
		.amdhsa_system_sgpr_workgroup_id_y 0
		.amdhsa_system_sgpr_workgroup_id_z 0
		.amdhsa_system_sgpr_workgroup_info 0
		.amdhsa_system_vgpr_workitem_id 0
		.amdhsa_next_free_vgpr 250
		.amdhsa_next_free_sgpr 92
		.amdhsa_accum_offset 252
		.amdhsa_reserve_vcc 1
		.amdhsa_float_round_mode_32 0
		.amdhsa_float_round_mode_16_64 0
		.amdhsa_float_denorm_mode_32 3
		.amdhsa_float_denorm_mode_16_64 3
		.amdhsa_dx10_clamp 1
		.amdhsa_ieee_mode 1
		.amdhsa_fp16_overflow 0
		.amdhsa_tg_split 0
		.amdhsa_exception_fp_ieee_invalid_op 0
		.amdhsa_exception_fp_denorm_src 0
		.amdhsa_exception_fp_ieee_div_zero 0
		.amdhsa_exception_fp_ieee_overflow 0
		.amdhsa_exception_fp_ieee_underflow 0
		.amdhsa_exception_fp_ieee_inexact 0
		.amdhsa_exception_int_div_zero 0
	.end_amdhsa_kernel

amdhsa.kernels:
  - .agpr_count:     16
    .args:
      - .actual_access:  read_only
        .address_space:  global
        .offset:         0
        .size:           8
        .value_kind:     global_buffer
      - .actual_access:  read_only
        .address_space:  global
        .offset:         8
        .size:           8
        .value_kind:     global_buffer
      - .actual_access:  write_only
        .address_space:  global
        .offset:         16
        .size:           8
        .value_kind:     global_buffer
    .group_segment_fixed_size: 45056
    .kernarg_segment_align: 8
    .kernarg_segment_size: 24
    .language:       OpenCL C
    .language_version:
      - 2
      - 0
    .max_flat_workgroup_size: 256
    .name:           _Z6k_attnPKDF16_PKfPDF16_
    .private_segment_fixed_size: 0
    .sgpr_count:     16
    .sgpr_spill_count: 0
    .symbol:         _Z6k_attnPKDF16_PKfPDF16_.kd
    .uniform_work_group_size: 1
    .uses_dynamic_stack: false
    .vgpr_count:     84
    .vgpr_spill_count: 0
    .wavefront_size: 64
  - .agpr_count:     0
    .args:
      - .actual_access:  read_only
        .address_space:  global
        .offset:         0
        .size:           8
        .value_kind:     global_buffer
      - .actual_access:  read_only
        .address_space:  global
        .offset:         8
        .size:           8
        .value_kind:     global_buffer
      - .actual_access:  write_only
        .address_space:  global
        .offset:         16
        .size:           8
        .value_kind:     global_buffer
      - .actual_access:  write_only
        .address_space:  global
        .offset:         24
        .size:           8
        .value_kind:     global_buffer
      - .actual_access:  write_only
        .address_space:  global
        .offset:         32
        .size:           8
        .value_kind:     global_buffer
      - .actual_access:  write_only
        .address_space:  global
        .offset:         40
        .size:           8
        .value_kind:     global_buffer
    .group_segment_fixed_size: 0
    .kernarg_segment_align: 8
    .kernarg_segment_size: 48
    .language:       OpenCL C
    .language_version:
      - 2
      - 0
    .max_flat_workgroup_size: 256
    .name:           _Z11k_prep_miscPKiPKfPfPDv2_fS3_S3_
    .private_segment_fixed_size: 0
    .sgpr_count:     16
    .sgpr_spill_count: 0
    .symbol:         _Z11k_prep_miscPKiPKfPfPDv2_fS3_S3_.kd
    .uniform_work_group_size: 1
    .uses_dynamic_stack: false
    .vgpr_count:     6
    .vgpr_spill_count: 0
    .wavefront_size: 64
  - .agpr_count:     0
    .args:
      - .actual_access:  read_only
        .address_space:  global
        .offset:         0
        .size:           8
        .value_kind:     global_buffer
      - .actual_access:  write_only
        .address_space:  global
        .offset:         8
        .size:           8
        .value_kind:     global_buffer
    .group_segment_fixed_size: 0
    .kernarg_segment_align: 8
    .kernarg_segment_size: 16
    .language:       OpenCL C
    .language_version:
      - 2
      - 0
    .max_flat_workgroup_size: 256
    .name:           _Z7k_cvt_xPKfPDF16_
    .private_segment_fixed_size: 0
    .sgpr_count:     14
    .sgpr_spill_count: 0
    .symbol:         _Z7k_cvt_xPKfPDF16_.kd
    .uniform_work_group_size: 1
    .uses_dynamic_stack: false
    .vgpr_count:     12
    .vgpr_spill_count: 0
    .wavefront_size: 64
  - .agpr_count:     0
    .args:
      - .offset:         0
        .size:           176
        .value_kind:     by_value
    .group_segment_fixed_size: 9216
    .kernarg_segment_align: 8
    .kernarg_segment_size: 176
    .language:       OpenCL C
    .language_version:
      - 2
      - 0
    .max_flat_workgroup_size: 256
    .name:           _Z8k_wtrans8PrepArgs
    .private_segment_fixed_size: 0
    .sgpr_count:     44
    .sgpr_spill_count: 0
    .symbol:         _Z8k_wtrans8PrepArgs.kd
    .uniform_work_group_size: 1
    .uses_dynamic_stack: false
    .vgpr_count:     18
    .vgpr_spill_count: 0
    .wavefront_size: 64
  - .agpr_count:     0
    .args:
      - .offset:         0
        .size:           176
        .value_kind:     by_value
      - .actual_access:  read_only
        .address_space:  global
        .offset:         176
        .size:           8
        .value_kind:     global_buffer
      - .actual_access:  read_only
        .address_space:  global
        .offset:         184
        .size:           8
        .value_kind:     global_buffer
    .group_segment_fixed_size: 2048
    .kernarg_segment_align: 8
    .kernarg_segment_size: 192
    .language:       OpenCL C
    .language_version:
      - 2
      - 0
    .max_flat_workgroup_size: 256
    .name:           _Z8k_colvec8PrepArgsPKfS1_
    .private_segment_fixed_size: 0
    .sgpr_count:     38
    .sgpr_spill_count: 0
    .symbol:         _Z8k_colvec8PrepArgsPKfS1_.kd
    .uniform_work_group_size: 1
    .uses_dynamic_stack: false
    .vgpr_count:     114
    .vgpr_spill_count: 0
    .wavefront_size: 64
  - .agpr_count:     0
    .args:
      - .actual_access:  read_only
        .address_space:  global
        .offset:         0
        .size:           8
        .value_kind:     global_buffer
      - .actual_access:  write_only
        .address_space:  global
        .offset:         8
        .size:           8
        .value_kind:     global_buffer
    .group_segment_fixed_size: 0
    .kernarg_segment_align: 8
    .kernarg_segment_size: 16
    .language:       OpenCL C
    .language_version:
      - 2
      - 0
    .max_flat_workgroup_size: 256
    .name:           _Z9k_rowstatPKDv2_fPS_
    .private_segment_fixed_size: 0
    .sgpr_count:     14
    .sgpr_spill_count: 0
    .symbol:         _Z9k_rowstatPKDv2_fPS_.kd
    .uniform_work_group_size: 1
    .uses_dynamic_stack: false
    .vgpr_count:     28
    .vgpr_spill_count: 0
    .wavefront_size: 64
  - .agpr_count:     0
    .args:
      - .actual_access:  read_only
        .address_space:  global
        .offset:         0
        .size:           8
        .value_kind:     global_buffer
      - .actual_access:  read_only
        .address_space:  global
        .offset:         8
        .size:           8
        .value_kind:     global_buffer
      - .actual_access:  read_only
        .address_space:  global
        .offset:         16
        .size:           8
        .value_kind:     global_buffer
      - .actual_access:  read_only
        .address_space:  global
        .offset:         24
        .size:           8
        .value_kind:     global_buffer
      - .actual_access:  write_only
        .address_space:  global
        .offset:         32
        .size:           8
        .value_kind:     global_buffer
    .group_segment_fixed_size: 0
    .kernarg_segment_align: 8
    .kernarg_segment_size: 40
    .language:       OpenCL C
    .language_version:
      - 2
      - 0
    .max_flat_workgroup_size: 256
    .name:           _Z10k_final_lnPKDF16_PKDv2_fPKfS5_Pf
    .private_segment_fixed_size: 0
    .sgpr_count:     19
    .sgpr_spill_count: 0
    .symbol:         _Z10k_final_lnPKDF16_PKDv2_fPKfS5_Pf.kd
    .uniform_work_group_size: 1
    .uses_dynamic_stack: false
    .vgpr_count:     19
    .vgpr_spill_count: 0
    .wavefront_size: 64
  - .agpr_count:     0
    .args:
      - .offset:         0
        .size:           32
        .value_kind:     by_value
      - .offset:         32
        .size:           32
        .value_kind:     by_value
      - .offset:         64
        .size:           4
        .value_kind:     hidden_block_count_x
      - .offset:         68
        .size:           4
        .value_kind:     hidden_block_count_y
      - .offset:         72
        .size:           4
        .value_kind:     hidden_block_count_z
      - .offset:         76
        .size:           2
        .value_kind:     hidden_group_size_x
      - .offset:         78
        .size:           2
        .value_kind:     hidden_group_size_y
      - .offset:         80
        .size:           2
        .value_kind:     hidden_group_size_z
      - .offset:         82
        .size:           2
        .value_kind:     hidden_remainder_x
      - .offset:         84
        .size:           2
        .value_kind:     hidden_remainder_y
      - .offset:         86
        .size:           2
        .value_kind:     hidden_remainder_z
      - .offset:         104
        .size:           8
        .value_kind:     hidden_global_offset_x
      - .offset:         112
        .size:           8
        .value_kind:     hidden_global_offset_y
      - .offset:         120
        .size:           8
        .value_kind:     hidden_global_offset_z
      - .offset:         128
        .size:           2
        .value_kind:     hidden_grid_dims
      - .offset:         184
        .size:           4
        .value_kind:     hidden_dynamic_lds_size
    .group_segment_fixed_size: 0
    .kernarg_segment_align: 8
    .kernarg_segment_size: 320
    .language:       OpenCL C
    .language_version:
      - 2
      - 0
    .max_flat_workgroup_size: 512
    .name:           _Z6k_gemmIN2pg6EpiLinILi0EEELi768EEvNS0_4GemmET_
    .private_segment_fixed_size: 0
    .sgpr_count:     84
    .sgpr_spill_count: 0
    .symbol:         _Z6k_gemmIN2pg6EpiLinILi0EEELi768EEvNS0_4GemmET_.kd
    .uniform_work_group_size: 1
    .uses_dynamic_stack: false
    .vgpr_count:     254
    .vgpr_spill_count: 0
    .wavefront_size: 64
  - .agpr_count:     0
    .args:
      - .offset:         0
        .size:           32
        .value_kind:     by_value
      - .offset:         32
        .size:           56
        .value_kind:     by_value
      - .offset:         88
        .size:           4
        .value_kind:     hidden_block_count_x
      - .offset:         92
        .size:           4
        .value_kind:     hidden_block_count_y
      - .offset:         96
        .size:           4
        .value_kind:     hidden_block_count_z
      - .offset:         100
        .size:           2
        .value_kind:     hidden_group_size_x
      - .offset:         102
        .size:           2
        .value_kind:     hidden_group_size_y
      - .offset:         104
        .size:           2
        .value_kind:     hidden_group_size_z
      - .offset:         106
        .size:           2
        .value_kind:     hidden_remainder_x
      - .offset:         108
        .size:           2
        .value_kind:     hidden_remainder_y
      - .offset:         110
        .size:           2
        .value_kind:     hidden_remainder_z
      - .offset:         128
        .size:           8
        .value_kind:     hidden_global_offset_x
      - .offset:         136
        .size:           8
        .value_kind:     hidden_global_offset_y
      - .offset:         144
        .size:           8
        .value_kind:     hidden_global_offset_z
      - .offset:         152
        .size:           2
        .value_kind:     hidden_grid_dims
      - .offset:         208
        .size:           4
        .value_kind:     hidden_dynamic_lds_size
    .group_segment_fixed_size: 0
    .kernarg_segment_align: 8
    .kernarg_segment_size: 344
    .language:       OpenCL C
    .language_version:
      - 2
      - 0
    .max_flat_workgroup_size: 512
    .name:           _Z6k_gemmIN2pg6EpiResELi768EEvNS0_4GemmET_
    .private_segment_fixed_size: 0
    .sgpr_count:     98
    .sgpr_spill_count: 0
    .symbol:         _Z6k_gemmIN2pg6EpiResELi768EEvNS0_4GemmET_.kd
    .uniform_work_group_size: 1
    .uses_dynamic_stack: false
    .vgpr_count:     250
    .vgpr_spill_count: 0
    .wavefront_size: 64
  - .agpr_count:     0
    .args:
      - .offset:         0
        .size:           32
        .value_kind:     by_value
      - .offset:         32
        .size:           32
        .value_kind:     by_value
      - .offset:         64
        .size:           4
        .value_kind:     hidden_block_count_x
      - .offset:         68
        .size:           4
        .value_kind:     hidden_block_count_y
      - .offset:         72
        .size:           4
        .value_kind:     hidden_block_count_z
      - .offset:         76
        .size:           2
        .value_kind:     hidden_group_size_x
      - .offset:         78
        .size:           2
        .value_kind:     hidden_group_size_y
      - .offset:         80
        .size:           2
        .value_kind:     hidden_group_size_z
      - .offset:         82
        .size:           2
        .value_kind:     hidden_remainder_x
      - .offset:         84
        .size:           2
        .value_kind:     hidden_remainder_y
      - .offset:         86
        .size:           2
        .value_kind:     hidden_remainder_z
      - .offset:         104
        .size:           8
        .value_kind:     hidden_global_offset_x
      - .offset:         112
        .size:           8
        .value_kind:     hidden_global_offset_y
      - .offset:         120
        .size:           8
        .value_kind:     hidden_global_offset_z
      - .offset:         128
        .size:           2
        .value_kind:     hidden_grid_dims
      - .offset:         184
        .size:           4
        .value_kind:     hidden_dynamic_lds_size
    .group_segment_fixed_size: 0
    .kernarg_segment_align: 8
    .kernarg_segment_size: 320
    .language:       OpenCL C
    .language_version:
      - 2
      - 0
    .max_flat_workgroup_size: 512
    .name:           _Z6k_gemmIN2pg6EpiLinILi1EEELi768EEvNS0_4GemmET_
    .private_segment_fixed_size: 0
    .sgpr_count:     84
    .sgpr_spill_count: 0
    .symbol:         _Z6k_gemmIN2pg6EpiLinILi1EEELi768EEvNS0_4GemmET_.kd
    .uniform_work_group_size: 1
    .uses_dynamic_stack: false
    .vgpr_count:     254
    .vgpr_spill_count: 0
    .wavefront_size: 64
  - .agpr_count:     0
    .args:
      - .offset:         0
        .size:           32
        .value_kind:     by_value
      - .offset:         32
        .size:           56
        .value_kind:     by_value
      - .offset:         88
        .size:           4
        .value_kind:     hidden_block_count_x
      - .offset:         92
        .size:           4
        .value_kind:     hidden_block_count_y
      - .offset:         96
        .size:           4
        .value_kind:     hidden_block_count_z
      - .offset:         100
        .size:           2
        .value_kind:     hidden_group_size_x
      - .offset:         102
        .size:           2
        .value_kind:     hidden_group_size_y
      - .offset:         104
        .size:           2
        .value_kind:     hidden_group_size_z
      - .offset:         106
        .size:           2
        .value_kind:     hidden_remainder_x
      - .offset:         108
        .size:           2
        .value_kind:     hidden_remainder_y
      - .offset:         110
        .size:           2
        .value_kind:     hidden_remainder_z
      - .offset:         128
        .size:           8
        .value_kind:     hidden_global_offset_x
      - .offset:         136
        .size:           8
        .value_kind:     hidden_global_offset_y
      - .offset:         144
        .size:           8
        .value_kind:     hidden_global_offset_z
      - .offset:         152
        .size:           2
        .value_kind:     hidden_grid_dims
      - .offset:         208
        .size:           4
        .value_kind:     hidden_dynamic_lds_size
    .group_segment_fixed_size: 0
    .kernarg_segment_align: 8
    .kernarg_segment_size: 344
    .language:       OpenCL C
    .language_version:
      - 2
      - 0
    .max_flat_workgroup_size: 512
    .name:           _Z6k_gemmIN2pg6EpiResELi3072EEvNS0_4GemmET_
    .private_segment_fixed_size: 0
    .sgpr_count:     98
    .sgpr_spill_count: 0
    .symbol:         _Z6k_gemmIN2pg6EpiResELi3072EEvNS0_4GemmET_.kd
    .uniform_work_group_size: 1
    .uses_dynamic_stack: false
    .vgpr_count:     250
    .vgpr_spill_count: 0
    .wavefront_size: 64
